# RG-LRU intermediate stored as log2(a) (SP pre-scaled by log2e in P0): the x*log2e multiplies in front of v_exp in the P8 and P9 scans removed (67 + 256 per unit/item)
# speedup vs baseline: 1.0066x; 1.0006x over previous
.LBB0_75:
	v_lshl_add_u64 v[10:11], s[18:19], 0, v[4:5]
	global_load_dword v7, v[10:11], off
	v_add_u32_e32 v2, s8, v2
	v_cmp_lt_i32_e32 vcc, s29, v2
	s_or_b64 s[14:15], vcc, s[14:15]
	v_lshl_add_u64 v[10:11], s[6:7], 0, v[4:5]
	v_lshl_add_u64 v[4:5], v[4:5], 0, s[10:11]
	s_waitcnt vmcnt(0)
	v_mul_f32_e32 v7, 0xbfb8aa3b, v7
	v_exp_f32_e32 v26, v7
	s_nop 0
	v_add_f32_e32 v7, 1.0, v26
	v_add_f32_e32 v14, -1.0, v7
	v_frexp_mant_f32_e32 v15, v7
	v_cvt_f64_f32_e32 v[12:13], v7
	v_sub_f32_e32 v16, v14, v7
	v_frexp_exp_i32_f64_e32 v12, v[12:13]
	v_cmp_gt_f32_e32 vcc, s3, v15
	v_sub_f32_e32 v14, v26, v14
	v_add_f32_e32 v13, 1.0, v16
	v_subbrev_co_u32_e32 v12, vcc, 0, v12, vcc
	v_add_f32_e32 v13, v14, v13
	v_sub_u32_e32 v14, 0, v12
	v_ldexp_f32 v7, v7, v14
	v_ldexp_f32 v13, v13, v14
	v_add_f32_e32 v14, -1.0, v7
	v_add_f32_e32 v16, 1.0, v7
	v_add_f32_e32 v15, 1.0, v14
	v_add_f32_e32 v17, -1.0, v16
	v_sub_f32_e32 v15, v7, v15
	v_sub_f32_e32 v7, v7, v17
	v_add_f32_e32 v7, v13, v7
	v_add_f32_e32 v17, v13, v15
	v_add_f32_e32 v13, v16, v7
	v_rcp_f32_e32 v20, v13
	v_add_f32_e32 v15, v14, v17
	v_sub_f32_e32 v16, v13, v16
	v_sub_f32_e32 v7, v7, v16
	v_mul_f32_e32 v22, v15, v20
	v_mul_f32_e32 v16, v13, v22
	v_fma_f32 v18, v22, v13, -v16
	v_sub_f32_e32 v14, v15, v14
	v_fmac_f32_e32 v18, v22, v7
	v_sub_f32_e32 v21, v17, v14
	v_add_f32_e32 v14, v16, v18
	v_sub_f32_e32 v17, v15, v14
	v_mov_b32_e32 v19, v14
	v_pk_add_f32 v[14:15], v[14:15], v[16:17] neg_lo:[0,1] neg_hi:[0,1]
	v_cvt_f32_i32_e32 v12, v12
	v_pk_add_f32 v[14:15], v[14:15], v[18:19] neg_lo:[0,1] neg_hi:[0,1]
	v_cmp_neq_f32_e32 vcc, s20, v26
	v_add_f32_e32 v15, v21, v15
	v_add_f32_e32 v14, v14, v15
	v_add_f32_e32 v15, v17, v14
	v_mul_f32_e32 v19, v20, v15
	v_mul_f32_e32 v16, v13, v19
	v_fma_f32 v18, v19, v13, -v16
	v_sub_f32_e32 v17, v17, v15
	v_fmac_f32_e32 v18, v19, v7
	v_add_f32_e32 v21, v14, v17
	v_add_f32_e32 v23, v22, v19
	v_add_f32_e32 v14, v16, v18
	v_sub_f32_e32 v13, v23, v22
	v_sub_f32_e32 v17, v15, v14
	v_sub_f32_e32 v7, v19, v13
	v_mov_b32_e32 v19, v14
	v_pk_add_f32 v[14:15], v[14:15], v[16:17] neg_lo:[0,1] neg_hi:[0,1]
	s_nop 0
	v_pk_add_f32 v[14:15], v[14:15], v[18:19] neg_lo:[0,1] neg_hi:[0,1]
	s_nop 0
	v_add_f32_e32 v13, v21, v15
	v_add_f32_e32 v13, v14, v13
	v_add_f32_e32 v13, v17, v13
	v_mul_f32_e32 v13, v20, v13
	v_add_f32_e32 v7, v7, v13
	v_add_f32_e32 v13, v23, v7
	v_mul_f32_e32 v14, v13, v13
	v_sub_f32_e32 v16, v13, v23
	v_fmamk_f32 v17, v14, 0x3e9b6dac, v1
	v_ldexp_f32 v15, v13, 1
	v_sub_f32_e32 v16, v7, v16
	v_mul_f32_e32 v13, v13, v14
	v_fmaak_f32 v7, v14, v17, 0x3f2aaada
	v_ldexp_f32 v19, v16, 1
	v_pk_mul_f32 v[16:17], v[12:13], v[6:7]
	s_nop 0
	v_fma_f32 v14, v12, s9, -v16
	v_fmac_f32_e32 v14, 0xb102e308, v12
	v_pk_add_f32 v[12:13], v[16:17], v[14:15]
	v_mov_b32_e32 v18, v16
	v_sub_f32_e32 v7, v13, v15
	v_sub_f32_e32 v7, v17, v7
	v_add_f32_e32 v19, v19, v7
	v_pk_add_f32 v[20:21], v[12:13], v[16:17] neg_lo:[0,1] neg_hi:[0,1]
	v_pk_add_f32 v[16:17], v[12:13], v[18:19]
	v_mov_b32_e32 v15, v12
	v_mov_b32_e32 v21, v17
	v_pk_add_f32 v[24:25], v[14:15], v[20:21] neg_lo:[0,1] neg_hi:[0,1]
	v_pk_add_f32 v[14:15], v[14:15], v[20:21]
	v_mov_b32_e32 v23, v12
	v_pk_add_f32 v[20:21], v[14:15], v[12:13] op_sel:[1,0] op_sel_hi:[0,1] neg_lo:[0,1] neg_hi:[0,1]
	v_mov_b32_e32 v22, v19
	v_mov_b32_e32 v18, v17
	v_mov_b32_e32 v19, v15
	v_pk_mov_b32 v[12:13], v[12:13], v[20:21] op_sel:[1,0]
	v_pk_add_f32 v[16:17], v[16:17], v[20:21] op_sel_hi:[1,0] neg_lo:[0,1] neg_hi:[0,1]
	v_pk_add_f32 v[12:13], v[18:19], v[12:13] neg_lo:[0,1] neg_hi:[0,1]
	v_mov_b32_e32 v16, v24
	v_pk_add_f32 v[12:13], v[22:23], v[12:13] neg_lo:[0,1] neg_hi:[0,1]
	v_mov_b32_e32 v25, v15
	v_pk_add_f32 v[16:17], v[16:17], v[12:13]
	s_nop 0
	v_pk_add_f32 v[18:19], v[16:17], v[16:17] op_sel:[0,1] op_sel_hi:[1,0]
	s_nop 0
	v_pk_add_f32 v[14:15], v[14:15], v[18:19] op_sel:[1,0] op_sel_hi:[0,1]
	v_mov_b32_e32 v17, v14
	v_mov_b32_e32 v13, v18
	v_pk_add_f32 v[18:19], v[16:17], v[24:25] neg_lo:[0,1] neg_hi:[0,1]
	s_nop 0
	v_sub_f32_e32 v7, v16, v18
	v_pk_add_f32 v[12:13], v[12:13], v[18:19] neg_lo:[0,1] neg_hi:[0,1]
	v_sub_f32_e32 v7, v24, v7
	v_add_f32_e32 v7, v12, v7
	v_add_f32_e32 v7, v7, v13
	v_add_f32_e32 v7, v14, v7
	v_cndmask_b32_e32 v7, v3, v7, vcc
	v_cmp_ngt_f32_e32 vcc, -1.0, v26
	s_nop 1
	v_cndmask_b32_e32 v7, v8, v7, vcc
	v_cmp_neq_f32_e32 vcc, -1.0, v26
	s_nop 1
	v_cndmask_b32_e32 v7, v9, v7, vcc
	v_cmp_lt_f32_e64 vcc, |v26|, s21
	s_nop 1
	v_cndmask_b32_e32 v7, v7, v26, vcc
	v_mul_f32_e32 v7, 0xc138aa3b, v7
	global_store_dword v[10:11], v7, off
	s_andn2_b64 exec, exec, s[14:15]
	s_cbranch_execnz .LBB0_75

.LBB0_1262:
	s_mov_b32 s98, 0x3fb17218
	s_mul_hi_i32 s20, s80, 0x66666667
	s_lshr_b32 s48, s20, 31
	s_ashr_i32 s20, s20, 2
	s_add_i32 s20, s20, s48
	s_mul_i32 s48, s20, 0xfffffb00
	s_add_i32 s48, s48, s35
	s_waitcnt lgkmcnt(0)
	v_add_u32_e32 v2, s48, v158
	v_ashrrev_i32_e32 v3, 31, v2
	v_lshlrev_b64 v[2:3], 2, v[2:3]
	v_lshl_add_u64 v[6:7], s[62:63], 0, v[2:3]
	v_add_co_u32_e32 v4, vcc, s3, v6
	global_load_dwordx4 v[58:61], v[6:7], off
	s_nop 0
	v_addc_co_u32_e32 v5, vcc, 0, v7, vcc
	global_load_dwordx4 v[94:97], v[4:5], off offset:1024
	v_lshl_add_u64 v[2:3], s[64:65], 0, v[2:3]
	global_load_dwordx4 v[70:73], v[2:3], off
	v_lshl_add_u64 v[4:5], v[6:7], 0, s[38:39]
	global_load_dwordx4 v[98:101], v[4:5], off offset:16
	global_load_dwordx4 v[62:65], v[6:7], off offset:16
	global_load_dwordx4 v[66:69], v[2:3], off offset:16
	s_mul_i32 s52, s20, 0xffffffec
	v_add_co_u32_e32 v2, vcc, s29, v6
	s_add_i32 s52, s33, s52
	s_nop 0
	v_addc_co_u32_e32 v3, vcc, 0, v7, vcc
	s_ashr_i32 s53, s52, 31
	v_add_co_u32_e32 v4, vcc, s47, v6
	s_lshl_b64 s[54:55], s[52:53], 16
	s_nop 0
	v_addc_co_u32_e32 v5, vcc, 0, v7, vcc
	v_lshl_add_u64 v[8:9], v[156:157], 0, s[54:55]
	global_load_dwordx4 v[102:105], v[4:5], off offset:3072
	global_load_dwordx4 v[86:89], v[2:3], off offset:2048
	global_load_dwordx4 v[42:45], v[8:9], off
	global_load_dwordx4 v[26:29], v[8:9], off offset:1024
	global_load_dwordx4 v[10:13], v[8:9], off offset:2048
	s_nop 0
	global_load_dwordx4 v[2:5], v[8:9], off offset:3072
	v_add_co_u32_e32 v22, vcc, s3, v8
	v_lshlrev_b32_e32 v111, 16, v201
	s_nop 0
	v_addc_co_u32_e32 v23, vcc, 0, v9, vcc
	v_add_co_u32_e32 v24, vcc, s29, v8
	v_lshlrev_b32_e32 v110, 16, v206
	s_nop 0
	v_addc_co_u32_e32 v25, vcc, 0, v9, vcc
	v_add_co_u32_e32 v82, vcc, s47, v8
	global_load_dwordx4 v[30:33], v[22:23], off offset:1024
	global_load_dwordx4 v[14:17], v[22:23], off offset:2048
	global_load_dwordx4 v[46:49], v[24:25], off offset:-4096
	global_load_dwordx4 v[50:53], v[24:25], off
	global_load_dwordx4 v[34:37], v[24:25], off offset:1024
	global_load_dwordx4 v[18:21], v[24:25], off offset:2048
	v_addc_co_u32_e32 v83, vcc, 0, v9, vcc
	v_lshl_add_u64 v[8:9], v[6:7], 0, s[40:41]
	v_lshl_add_u64 v[6:7], v[6:7], 0, s[42:43]
	global_load_dwordx4 v[106:109], v[6:7], off offset:16
	global_load_dwordx4 v[74:77], v[8:9], off offset:16
	global_load_dwordx4 v[78:81], v[24:25], off offset:3072
	s_nop 0
	global_load_dwordx4 v[6:9], v[22:23], off offset:3072
	global_load_dwordx4 v[54:57], v[82:83], off
	global_load_dwordx4 v[38:41], v[82:83], off offset:1024
	s_nop 0
	global_load_dwordx4 v[22:25], v[82:83], off offset:2048
	s_nop 0
	global_load_dwordx4 v[82:85], v[82:83], off offset:3072
	v_lshlrev_b32_e32 v114, 16, v207
	v_lshlrev_b32_e32 v115, 16, v202
	v_and_b32_e32 v117, 0xffff0000, v202
	v_and_b32_e32 v116, 0xffff0000, v207
	v_and_b32_e32 v113, 0xffff0000, v201
	v_and_b32_e32 v112, 0xffff0000, v206
	v_and_b32_e32 v121, 0xffff0000, v203
	v_and_b32_e32 v120, 0xffff0000, v209
	v_lshlrev_b32_e32 v122, 16, v210
	v_lshlrev_b32_e32 v123, 16, v205
	v_and_b32_e32 v125, 0xffff0000, v205
	v_and_b32_e32 v124, 0xffff0000, v210
	v_lshlrev_b32_e32 v127, 16, v212
	v_lshlrev_b32_e32 v126, 16, v218
	v_and_b32_e32 v129, 0xffff0000, v212
	v_and_b32_e32 v128, 0xffff0000, v218
	v_lshlrev_b32_e32 v131, 16, v213
	v_and_b32_e32 v133, 0xffff0000, v213
	v_and_b32_e32 v132, 0xffff0000, v219
	v_lshlrev_b32_e32 v135, 16, v215
	v_and_b32_e32 v137, 0xffff0000, v215
	v_and_b32_e32 v136, 0xffff0000, v221
	v_lshlrev_b32_e32 v139, 16, v216
	v_and_b32_e32 v141, 0xffff0000, v216
	v_and_b32_e32 v140, 0xffff0000, v222
	s_and_b32 s49, s79, 0x8000
	s_add_i32 s49, s49, 0
	v_add3_u32 v147, s49, v186, v187
	s_add_i32 s53, s31, s49
	s_add_i32 s52, s52, 1
	v_add_u32_e32 v245, s49, v165
	s_waitcnt vmcnt(14)
	v_mov_b32_e32 v93, v58
	v_mov_b32_e32 v91, v60
	v_mov_b32_e32 v92, v94
	v_mov_b32_e32 v58, v95
	v_mov_b32_e32 v90, v96
	v_mov_b32_e32 v60, v97
	v_fma_f32 v95, v93, v111, v70
	v_pk_mul_f32 v[118:119], v[90:91], v[114:115]
	v_fma_f32 v115, v92, v110, v95
	v_add_f32_e32 v111, v119, v72
	v_fma_f32 v95, v61, v117, v73
	v_fma_f32 v97, v59, v113, v71
	v_add_f32_e32 v111, v118, v111
	v_fma_f32 v134, v60, v116, v95
	v_lshlrev_b32_e32 v119, 16, v203
	v_lshlrev_b32_e32 v118, 16, v209
	v_mov_b32_e32 v94, v98
	v_mov_b32_e32 v95, v62
	v_fma_f32 v130, v58, v112, v97
	s_nop 0
	v_fma_f32 v62, v95, v119, v66
	v_fma_f32 v119, v94, v118, v62
	v_mov_b32_e32 v62, v99
	s_nop 0
	v_fma_f32 v97, v63, v121, v67
	v_fma_f32 v138, v62, v120, v97
	v_mov_b32_e32 v96, v100
	v_mov_b32_e32 v97, v64
	s_nop 0
	v_fma_f32 v64, v97, v123, v68
	v_fma_f32 v123, v96, v122, v64
	v_mov_b32_e32 v64, v101
	s_nop 0
	v_fma_f32 v99, v65, v125, v69
	v_fma_f32 v142, v64, v124, v99
	v_mov_b32_e32 v98, v102
	v_mov_b32_e32 v99, v86
	s_nop 0
	v_fma_f32 v86, v99, v127, v115
	v_fma_f32 v115, v98, v126, v86
	v_mov_b32_e32 v86, v103
	s_nop 0
	v_fma_f32 v101, v87, v129, v130
	v_fma_f32 v143, v86, v128, v101
	v_lshlrev_b32_e32 v130, 16, v219
	v_mov_b32_e32 v100, v104
	v_mov_b32_e32 v101, v88
	s_nop 0
	v_fma_f32 v88, v101, v131, v111
	v_fma_f32 v111, v100, v130, v88
	v_mov_b32_e32 v88, v105
	s_nop 0
	v_fma_f32 v103, v89, v133, v134
	v_fma_f32 v144, v88, v132, v103
	v_lshlrev_b32_e32 v134, 16, v221
	s_waitcnt vmcnt(7)
	v_mov_b32_e32 v102, v106
	s_waitcnt vmcnt(6)
	v_mov_b32_e32 v103, v74
	s_nop 0
	v_fma_f32 v74, v103, v135, v119
	v_fma_f32 v119, v102, v134, v74
	v_mov_b32_e32 v74, v107
	s_nop 0
	v_fma_f32 v105, v75, v137, v138
	v_fma_f32 v145, v74, v136, v105
	v_lshlrev_b32_e32 v138, 16, v222
	v_mov_b32_e32 v104, v108
	v_mov_b32_e32 v105, v76
	s_nop 0
	v_fma_f32 v76, v105, v139, v123
	v_fma_f32 v123, v104, v138, v76
	v_mov_b32_e32 v76, v109
	s_nop 0
	v_fma_f32 v107, v77, v141, v142
	v_fma_f32 v109, v76, v140, v107
	v_cvt_pk_bf16_f32 v106, v115, v143
	v_cvt_pk_bf16_f32 v107, v111, v144
	v_add3_u32 v111, s49, v184, v185
	v_cvt_pk_bf16_f32 v108, v119, v145
	v_cvt_pk_bf16_f32 v109, v123, v109
	ds_write_b128 v111, v[106:109]
	v_pk_mov_b32 v[106:107], v[126:127], v[110:111] op_sel:[1,0]
	v_lshlrev_b32_e32 v111, 16, v224
	v_lshlrev_b32_e32 v110, 16, v228
	v_fma_f32 v107, v93, v107, v70
	v_fma_f32 v108, v92, v106, v107
	v_pk_mov_b32 v[106:107], v[128:129], v[112:113] op_sel:[1,0]
	v_pk_mov_b32 v[112:113], v[110:111], v[126:127] op_sel:[1,0]
	s_nop 0
	v_fma_f32 v107, v59, v107, v71
	v_fma_f32 v109, v58, v106, v107
	v_pk_mov_b32 v[106:107], v[130:131], v[114:115] op_sel:[1,0]
	v_and_b32_e32 v115, 0xffff0000, v224
	s_nop 0
	v_fma_f32 v107, v91, v107, v72
	v_fma_f32 v123, v90, v106, v107
	v_pk_mov_b32 v[106:107], v[132:133], v[116:117] op_sel:[1,0]
	s_nop 0
	s_nop 0
	v_fma_f32 v107, v61, v107, v73
	v_fma_f32 v142, v60, v106, v107
	v_pk_mov_b32 v[106:107], v[134:135], v[118:119] op_sel:[1,0]
	s_nop 0
	s_nop 0
	v_fma_f32 v107, v95, v107, v66
	v_fma_f32 v143, v94, v106, v107
	v_pk_mov_b32 v[106:107], v[136:137], v[120:121] op_sel:[1,0]
	s_nop 0
	s_nop 0
	v_fma_f32 v107, v63, v107, v67
	v_fma_f32 v144, v62, v106, v107
	v_pk_mov_b32 v[106:107], v[138:139], v[122:123] op_sel:[1,0]
	s_nop 0
	s_nop 0
	v_fma_f32 v107, v97, v107, v68
	v_fma_f32 v145, v96, v106, v107
	v_pk_mov_b32 v[106:107], v[140:141], v[124:125] op_sel:[1,0]
	s_nop 0
	s_nop 0
	v_fma_f32 v107, v65, v107, v69
	v_fma_f32 v146, v64, v106, v107
	v_pk_mul_f32 v[106:107], v[92:93], v[126:127]
	v_lshlrev_b32_e32 v127, 16, v226
	v_add_f32_e32 v107, v107, v70
	v_add_f32_e32 v114, v106, v107
	v_pk_mul_f32 v[92:93], v[92:93], v[112:113]
	v_fma_f32 v107, v59, v129, v71
	v_fma_f32 v118, v58, v128, v107
	v_add_f32_e32 v70, v93, v70
	v_fma_f32 v107, v91, v131, v72
	v_fma_f32 v122, v90, v130, v107
	v_add_f32_e32 v70, v92, v70
	v_fma_f32 v107, v61, v133, v73
	v_fma_f32 v148, v60, v132, v107
	s_nop 0
	v_fma_f32 v107, v95, v135, v66
	v_fma_f32 v149, v94, v134, v107
	s_nop 0
	v_fma_f32 v107, v63, v137, v67
	v_fma_f32 v150, v62, v136, v107
	s_nop 0
	v_fma_f32 v107, v97, v139, v68
	v_fma_f32 v151, v96, v138, v107
	s_nop 0
	v_fma_f32 v107, v65, v141, v69
	v_fma_f32 v152, v64, v140, v107
	s_nop 0
	v_fma_f32 v107, v99, v113, v108
	v_fma_f32 v119, v98, v112, v107
	s_nop 0
	v_fma_f32 v107, v99, v111, v114
	v_and_b32_e32 v114, 0xffff0000, v228
	v_pk_mov_b32 v[116:117], v[114:115], v[128:129] op_sel:[1,0]
	v_fma_f32 v111, v98, v110, v107
	v_pk_mul_f32 v[58:59], v[58:59], v[116:117]
	v_fma_f32 v107, v87, v117, v109
	v_fma_f32 v106, v86, v116, v107
	v_cvt_pk_bf16_f32 v106, v119, v106
	v_lshlrev_b32_e32 v119, 16, v225
	v_fma_f32 v107, v87, v115, v118
	v_lshlrev_b32_e32 v118, 16, v229
	v_pk_mov_b32 v[120:121], v[118:119], v[130:131] op_sel:[1,0]
	v_fma_f32 v115, v86, v114, v107
	v_and_b32_e32 v131, 0xffff0000, v226
	v_fma_f32 v107, v101, v121, v123
	v_fma_f32 v107, v100, v120, v107
	v_and_b32_e32 v123, 0xffff0000, v225
	v_fma_f32 v109, v101, v119, v122
	v_and_b32_e32 v122, 0xffff0000, v229
	v_pk_mov_b32 v[124:125], v[122:123], v[132:133] op_sel:[1,0]
	v_fma_f32 v119, v100, v118, v109
	v_and_b32_e32 v130, 0xffff0000, v230
	v_fma_f32 v109, v89, v125, v142
	v_fma_f32 v126, v88, v124, v109
	v_cvt_pk_bf16_f32 v107, v107, v126
	v_lshlrev_b32_e32 v126, 16, v230
	v_fma_f32 v109, v89, v123, v148
	v_pk_mov_b32 v[128:129], v[126:127], v[134:135] op_sel:[1,0]
	v_fma_f32 v123, v88, v122, v109
	v_pk_mov_b32 v[132:133], v[130:131], v[136:137] op_sel:[1,0]
	v_fma_f32 v109, v103, v129, v143
	v_fma_f32 v142, v102, v128, v109
	v_add_f32_e32 v59, v59, v71
	v_fma_f32 v109, v103, v127, v149
	v_fma_f32 v127, v102, v126, v109
	v_fma_f32 v109, v75, v133, v144
	v_add_f32_e32 v71, v58, v59
	v_fma_f32 v108, v74, v132, v109
	v_fma_f32 v109, v75, v131, v150
	v_fma_f32 v59, v91, v121, v72
	v_fma_f32 v131, v74, v130, v109
	v_lshlrev_b32_e32 v134, 16, v231
	v_lshlrev_b32_e32 v135, 16, v227
	v_fma_f32 v72, v90, v120, v59
	v_pk_mov_b32 v[136:137], v[134:135], v[138:139] op_sel:[1,0]
	v_fma_f32 v59, v61, v125, v73
	v_fma_f32 v60, v60, v124, v59
	v_fma_f32 v109, v105, v137, v145
	v_fma_f32 v59, v95, v129, v66
	v_fma_f32 v109, v104, v136, v109
	v_fma_f32 v61, v94, v128, v59
	v_fma_f32 v135, v105, v135, v151
	v_fma_f32 v59, v63, v133, v67
	v_fma_f32 v135, v104, v134, v135
	v_and_b32_e32 v139, 0xffff0000, v227
	v_and_b32_e32 v138, 0xffff0000, v231
	v_fma_f32 v62, v62, v132, v59
	v_pk_mov_b32 v[140:141], v[138:139], v[140:141] op_sel:[1,0]
	v_fma_f32 v59, v97, v137, v68
	v_fma_f32 v63, v96, v136, v59
	v_cvt_pk_bf16_f32 v108, v142, v108
	v_fma_f32 v59, v65, v141, v69
	v_fma_f32 v64, v64, v140, v59
	v_lshlrev_b32_e32 v58, 16, v232
	v_mov_b32_e32 v59, v110
	v_fma_f32 v143, v77, v141, v146
	v_fma_f32 v59, v99, v59, v70
	v_fma_f32 v65, v98, v58, v59
	v_and_b32_e32 v58, 0xffff0000, v232
	v_mov_b32_e32 v59, v114
	v_fma_f32 v144, v76, v140, v143
	v_fma_f32 v59, v87, v59, v71
	v_fma_f32 v66, v86, v58, v59
	v_lshlrev_b32_e32 v58, 16, v233
	v_mov_b32_e32 v59, v118
	v_pk_mul_f32 v[142:143], v[76:77], v[138:139]
	v_fma_f32 v59, v101, v59, v72
	v_fma_f32 v67, v100, v58, v59
	v_and_b32_e32 v58, 0xffff0000, v233
	v_mov_b32_e32 v59, v122
	v_add_f32_e32 v139, v143, v152
	v_fma_f32 v59, v89, v59, v60
	v_fma_f32 v60, v88, v58, v59
	v_lshlrev_b32_e32 v58, 16, v234
	v_mov_b32_e32 v59, v126
	v_cvt_pk_bf16_f32 v109, v109, v144
	ds_write_b128 v147, v[106:109]
	v_fma_f32 v59, v103, v59, v61
	v_fma_f32 v61, v102, v58, v59
	v_and_b32_e32 v58, 0xffff0000, v234
	v_mov_b32_e32 v59, v130
	v_add_f32_e32 v109, v142, v139
	v_fma_f32 v59, v75, v59, v62
	v_fma_f32 v62, v74, v58, v59
	v_lshlrev_b32_e32 v58, 16, v235
	v_mov_b32_e32 v59, v134
	v_cvt_pk_bf16_f32 v106, v111, v115
	v_add3_u32 v111, s49, v188, v189
	v_fma_f32 v59, v105, v59, v63
	v_fma_f32 v63, v104, v58, v59
	v_and_b32_e32 v58, 0xffff0000, v235
	v_mov_b32_e32 v59, v138
	v_cvt_pk_bf16_f32 v107, v119, v123
	v_cvt_pk_bf16_f32 v108, v127, v131
	v_cvt_pk_bf16_f32 v109, v135, v109
	ds_write_b128 v111, v[106:109]
	v_fma_f32 v59, v77, v59, v64
	v_fma_f32 v64, v76, v58, v59
	v_cvt_pk_bf16_f32 v58, v65, v66
	v_cvt_pk_bf16_f32 v59, v67, v60
	v_cvt_pk_bf16_f32 v60, v61, v62
	v_add3_u32 v62, s49, v190, v191
	v_cvt_pk_bf16_f32 v61, v63, v64
	ds_write_b128 v62, v[58:61]
	v_add_u32_e32 v58, s53, v192
	v_add_u32_e32 v242, v58, v193
	s_waitcnt lgkmcnt(0)
	s_barrier
	ds_read_b128 v[58:61], v242
	ds_read_b128 v[62:65], v242 offset:4096
	ds_read_b128 v[98:101], v242 offset:8192
	ds_read_b128 v[102:105], v242 offset:12288
	s_waitcnt lgkmcnt(3)
	v_mfma_f32_16x16x32_bf16 v[66:69], v[42:45], v[58:61], 0
	v_mfma_f32_16x16x32_bf16 v[70:73], v[46:49], v[58:61], 0
	v_mfma_f32_16x16x32_bf16 v[74:77], v[50:53], v[58:61], 0
	s_waitcnt vmcnt(3)
	v_mfma_f32_16x16x32_bf16 v[58:61], v[54:57], v[58:61], 0
	s_waitcnt lgkmcnt(2)
	v_mfma_f32_16x16x32_bf16 v[86:89], v[42:45], v[62:65], 0
	v_mfma_f32_16x16x32_bf16 v[90:93], v[46:49], v[62:65], 0
	v_mfma_f32_16x16x32_bf16 v[94:97], v[50:53], v[62:65], 0
	v_mfma_f32_16x16x32_bf16 v[62:65], v[54:57], v[62:65], 0
	s_waitcnt lgkmcnt(1)
	v_mfma_f32_16x16x32_bf16 v[106:109], v[42:45], v[98:101], 0
	v_mfma_f32_16x16x32_bf16 v[110:113], v[46:49], v[98:101], 0
	v_mfma_f32_16x16x32_bf16 v[114:117], v[50:53], v[98:101], 0
	v_mfma_f32_16x16x32_bf16 v[98:101], v[54:57], v[98:101], 0
	s_waitcnt lgkmcnt(0)
	v_mfma_f32_16x16x32_bf16 v[42:45], v[42:45], v[102:105], 0
	v_mfma_f32_16x16x32_bf16 v[46:49], v[46:49], v[102:105], 0
	v_mfma_f32_16x16x32_bf16 v[50:53], v[50:53], v[102:105], 0
	v_mfma_f32_16x16x32_bf16 v[54:57], v[54:57], v[102:105], 0
	v_add_u32_e32 v102, s53, v194
	v_add_u32_e32 v243, v102, v193
	ds_read_b128 v[102:105], v243
	ds_read_b128 v[118:121], v243 offset:4096
	s_waitcnt lgkmcnt(1)
	v_mfma_f32_16x16x32_bf16 v[66:69], v[26:29], v[102:105], v[66:69]
	v_mfma_f32_16x16x32_bf16 v[70:73], v[30:33], v[102:105], v[70:73]
	v_mfma_f32_16x16x32_bf16 v[74:77], v[34:37], v[102:105], v[74:77]
	s_waitcnt vmcnt(2)
	v_mfma_f32_16x16x32_bf16 v[58:61], v[38:41], v[102:105], v[58:61]
	s_waitcnt lgkmcnt(0)
	v_mfma_f32_16x16x32_bf16 v[86:89], v[26:29], v[118:121], v[86:89]
	v_mfma_f32_16x16x32_bf16 v[90:93], v[30:33], v[118:121], v[90:93]
	v_mfma_f32_16x16x32_bf16 v[94:97], v[34:37], v[118:121], v[94:97]
	v_mfma_f32_16x16x32_bf16 v[62:65], v[38:41], v[118:121], v[62:65]
	ds_read_b128 v[102:105], v243 offset:8192
	ds_read_b128 v[118:121], v243 offset:12288
	s_waitcnt lgkmcnt(1)
	v_mfma_f32_16x16x32_bf16 v[106:109], v[26:29], v[102:105], v[106:109]
	s_waitcnt lgkmcnt(0)
	v_mfma_f32_16x16x32_bf16 v[26:29], v[26:29], v[118:121], v[42:45]
	s_nop 2
	v_add_u32_e32 v42, s53, v195
	v_add_u32_e32 v244, v42, v193
	v_mfma_f32_16x16x32_bf16 v[110:113], v[30:33], v[102:105], v[110:113]
	v_mfma_f32_16x16x32_bf16 v[30:33], v[30:33], v[118:121], v[46:49]
	ds_read_b128 v[42:45], v244
	s_nop 1
	ds_read_b128 v[46:49], v244 offset:4096
	v_mfma_f32_16x16x32_bf16 v[114:117], v[34:37], v[102:105], v[114:117]
	v_mfma_f32_16x16x32_bf16 v[98:101], v[38:41], v[102:105], v[98:101]
	v_mfma_f32_16x16x32_bf16 v[34:37], v[34:37], v[118:121], v[50:53]
	v_mfma_f32_16x16x32_bf16 v[38:41], v[38:41], v[118:121], v[54:57]
	s_waitcnt lgkmcnt(1)
	v_mfma_f32_16x16x32_bf16 v[50:53], v[10:13], v[42:45], v[66:69]
	v_mfma_f32_16x16x32_bf16 v[54:57], v[14:17], v[42:45], v[70:73]
	v_mfma_f32_16x16x32_bf16 v[66:69], v[18:21], v[42:45], v[74:77]
	s_waitcnt vmcnt(1)
	v_mfma_f32_16x16x32_bf16 v[42:45], v[22:25], v[42:45], v[58:61]
	s_waitcnt lgkmcnt(0)
	v_mfma_f32_16x16x32_bf16 v[58:61], v[10:13], v[46:49], v[86:89]
	v_mfma_f32_16x16x32_bf16 v[70:73], v[14:17], v[46:49], v[90:93]
	v_mfma_f32_16x16x32_bf16 v[74:77], v[18:21], v[46:49], v[94:97]
	v_mfma_f32_16x16x32_bf16 v[46:49], v[22:25], v[46:49], v[62:65]
	s_nop 2
	ds_read_b128 v[62:65], v244 offset:8192
	ds_read_b128 v[86:89], v244 offset:12288
	s_waitcnt lgkmcnt(1)
	v_mfma_f32_16x16x32_bf16 v[114:117], v[18:21], v[62:65], v[114:117]
	s_waitcnt lgkmcnt(0)
	v_mfma_f32_16x16x32_bf16 v[176:179], v[18:21], v[86:89], v[34:37]
	v_add_u32_e32 v18, s53, v196
	v_add_u32_e32 v241, v18, v193
	s_ashr_i32 s53, s52, 31
	v_mfma_f32_16x16x32_bf16 v[90:93], v[10:13], v[62:65], v[106:109]
	s_lshl_b64 s[52:53], s[52:53], 16
	v_mfma_f32_16x16x32_bf16 v[110:113], v[14:17], v[62:65], v[110:113]
	v_mfma_f32_16x16x32_bf16 v[62:65], v[22:25], v[62:65], v[98:101]
	v_mfma_f32_16x16x32_bf16 v[180:183], v[22:25], v[86:89], v[38:41]
	ds_read_b128 v[18:21], v241
	ds_read_b128 v[22:25], v241 offset:4096
	s_waitcnt lgkmcnt(1)
	v_mfma_f32_16x16x32_bf16 v[150:153], v[2:5], v[18:21], v[50:53]
	v_mfma_f32_16x16x32_bf16 v[146:149], v[6:9], v[18:21], v[54:57]
	v_mfma_f32_16x16x32_bf16 v[106:109], v[78:81], v[18:21], v[66:69]
	s_waitcnt vmcnt(0)
	v_mfma_f32_16x16x32_bf16 v[102:105], v[82:85], v[18:21], v[42:45]
	ds_read_b128 v[18:21], v241 offset:8192
	ds_read_b128 v[246:249], v241 offset:12288
	s_waitcnt lgkmcnt(2)
	v_mfma_f32_16x16x32_bf16 v[142:145], v[2:5], v[22:25], v[58:61]
	v_mfma_f32_16x16x32_bf16 v[138:141], v[6:9], v[22:25], v[70:73]
	v_mfma_f32_16x16x32_bf16 v[98:101], v[78:81], v[22:25], v[74:77]
	v_mfma_f32_16x16x32_bf16 v[94:97], v[82:85], v[22:25], v[46:49]
	v_add_u32_e32 v22, s48, v159
	v_ashrrev_i32_e32 v23, 31, v22
	v_lshlrev_b64 v[24:25], 2, v[22:23]
	v_lshl_add_u64 v[174:175], s[12:13], 0, v[24:25]
	s_waitcnt lgkmcnt(1)
	v_mfma_f32_16x16x32_bf16 v[134:137], v[2:5], v[18:21], v[90:93]
	v_lshl_add_u64 v[172:173], s[16:17], 0, v[24:25]
	v_add_u32_e32 v22, 16, v22
	v_ashrrev_i32_e32 v23, 31, v22
	v_mfma_f32_16x16x32_bf16 v[90:93], v[78:81], v[18:21], v[114:117]
	global_load_dwordx4 v[118:121], v[174:175], off
	global_load_dwordx4 v[74:77], v[174:175], off offset:64
	s_nop 0
	global_load_dwordx4 v[114:117], v[172:173], off
	global_load_dwordx4 v[70:73], v[172:173], off offset:64
	v_lshl_add_u64 v[168:169], s[18:19], 0, v[24:25]
	s_waitcnt vmcnt(3)
	v_pk_add_f32 v[150:151], v[118:119], v[150:151]
	v_mfma_f32_16x16x32_bf16 v[10:13], v[10:13], v[86:89], v[26:29]
	s_waitcnt vmcnt(1)
	v_pk_add_f32 v[146:147], v[114:115], v[146:147]
	v_pk_mul_f32 v[150:151], v[150:151], s[44:45] op_sel_hi:[1,0]
	v_pk_mul_f32 v[146:147], v[146:147], s[44:45] op_sel_hi:[1,0]
	v_mfma_f32_16x16x32_bf16 v[14:17], v[14:17], v[86:89], v[30:33]
	v_exp_f32_e32 v150, v150
	v_exp_f32_e32 v151, v151
	s_waitcnt lgkmcnt(0)
	v_mfma_f32_16x16x32_bf16 v[126:129], v[2:5], v[246:249], v[10:13]
	v_lshl_add_u64 v[2:3], v[22:23], 2, s[18:19]
	s_nop 1
	v_lshl_add_u64 v[10:11], v[156:157], 0, s[52:53]
	v_add_co_u32_e32 v12, vcc, s3, v10
	v_mfma_f32_16x16x32_bf16 v[130:133], v[6:9], v[18:21], v[110:113]
	s_nop 0
	v_addc_co_u32_e32 v13, vcc, 0, v11, vcc
	s_nop 0
	global_load_dwordx4 v[110:113], v[168:169], off
	global_load_dwordx4 v[66:69], v[2:3], off
	v_mfma_f32_16x16x32_bf16 v[122:125], v[6:9], v[246:249], v[14:17]
	v_add_co_u32_e32 v6, vcc, s29, v10
	s_nop 1
	v_addc_co_u32_e32 v7, vcc, 0, v11, vcc
	v_mfma_f32_16x16x32_bf16 v[86:89], v[82:85], v[18:21], v[62:65]
	global_load_dwordx4 v[46:49], v[10:11], off
	global_load_dwordx4 v[30:33], v[10:11], off offset:1024
	global_load_dwordx4 v[18:21], v[10:11], off offset:2048
	global_load_dwordx4 v[2:5], v[10:11], off offset:3072
	global_load_dwordx4 v[38:41], v[12:13], off offset:1024
	global_load_dwordx4 v[22:25], v[12:13], off offset:2048
	global_load_dwordx4 v[54:57], v[6:7], off offset:-4096
	global_load_dwordx4 v[58:61], v[6:7], off
	global_load_dwordx4 v[42:45], v[6:7], off offset:1024
	global_load_dwordx4 v[26:29], v[6:7], off offset:2048
	s_nop 0
	global_load_dwordx4 v[6:9], v[6:7], off offset:3072
	v_add_co_u32_e32 v10, vcc, s47, v10
	v_mfma_f32_16x16x32_bf16 v[78:81], v[78:81], v[246:249], v[176:179]
	s_nop 0
	v_addc_co_u32_e32 v11, vcc, 0, v11, vcc
	global_load_dwordx4 v[14:17], v[12:13], off offset:3072
	global_load_dwordx4 v[62:65], v[10:11], off
	global_load_dwordx4 v[50:53], v[10:11], off offset:1024
	global_load_dwordx4 v[34:37], v[10:11], off offset:2048
	s_nop 0
	global_load_dwordx4 v[10:13], v[10:11], off offset:3072
	v_exp_f32_e32 v176, v146
	v_exp_f32_e32 v177, v147
	v_pk_add_f32 v[146:147], v[150:151], 1.0 op_sel_hi:[1,0]
	v_mfma_f32_16x16x32_bf16 v[82:85], v[82:85], v[246:249], v[180:183]
	v_add_f32_e64 v176, v176, 1.0
	v_add_f32_e64 v177, v177, 1.0
	v_pk_mul_f32 v[150:151], v[146:147], v[176:177]
	s_nop 0
	v_rcp_f32_e32 v178, v150
	v_rcp_f32_e32 v179, v151
	v_add_u32_e32 v150, v245, v197
	v_add_u32_e32 v154, v150, v198
	ds_read_b64 v[150:151], v154
	v_pk_mul_f32 v[176:177], v[176:177], v[178:179]
	s_waitcnt vmcnt(17)
	v_pk_mul_f32 v[176:177], v[110:111], v[176:177]
	s_nop 0
	v_pk_mul_f32 v[182:183], v[176:177], s[98:99] op_sel_hi:[1,0]
	s_nop 0
	v_pk_fma_f32 v[180:181], v[182:183], s[46:47], v[164:165] op_sel_hi:[1,0,0]
	v_min_f32_e32 v170, v182, v183
	v_pk_fma_f32 v[180:181], v[182:183], v[180:181], 0.5 op_sel_hi:[1,1,0]
	v_cmp_ge_f32_e32 vcc, s66, v170
	v_pk_fma_f32 v[180:181], v[182:183], v[180:181], 1.0 op_sel_hi:[1,1,0]
	s_nop 0
	v_pk_mul_f32 v[180:181], v[180:181], v[182:183] neg_lo:[0,1] neg_hi:[0,1]
	s_and_saveexec_b64 s[52:53], vcc
	s_cbranch_execnz .LBB0_1308
.LBB0_1263:
	s_or_b64 exec, exec, s[52:53]
	v_pk_add_f32 v[152:153], v[120:121], v[152:153]
	v_pk_add_f32 v[148:149], v[116:117], v[148:149]
	v_pk_mul_f32 v[152:153], v[152:153], s[44:45] op_sel_hi:[1,0]
	v_pk_mul_f32 v[148:149], v[148:149], s[44:45] op_sel_hi:[1,0]
	v_exp_f32_e32 v152, v152
	v_exp_f32_e32 v153, v153
	v_exp_f32_e32 v148, v148
	v_exp_f32_e32 v149, v149
	v_pk_mul_f32 v[146:147], v[146:147], v[178:179]
	v_pk_add_f32 v[152:153], v[152:153], 1.0 op_sel_hi:[1,0]
	v_sqrt_f32_e32 v180, v180
	v_pk_add_f32 v[148:149], v[148:149], 1.0 op_sel_hi:[1,0]
	v_sqrt_f32_e32 v181, v181
	v_pk_mul_f32 v[178:179], v[152:153], v[148:149]
	s_waitcnt lgkmcnt(0)
	v_lshlrev_b32_e32 v182, 16, v150
	v_rcp_f32_e32 v178, v178
	v_rcp_f32_e32 v179, v179
	v_and_b32_e32 v183, 0xffff0000, v150
	v_pk_mul_f32 v[146:147], v[146:147], v[180:181]
	v_pk_mul_f32 v[148:149], v[148:149], v[178:179]
	s_nop 0
	v_pk_mul_f32 v[148:149], v[112:113], v[148:149]
	v_pk_mul_f32 v[146:147], v[146:147], v[182:183]
	v_pk_mul_f32 v[180:181], v[148:149], s[98:99] op_sel_hi:[1,0]
	v_cvt_pk_bf16_f32 v146, v176, v146
	v_cvt_pk_bf16_f32 v147, v177, v147
	s_nop 0
	v_pk_fma_f32 v[176:177], v[180:181], s[46:47], v[164:165] op_sel_hi:[1,0,0]
	v_min_f32_e32 v150, v180, v181
	v_pk_fma_f32 v[176:177], v[180:181], v[176:177], 0.5 op_sel_hi:[1,1,0]
	v_cmp_ge_f32_e32 vcc, s66, v150
	v_pk_fma_f32 v[176:177], v[180:181], v[176:177], 1.0 op_sel_hi:[1,1,0]
	s_nop 0
	v_pk_mul_f32 v[176:177], v[176:177], v[180:181] neg_lo:[0,1] neg_hi:[0,1]
	s_and_saveexec_b64 s[52:53], vcc
	s_cbranch_execnz .LBB0_1309
.LBB0_1264:
	s_or_b64 exec, exec, s[52:53]
	v_sqrt_f32_e32 v176, v176
	v_sqrt_f32_e32 v177, v177
	v_pk_add_f32 v[142:143], v[118:119], v[142:143]
	v_pk_add_f32 v[138:139], v[114:115], v[138:139]
	v_pk_mul_f32 v[152:153], v[152:153], v[178:179]
	v_pk_mul_f32 v[142:143], v[142:143], s[44:45] op_sel_hi:[1,0]
	v_pk_mul_f32 v[138:139], v[138:139], s[44:45] op_sel_hi:[1,0]
	v_pk_mul_f32 v[152:153], v[152:153], v[176:177]
	v_exp_f32_e32 v142, v142
	v_exp_f32_e32 v143, v143
	v_exp_f32_e32 v176, v138
	v_exp_f32_e32 v177, v139
	v_lshlrev_b32_e32 v150, 16, v151
	v_pk_add_f32 v[138:139], v[142:143], 1.0 op_sel_hi:[1,0]
	v_and_b32_e32 v151, 0xffff0000, v151
	v_pk_add_f32 v[176:177], v[176:177], 1.0 op_sel_hi:[1,0]
	v_pk_mul_f32 v[152:153], v[152:153], v[150:151]
	v_pk_mul_f32 v[142:143], v[138:139], v[176:177]
	v_cvt_pk_bf16_f32 v148, v148, v152
	v_cvt_pk_bf16_f32 v149, v149, v153
	ds_write_b128 v236, v[146:149]
	v_rcp_f32_e32 v150, v142
	v_rcp_f32_e32 v151, v143
	ds_read_b64 v[142:143], v154 offset:4096
	v_pk_mul_f32 v[146:147], v[176:177], v[150:151]
	s_nop 0
	v_pk_mul_f32 v[146:147], v[110:111], v[146:147]
	s_nop 0
	v_pk_mul_f32 v[152:153], v[146:147], s[98:99] op_sel_hi:[1,0]
	s_nop 0
	v_pk_fma_f32 v[148:149], v[152:153], s[46:47], v[164:165] op_sel_hi:[1,0,0]
	v_min_f32_e32 v170, v152, v153
	v_pk_fma_f32 v[148:149], v[152:153], v[148:149], 0.5 op_sel_hi:[1,1,0]
	v_cmp_ge_f32_e32 vcc, s66, v170
	v_pk_fma_f32 v[148:149], v[152:153], v[148:149], 1.0 op_sel_hi:[1,1,0]
	s_nop 0
	v_pk_mul_f32 v[148:149], v[148:149], v[152:153] neg_lo:[0,1] neg_hi:[0,1]
	s_and_saveexec_b64 s[52:53], vcc
	s_cbranch_execnz .LBB0_1310
.LBB0_1265:
	s_or_b64 exec, exec, s[52:53]
	v_pk_add_f32 v[144:145], v[120:121], v[144:145]
	v_pk_add_f32 v[140:141], v[116:117], v[140:141]
	v_pk_mul_f32 v[144:145], v[144:145], s[44:45] op_sel_hi:[1,0]
	v_pk_mul_f32 v[140:141], v[140:141], s[44:45] op_sel_hi:[1,0]
	v_exp_f32_e32 v144, v144
	v_exp_f32_e32 v145, v145
	v_exp_f32_e32 v140, v140
	v_exp_f32_e32 v141, v141
	v_sqrt_f32_e32 v148, v148
	v_sqrt_f32_e32 v149, v149
	v_pk_mul_f32 v[138:139], v[138:139], v[150:151]
	v_pk_add_f32 v[144:145], v[144:145], 1.0 op_sel_hi:[1,0]
	v_pk_add_f32 v[140:141], v[140:141], 1.0 op_sel_hi:[1,0]
	v_pk_mul_f32 v[138:139], v[138:139], v[148:149]
	v_pk_mul_f32 v[148:149], v[144:145], v[140:141]
	s_waitcnt lgkmcnt(0)
	v_lshlrev_b32_e32 v152, 16, v142
	v_rcp_f32_e32 v148, v148
	v_rcp_f32_e32 v149, v149
	v_and_b32_e32 v153, 0xffff0000, v142
	v_pk_mul_f32 v[138:139], v[138:139], v[152:153]
	v_pk_mul_f32 v[140:141], v[140:141], v[148:149]
	s_nop 0
	v_pk_mul_f32 v[140:141], v[112:113], v[140:141]
	v_cvt_pk_bf16_f32 v138, v146, v138
	v_cvt_pk_bf16_f32 v139, v147, v139
	s_nop 0
	v_pk_mul_f32 v[146:147], v[140:141], s[98:99] op_sel_hi:[1,0]
	s_nop 0
	v_pk_fma_f32 v[150:151], v[146:147], s[46:47], v[164:165] op_sel_hi:[1,0,0]
	v_min_f32_e32 v142, v146, v147
	v_pk_fma_f32 v[150:151], v[146:147], v[150:151], 0.5 op_sel_hi:[1,1,0]
	v_cmp_ge_f32_e32 vcc, s66, v142
	v_pk_fma_f32 v[150:151], v[146:147], v[150:151], 1.0 op_sel_hi:[1,1,0]
	s_nop 0
	v_pk_mul_f32 v[150:151], v[150:151], v[146:147] neg_lo:[0,1] neg_hi:[0,1]
	s_and_saveexec_b64 s[52:53], vcc
	s_cbranch_execnz .LBB0_1311
.LBB0_1266:
	s_or_b64 exec, exec, s[52:53]
	v_sqrt_f32_e32 v146, v150
	v_sqrt_f32_e32 v147, v151
	v_pk_add_f32 v[134:135], v[118:119], v[134:135]
	v_pk_add_f32 v[130:131], v[114:115], v[130:131]
	v_pk_mul_f32 v[144:145], v[144:145], v[148:149]
	v_pk_mul_f32 v[134:135], v[134:135], s[44:45] op_sel_hi:[1,0]
	v_pk_mul_f32 v[130:131], v[130:131], s[44:45] op_sel_hi:[1,0]
	v_pk_mul_f32 v[144:145], v[144:145], v[146:147]
	v_exp_f32_e32 v134, v134
	v_exp_f32_e32 v135, v135
	v_exp_f32_e32 v146, v130
	v_exp_f32_e32 v147, v131
	v_lshlrev_b32_e32 v142, 16, v143
	v_pk_add_f32 v[130:131], v[134:135], 1.0 op_sel_hi:[1,0]
	v_and_b32_e32 v143, 0xffff0000, v143
	v_pk_add_f32 v[146:147], v[146:147], 1.0 op_sel_hi:[1,0]
	v_pk_mul_f32 v[144:145], v[144:145], v[142:143]
	v_pk_mul_f32 v[134:135], v[130:131], v[146:147]
	v_cvt_pk_bf16_f32 v140, v140, v144
	v_cvt_pk_bf16_f32 v141, v141, v145
	ds_write_b128 v236, v[138:141] offset:2432
	v_rcp_f32_e32 v142, v134
	v_rcp_f32_e32 v143, v135
	ds_read_b64 v[134:135], v154 offset:8192
	v_pk_mul_f32 v[138:139], v[146:147], v[142:143]
	s_nop 0
	v_pk_mul_f32 v[138:139], v[110:111], v[138:139]
	s_nop 0
	v_pk_mul_f32 v[144:145], v[138:139], s[98:99] op_sel_hi:[1,0]
	s_nop 0
	v_pk_fma_f32 v[140:141], v[144:145], s[46:47], v[164:165] op_sel_hi:[1,0,0]
	v_min_f32_e32 v146, v144, v145
	v_pk_fma_f32 v[140:141], v[144:145], v[140:141], 0.5 op_sel_hi:[1,1,0]
	v_cmp_ge_f32_e32 vcc, s66, v146
	v_pk_fma_f32 v[140:141], v[144:145], v[140:141], 1.0 op_sel_hi:[1,1,0]
	s_nop 0
	v_pk_mul_f32 v[140:141], v[140:141], v[144:145] neg_lo:[0,1] neg_hi:[0,1]
	s_and_saveexec_b64 s[52:53], vcc
	s_cbranch_execnz .LBB0_1312
.LBB0_1267:
	s_or_b64 exec, exec, s[52:53]
	v_pk_add_f32 v[136:137], v[120:121], v[136:137]
	v_pk_add_f32 v[132:133], v[116:117], v[132:133]
	v_pk_mul_f32 v[136:137], v[136:137], s[44:45] op_sel_hi:[1,0]
	v_pk_mul_f32 v[132:133], v[132:133], s[44:45] op_sel_hi:[1,0]
	v_exp_f32_e32 v136, v136
	v_exp_f32_e32 v137, v137
	v_exp_f32_e32 v132, v132
	v_exp_f32_e32 v133, v133
	v_sqrt_f32_e32 v140, v140
	v_sqrt_f32_e32 v141, v141
	v_pk_mul_f32 v[130:131], v[130:131], v[142:143]
	v_pk_add_f32 v[136:137], v[136:137], 1.0 op_sel_hi:[1,0]
	v_pk_add_f32 v[132:133], v[132:133], 1.0 op_sel_hi:[1,0]
	v_pk_mul_f32 v[130:131], v[130:131], v[140:141]
	v_pk_mul_f32 v[140:141], v[136:137], v[132:133]
	s_waitcnt lgkmcnt(0)
	v_lshlrev_b32_e32 v144, 16, v134
	v_rcp_f32_e32 v140, v140
	v_rcp_f32_e32 v141, v141
	v_and_b32_e32 v145, 0xffff0000, v134
	v_pk_mul_f32 v[130:131], v[130:131], v[144:145]
	v_pk_mul_f32 v[132:133], v[132:133], v[140:141]
	s_nop 0
	v_pk_mul_f32 v[132:133], v[112:113], v[132:133]
	v_cvt_pk_bf16_f32 v130, v138, v130
	v_cvt_pk_bf16_f32 v131, v139, v131
	s_nop 0
	v_pk_mul_f32 v[138:139], v[132:133], s[98:99] op_sel_hi:[1,0]
	s_nop 0
	v_pk_fma_f32 v[142:143], v[138:139], s[46:47], v[164:165] op_sel_hi:[1,0,0]
	v_min_f32_e32 v134, v138, v139
	v_pk_fma_f32 v[142:143], v[138:139], v[142:143], 0.5 op_sel_hi:[1,1,0]
	v_cmp_ge_f32_e32 vcc, s66, v134
	v_pk_fma_f32 v[142:143], v[138:139], v[142:143], 1.0 op_sel_hi:[1,1,0]
	s_nop 0
	v_pk_mul_f32 v[142:143], v[142:143], v[138:139] neg_lo:[0,1] neg_hi:[0,1]
	s_and_saveexec_b64 s[52:53], vcc
	s_cbranch_execnz .LBB0_1313
.LBB0_1268:
	s_or_b64 exec, exec, s[52:53]
	v_pk_add_f32 v[118:119], v[118:119], v[126:127]
	v_pk_add_f32 v[114:115], v[114:115], v[122:123]
	v_sqrt_f32_e32 v138, v142
	v_sqrt_f32_e32 v139, v143
	v_pk_mul_f32 v[118:119], v[118:119], s[44:45] op_sel_hi:[1,0]
	v_pk_mul_f32 v[114:115], v[114:115], s[44:45] op_sel_hi:[1,0]
	v_exp_f32_e32 v118, v118
	v_exp_f32_e32 v119, v119
	v_exp_f32_e32 v114, v114
	v_exp_f32_e32 v115, v115
	v_pk_mul_f32 v[136:137], v[136:137], v[140:141]
	v_lshlrev_b32_e32 v134, 16, v135
	v_and_b32_e32 v135, 0xffff0000, v135
	v_pk_mul_f32 v[136:137], v[136:137], v[138:139]
	v_pk_add_f32 v[118:119], v[118:119], 1.0 op_sel_hi:[1,0]
	v_pk_mul_f32 v[126:127], v[136:137], v[134:135]
	v_pk_add_f32 v[134:135], v[114:115], 1.0 op_sel_hi:[1,0]
	v_cvt_pk_bf16_f32 v132, v132, v126
	v_cvt_pk_bf16_f32 v133, v133, v127
	ds_write_b128 v236, v[130:133] offset:4864
	v_pk_mul_f32 v[114:115], v[118:119], v[134:135]
	s_nop 0
	v_rcp_f32_e32 v122, v114
	v_rcp_f32_e32 v123, v115
	ds_read_b64 v[114:115], v154 offset:12288
	v_pk_mul_f32 v[126:127], v[134:135], v[122:123]
	s_nop 0
	v_pk_mul_f32 v[110:111], v[110:111], v[126:127]
	s_nop 0
	v_pk_mul_f32 v[130:131], v[110:111], s[98:99] op_sel_hi:[1,0]
	s_nop 0
	v_pk_fma_f32 v[126:127], v[130:131], s[46:47], v[164:165] op_sel_hi:[1,0,0]
	v_min_f32_e32 v132, v130, v131
	v_pk_fma_f32 v[126:127], v[130:131], v[126:127], 0.5 op_sel_hi:[1,1,0]
	v_cmp_ge_f32_e32 vcc, s66, v132
	v_pk_fma_f32 v[126:127], v[130:131], v[126:127], 1.0 op_sel_hi:[1,1,0]
	s_nop 0
	v_pk_mul_f32 v[126:127], v[126:127], v[130:131] neg_lo:[0,1] neg_hi:[0,1]
	s_and_saveexec_b64 s[52:53], vcc
	s_cbranch_execnz .LBB0_1314
.LBB0_1269:
	s_or_b64 exec, exec, s[52:53]
	v_pk_add_f32 v[120:121], v[120:121], v[128:129]
	v_pk_add_f32 v[116:117], v[116:117], v[124:125]
	v_pk_mul_f32 v[120:121], v[120:121], s[44:45] op_sel_hi:[1,0]
	v_pk_mul_f32 v[116:117], v[116:117], s[44:45] op_sel_hi:[1,0]
	v_sqrt_f32_e32 v126, v126
	v_sqrt_f32_e32 v127, v127
	v_exp_f32_e32 v120, v120
	v_exp_f32_e32 v121, v121
	v_exp_f32_e32 v128, v116
	v_exp_f32_e32 v129, v117
	v_pk_mul_f32 v[116:117], v[118:119], v[122:123]
	s_waitcnt lgkmcnt(0)
	v_lshlrev_b32_e32 v124, 16, v114
	v_pk_mul_f32 v[122:123], v[116:117], v[126:127]
	v_pk_add_f32 v[116:117], v[120:121], 1.0 op_sel_hi:[1,0]
	v_pk_add_f32 v[120:121], v[128:129], 1.0 op_sel_hi:[1,0]
	v_and_b32_e32 v125, 0xffff0000, v114
	v_pk_mul_f32 v[118:119], v[116:117], v[120:121]
	v_pk_mul_f32 v[122:123], v[122:123], v[124:125]
	v_rcp_f32_e32 v118, v118
	v_rcp_f32_e32 v119, v119
	v_cvt_pk_bf16_f32 v110, v110, v122
	v_cvt_pk_bf16_f32 v111, v111, v123
	s_nop 0
	v_pk_mul_f32 v[120:121], v[120:121], v[118:119]
	s_nop 0
	v_pk_mul_f32 v[112:113], v[112:113], v[120:121]
	s_nop 0
	v_pk_mul_f32 v[120:121], v[112:113], s[98:99] op_sel_hi:[1,0]
	s_nop 0
	v_pk_fma_f32 v[122:123], v[120:121], s[46:47], v[164:165] op_sel_hi:[1,0,0]
	v_min_f32_e32 v114, v120, v121
	v_pk_fma_f32 v[122:123], v[120:121], v[122:123], 0.5 op_sel_hi:[1,1,0]
	v_cmp_ge_f32_e32 vcc, s66, v114
	v_pk_fma_f32 v[122:123], v[120:121], v[122:123], 1.0 op_sel_hi:[1,1,0]
	s_nop 0
	v_pk_mul_f32 v[122:123], v[122:123], v[120:121] neg_lo:[0,1] neg_hi:[0,1]
	s_and_saveexec_b64 s[52:53], vcc
	s_cbranch_execnz .LBB0_1315
.LBB0_1270:
	s_or_b64 exec, exec, s[52:53]
	v_sqrt_f32_e32 v120, v122
	v_sqrt_f32_e32 v121, v123
	v_pk_mul_f32 v[116:117], v[116:117], v[118:119]
	v_pk_add_f32 v[106:107], v[74:75], v[106:107]
	v_pk_add_f32 v[102:103], v[70:71], v[102:103]
	v_lshlrev_b32_e32 v114, 16, v115
	v_and_b32_e32 v115, 0xffff0000, v115
	v_pk_mul_f32 v[116:117], v[116:117], v[120:121]
	v_pk_mul_f32 v[106:107], v[106:107], s[44:45] op_sel_hi:[1,0]
	v_pk_mul_f32 v[102:103], v[102:103], s[44:45] op_sel_hi:[1,0]
	v_pk_mul_f32 v[114:115], v[116:117], v[114:115]
	v_exp_f32_e32 v106, v106
	v_exp_f32_e32 v107, v107
	v_exp_f32_e32 v116, v102
	v_exp_f32_e32 v117, v103
	v_cvt_pk_bf16_f32 v112, v112, v114
	v_cvt_pk_bf16_f32 v113, v113, v115
	ds_write_b128 v236, v[110:113] offset:7296
	v_pk_add_f32 v[102:103], v[106:107], 1.0 op_sel_hi:[1,0]
	v_pk_add_f32 v[110:111], v[116:117], 1.0 op_sel_hi:[1,0]
	s_nop 0
	v_pk_mul_f32 v[106:107], v[102:103], v[110:111]
	s_nop 0
	v_rcp_f32_e32 v112, v106
	v_rcp_f32_e32 v113, v107
	v_add_u32_e32 v106, v245, v199
	v_add_u32_e32 v118, v106, v198
	ds_read_b64 v[106:107], v118
	v_pk_mul_f32 v[110:111], v[110:111], v[112:113]
	s_waitcnt vmcnt(16)
	v_pk_mul_f32 v[110:111], v[66:67], v[110:111]
	s_nop 0
	v_pk_mul_f32 v[116:117], v[110:111], s[98:99] op_sel_hi:[1,0]
	s_nop 0
	v_pk_fma_f32 v[114:115], v[116:117], s[46:47], v[164:165] op_sel_hi:[1,0,0]
	v_min_f32_e32 v119, v116, v117
	v_pk_fma_f32 v[114:115], v[116:117], v[114:115], 0.5 op_sel_hi:[1,1,0]
	v_cmp_ge_f32_e32 vcc, s66, v119
	v_pk_fma_f32 v[114:115], v[116:117], v[114:115], 1.0 op_sel_hi:[1,1,0]
	s_nop 0
	v_pk_mul_f32 v[114:115], v[114:115], v[116:117] neg_lo:[0,1] neg_hi:[0,1]
	s_and_saveexec_b64 s[52:53], vcc
	s_cbranch_execnz .LBB0_1316
.LBB0_1271:
	s_or_b64 exec, exec, s[52:53]
	v_pk_add_f32 v[108:109], v[76:77], v[108:109]
	v_pk_add_f32 v[104:105], v[72:73], v[104:105]
	v_pk_mul_f32 v[108:109], v[108:109], s[44:45] op_sel_hi:[1,0]
	v_pk_mul_f32 v[104:105], v[104:105], s[44:45] op_sel_hi:[1,0]
	v_exp_f32_e32 v108, v108
	v_exp_f32_e32 v109, v109
	v_exp_f32_e32 v104, v104
	v_exp_f32_e32 v105, v105
	v_pk_mul_f32 v[102:103], v[102:103], v[112:113]
	v_pk_add_f32 v[108:109], v[108:109], 1.0 op_sel_hi:[1,0]
	v_sqrt_f32_e32 v114, v114
	v_pk_add_f32 v[104:105], v[104:105], 1.0 op_sel_hi:[1,0]
	v_sqrt_f32_e32 v115, v115
	v_pk_mul_f32 v[112:113], v[108:109], v[104:105]
	s_waitcnt lgkmcnt(0)
	v_lshlrev_b32_e32 v116, 16, v106
	v_rcp_f32_e32 v112, v112
	v_rcp_f32_e32 v113, v113
	v_and_b32_e32 v117, 0xffff0000, v106
	v_pk_mul_f32 v[102:103], v[102:103], v[114:115]
	v_pk_mul_f32 v[104:105], v[104:105], v[112:113]
	s_nop 0
	v_pk_mul_f32 v[104:105], v[68:69], v[104:105]
	v_pk_mul_f32 v[102:103], v[102:103], v[116:117]
	v_pk_mul_f32 v[114:115], v[104:105], s[98:99] op_sel_hi:[1,0]
	v_cvt_pk_bf16_f32 v102, v110, v102
	v_cvt_pk_bf16_f32 v103, v111, v103
	s_nop 0
	v_pk_fma_f32 v[110:111], v[114:115], s[46:47], v[164:165] op_sel_hi:[1,0,0]
	v_min_f32_e32 v106, v114, v115
	v_pk_fma_f32 v[110:111], v[114:115], v[110:111], 0.5 op_sel_hi:[1,1,0]
	v_cmp_ge_f32_e32 vcc, s66, v106
	v_pk_fma_f32 v[110:111], v[114:115], v[110:111], 1.0 op_sel_hi:[1,1,0]
	s_nop 0
	v_pk_mul_f32 v[110:111], v[110:111], v[114:115] neg_lo:[0,1] neg_hi:[0,1]
	s_and_saveexec_b64 s[52:53], vcc
	s_cbranch_execnz .LBB0_1317
.LBB0_1272:
	s_or_b64 exec, exec, s[52:53]
	v_sqrt_f32_e32 v110, v110
	v_sqrt_f32_e32 v111, v111
	v_pk_add_f32 v[98:99], v[74:75], v[98:99]
	v_pk_add_f32 v[94:95], v[70:71], v[94:95]
	v_pk_mul_f32 v[108:109], v[108:109], v[112:113]
	v_pk_mul_f32 v[98:99], v[98:99], s[44:45] op_sel_hi:[1,0]
	v_pk_mul_f32 v[94:95], v[94:95], s[44:45] op_sel_hi:[1,0]
	v_pk_mul_f32 v[108:109], v[108:109], v[110:111]
	v_exp_f32_e32 v98, v98
	v_exp_f32_e32 v99, v99
	v_exp_f32_e32 v110, v94
	v_exp_f32_e32 v111, v95
	v_lshlrev_b32_e32 v106, 16, v107
	v_pk_add_f32 v[94:95], v[98:99], 1.0 op_sel_hi:[1,0]
	v_and_b32_e32 v107, 0xffff0000, v107
	v_pk_add_f32 v[110:111], v[110:111], 1.0 op_sel_hi:[1,0]
	v_pk_mul_f32 v[108:109], v[108:109], v[106:107]
	v_pk_mul_f32 v[98:99], v[94:95], v[110:111]
	v_cvt_pk_bf16_f32 v104, v104, v108
	v_cvt_pk_bf16_f32 v105, v105, v109
	ds_write_b128 v236, v[102:105] offset:64
	v_rcp_f32_e32 v106, v98
	v_rcp_f32_e32 v107, v99
	ds_read_b64 v[98:99], v118 offset:4096
	v_pk_mul_f32 v[102:103], v[110:111], v[106:107]
	s_nop 0
	v_pk_mul_f32 v[102:103], v[66:67], v[102:103]
	s_nop 0
	v_pk_mul_f32 v[108:109], v[102:103], s[98:99] op_sel_hi:[1,0]
	s_nop 0
	v_pk_fma_f32 v[104:105], v[108:109], s[46:47], v[164:165] op_sel_hi:[1,0,0]
	v_min_f32_e32 v110, v108, v109
	v_pk_fma_f32 v[104:105], v[108:109], v[104:105], 0.5 op_sel_hi:[1,1,0]
	v_cmp_ge_f32_e32 vcc, s66, v110
	v_pk_fma_f32 v[104:105], v[108:109], v[104:105], 1.0 op_sel_hi:[1,1,0]
	s_nop 0
	v_pk_mul_f32 v[104:105], v[104:105], v[108:109] neg_lo:[0,1] neg_hi:[0,1]
	s_and_saveexec_b64 s[52:53], vcc
	s_cbranch_execnz .LBB0_1318
.LBB0_1273:
	s_or_b64 exec, exec, s[52:53]
	v_pk_add_f32 v[100:101], v[76:77], v[100:101]
	v_pk_add_f32 v[96:97], v[72:73], v[96:97]
	v_pk_mul_f32 v[100:101], v[100:101], s[44:45] op_sel_hi:[1,0]
	v_pk_mul_f32 v[96:97], v[96:97], s[44:45] op_sel_hi:[1,0]
	v_exp_f32_e32 v100, v100
	v_exp_f32_e32 v101, v101
	v_exp_f32_e32 v96, v96
	v_exp_f32_e32 v97, v97
	v_sqrt_f32_e32 v104, v104
	v_sqrt_f32_e32 v105, v105
	v_pk_mul_f32 v[94:95], v[94:95], v[106:107]
	v_pk_add_f32 v[100:101], v[100:101], 1.0 op_sel_hi:[1,0]
	v_pk_add_f32 v[96:97], v[96:97], 1.0 op_sel_hi:[1,0]
	v_pk_mul_f32 v[94:95], v[94:95], v[104:105]
	v_pk_mul_f32 v[104:105], v[100:101], v[96:97]
	s_waitcnt lgkmcnt(0)
	v_lshlrev_b32_e32 v108, 16, v98
	v_rcp_f32_e32 v104, v104
	v_rcp_f32_e32 v105, v105
	v_and_b32_e32 v109, 0xffff0000, v98
	v_pk_mul_f32 v[94:95], v[94:95], v[108:109]
	v_pk_mul_f32 v[96:97], v[96:97], v[104:105]
	s_nop 0
	v_pk_mul_f32 v[96:97], v[68:69], v[96:97]
	v_cvt_pk_bf16_f32 v94, v102, v94
	v_cvt_pk_bf16_f32 v95, v103, v95
	s_nop 0
	v_pk_mul_f32 v[102:103], v[96:97], s[98:99] op_sel_hi:[1,0]
	s_nop 0
	v_pk_fma_f32 v[106:107], v[102:103], s[46:47], v[164:165] op_sel_hi:[1,0,0]
	v_min_f32_e32 v98, v102, v103
	v_pk_fma_f32 v[106:107], v[102:103], v[106:107], 0.5 op_sel_hi:[1,1,0]
	v_cmp_ge_f32_e32 vcc, s66, v98
	v_pk_fma_f32 v[106:107], v[102:103], v[106:107], 1.0 op_sel_hi:[1,1,0]
	s_nop 0
	v_pk_mul_f32 v[106:107], v[106:107], v[102:103] neg_lo:[0,1] neg_hi:[0,1]
	s_and_saveexec_b64 s[52:53], vcc
	s_cbranch_execnz .LBB0_1319
.LBB0_1274:
	s_or_b64 exec, exec, s[52:53]
	v_sqrt_f32_e32 v102, v106
	v_sqrt_f32_e32 v103, v107
	v_pk_add_f32 v[90:91], v[74:75], v[90:91]
	v_pk_add_f32 v[86:87], v[70:71], v[86:87]
	v_pk_mul_f32 v[100:101], v[100:101], v[104:105]
	v_pk_mul_f32 v[90:91], v[90:91], s[44:45] op_sel_hi:[1,0]
	v_pk_mul_f32 v[86:87], v[86:87], s[44:45] op_sel_hi:[1,0]
	v_pk_mul_f32 v[100:101], v[100:101], v[102:103]
	v_exp_f32_e32 v90, v90
	v_exp_f32_e32 v91, v91
	v_exp_f32_e32 v102, v86
	v_exp_f32_e32 v103, v87
	v_lshlrev_b32_e32 v98, 16, v99
	v_pk_add_f32 v[86:87], v[90:91], 1.0 op_sel_hi:[1,0]
	v_and_b32_e32 v99, 0xffff0000, v99
	v_pk_add_f32 v[102:103], v[102:103], 1.0 op_sel_hi:[1,0]
	v_pk_mul_f32 v[100:101], v[100:101], v[98:99]
	v_pk_mul_f32 v[90:91], v[86:87], v[102:103]
	v_cvt_pk_bf16_f32 v96, v96, v100
	v_cvt_pk_bf16_f32 v97, v97, v101
	ds_write_b128 v236, v[94:97] offset:2496
	v_rcp_f32_e32 v98, v90
	v_rcp_f32_e32 v99, v91
	ds_read_b64 v[90:91], v118 offset:8192
	v_pk_mul_f32 v[94:95], v[102:103], v[98:99]
	s_nop 0
	v_pk_mul_f32 v[94:95], v[66:67], v[94:95]
	s_nop 0
	v_pk_mul_f32 v[100:101], v[94:95], s[98:99] op_sel_hi:[1,0]
	s_nop 0
	v_pk_fma_f32 v[96:97], v[100:101], s[46:47], v[164:165] op_sel_hi:[1,0,0]
	v_min_f32_e32 v102, v100, v101
	v_pk_fma_f32 v[96:97], v[100:101], v[96:97], 0.5 op_sel_hi:[1,1,0]
	v_cmp_ge_f32_e32 vcc, s66, v102
	v_pk_fma_f32 v[96:97], v[100:101], v[96:97], 1.0 op_sel_hi:[1,1,0]
	s_nop 0
	v_pk_mul_f32 v[96:97], v[96:97], v[100:101] neg_lo:[0,1] neg_hi:[0,1]
	s_and_saveexec_b64 s[52:53], vcc
	s_cbranch_execnz .LBB0_1320
.LBB0_1275:
	s_or_b64 exec, exec, s[52:53]
	v_pk_add_f32 v[92:93], v[76:77], v[92:93]
	v_pk_add_f32 v[88:89], v[72:73], v[88:89]
	v_pk_mul_f32 v[92:93], v[92:93], s[44:45] op_sel_hi:[1,0]
	v_pk_mul_f32 v[88:89], v[88:89], s[44:45] op_sel_hi:[1,0]
	v_exp_f32_e32 v92, v92
	v_exp_f32_e32 v93, v93
	v_exp_f32_e32 v88, v88
	v_exp_f32_e32 v89, v89
	v_sqrt_f32_e32 v96, v96
	v_sqrt_f32_e32 v97, v97
	v_pk_mul_f32 v[86:87], v[86:87], v[98:99]
	v_pk_add_f32 v[92:93], v[92:93], 1.0 op_sel_hi:[1,0]
	v_pk_add_f32 v[88:89], v[88:89], 1.0 op_sel_hi:[1,0]
	v_pk_mul_f32 v[86:87], v[86:87], v[96:97]
	v_pk_mul_f32 v[96:97], v[92:93], v[88:89]
	s_waitcnt lgkmcnt(0)
	v_lshlrev_b32_e32 v100, 16, v90
	v_rcp_f32_e32 v96, v96
	v_rcp_f32_e32 v97, v97
	v_and_b32_e32 v101, 0xffff0000, v90
	v_pk_mul_f32 v[86:87], v[86:87], v[100:101]
	v_pk_mul_f32 v[88:89], v[88:89], v[96:97]
	s_nop 0
	v_pk_mul_f32 v[88:89], v[68:69], v[88:89]
	v_cvt_pk_bf16_f32 v86, v94, v86
	v_cvt_pk_bf16_f32 v87, v95, v87
	s_nop 0
	v_pk_mul_f32 v[94:95], v[88:89], s[98:99] op_sel_hi:[1,0]
	s_nop 0
	v_pk_fma_f32 v[98:99], v[94:95], s[46:47], v[164:165] op_sel_hi:[1,0,0]
	v_min_f32_e32 v90, v94, v95
	v_pk_fma_f32 v[98:99], v[94:95], v[98:99], 0.5 op_sel_hi:[1,1,0]
	v_cmp_ge_f32_e32 vcc, s66, v90
	v_pk_fma_f32 v[98:99], v[94:95], v[98:99], 1.0 op_sel_hi:[1,1,0]
	s_nop 0
	v_pk_mul_f32 v[98:99], v[98:99], v[94:95] neg_lo:[0,1] neg_hi:[0,1]
	s_and_saveexec_b64 s[52:53], vcc
	s_cbranch_execnz .LBB0_1321
.LBB0_1276:
	s_or_b64 exec, exec, s[52:53]
	v_pk_add_f32 v[74:75], v[74:75], v[78:79]
	v_pk_add_f32 v[70:71], v[70:71], v[82:83]
	v_sqrt_f32_e32 v94, v98
	v_sqrt_f32_e32 v95, v99
	v_pk_mul_f32 v[74:75], v[74:75], s[44:45] op_sel_hi:[1,0]
	v_pk_mul_f32 v[70:71], v[70:71], s[44:45] op_sel_hi:[1,0]
	v_exp_f32_e32 v74, v74
	v_exp_f32_e32 v75, v75
	v_exp_f32_e32 v70, v70
	v_exp_f32_e32 v71, v71
	v_pk_mul_f32 v[92:93], v[92:93], v[96:97]
	v_lshlrev_b32_e32 v90, 16, v91
	v_and_b32_e32 v91, 0xffff0000, v91
	v_pk_mul_f32 v[92:93], v[92:93], v[94:95]
	v_pk_add_f32 v[74:75], v[74:75], 1.0 op_sel_hi:[1,0]
	v_pk_mul_f32 v[82:83], v[92:93], v[90:91]
	v_pk_add_f32 v[90:91], v[70:71], 1.0 op_sel_hi:[1,0]
	v_cvt_pk_bf16_f32 v88, v88, v82
	v_cvt_pk_bf16_f32 v89, v89, v83
	ds_write_b128 v236, v[86:89] offset:4928
	v_pk_mul_f32 v[70:71], v[74:75], v[90:91]
	s_nop 0
	v_rcp_f32_e32 v78, v70
	v_rcp_f32_e32 v79, v71
	ds_read_b64 v[70:71], v118 offset:12288
	v_pk_mul_f32 v[82:83], v[90:91], v[78:79]
	s_nop 0
	v_pk_mul_f32 v[66:67], v[66:67], v[82:83]
	s_nop 0
	v_pk_mul_f32 v[86:87], v[66:67], s[98:99] op_sel_hi:[1,0]
	s_nop 0
	v_pk_fma_f32 v[82:83], v[86:87], s[46:47], v[164:165] op_sel_hi:[1,0,0]
	v_min_f32_e32 v88, v86, v87
	v_pk_fma_f32 v[82:83], v[86:87], v[82:83], 0.5 op_sel_hi:[1,1,0]
	v_cmp_ge_f32_e32 vcc, s66, v88
	v_pk_fma_f32 v[82:83], v[86:87], v[82:83], 1.0 op_sel_hi:[1,1,0]
	s_nop 0
	v_pk_mul_f32 v[82:83], v[82:83], v[86:87] neg_lo:[0,1] neg_hi:[0,1]
	s_and_saveexec_b64 s[52:53], vcc
	s_cbranch_execnz .LBB0_1322
.LBB0_1277:
	s_or_b64 exec, exec, s[52:53]
	v_pk_add_f32 v[76:77], v[76:77], v[80:81]
	v_pk_add_f32 v[72:73], v[72:73], v[84:85]
	v_pk_mul_f32 v[76:77], v[76:77], s[44:45] op_sel_hi:[1,0]
	v_pk_mul_f32 v[72:73], v[72:73], s[44:45] op_sel_hi:[1,0]
	v_sqrt_f32_e32 v82, v82
	v_sqrt_f32_e32 v83, v83
	v_exp_f32_e32 v76, v76
	v_exp_f32_e32 v77, v77
	v_exp_f32_e32 v84, v72
	v_exp_f32_e32 v85, v73
	v_pk_mul_f32 v[72:73], v[74:75], v[78:79]
	s_waitcnt lgkmcnt(0)
	v_lshlrev_b32_e32 v80, 16, v70
	v_pk_mul_f32 v[78:79], v[72:73], v[82:83]
	v_pk_add_f32 v[72:73], v[76:77], 1.0 op_sel_hi:[1,0]
	v_pk_add_f32 v[76:77], v[84:85], 1.0 op_sel_hi:[1,0]
	v_and_b32_e32 v81, 0xffff0000, v70
	v_pk_mul_f32 v[74:75], v[72:73], v[76:77]
	v_pk_mul_f32 v[78:79], v[78:79], v[80:81]
	v_rcp_f32_e32 v74, v74
	v_rcp_f32_e32 v75, v75
	v_cvt_pk_bf16_f32 v66, v66, v78
	v_cvt_pk_bf16_f32 v67, v67, v79
	s_nop 0
	v_pk_mul_f32 v[76:77], v[76:77], v[74:75]
	s_nop 0
	v_pk_mul_f32 v[68:69], v[68:69], v[76:77]
	s_nop 0
	v_pk_mul_f32 v[78:79], v[68:69], s[98:99] op_sel_hi:[1,0]
	s_nop 0
	v_pk_fma_f32 v[76:77], v[78:79], s[46:47], v[164:165] op_sel_hi:[1,0,0]
	v_min_f32_e32 v70, v78, v79
	v_pk_fma_f32 v[76:77], v[78:79], v[76:77], 0.5 op_sel_hi:[1,1,0]
	v_cmp_ge_f32_e32 vcc, s66, v70
	v_pk_fma_f32 v[76:77], v[78:79], v[76:77], 1.0 op_sel_hi:[1,1,0]
	s_nop 0
	v_pk_mul_f32 v[76:77], v[76:77], v[78:79] neg_lo:[0,1] neg_hi:[0,1]
	s_and_saveexec_b64 s[52:53], vcc
	s_cbranch_execnz .LBB0_1323
.LBB0_1278:
	s_or_b64 exec, exec, s[52:53]
	v_sqrt_f32_e32 v76, v76
	v_sqrt_f32_e32 v77, v77
	v_pk_mul_f32 v[72:73], v[72:73], v[74:75]
	v_lshlrev_b32_e32 v70, 16, v71
	v_and_b32_e32 v71, 0xffff0000, v71
	v_pk_mul_f32 v[72:73], v[72:73], v[76:77]
	s_lshl_b32 s81, s20, 1
	v_pk_mul_f32 v[70:71], v[72:73], v[70:71]
	s_ashr_i32 s49, s48, 31
	v_cvt_pk_bf16_f32 v68, v68, v70
	v_cvt_pk_bf16_f32 v69, v69, v71
	ds_write_b128 v236, v[66:69] offset:7360
	ds_read2_b64 v[66:69], v237 offset1:18
	s_add_i32 s81, s81, s30
	v_lshl_add_u64 v[94:95], s[48:49], 0, v[160:161]
	s_waitcnt lgkmcnt(0)
	v_lshlrev_b32_e32 v70, 16, v66
	v_lshlrev_b32_e32 v71, 16, v67
	v_add_f32_e32 v72, 0, v70
	v_add_f32_e32 v73, 0, v71
	v_exp_f32_e32 v70, v70
	v_exp_f32_e32 v71, v71
	v_and_b32_e32 v66, 0xffff0000, v66
	v_fmac_f32_e32 v66, 0, v70
	v_and_b32_e32 v67, 0xffff0000, v67
	v_lshlrev_b32_e32 v70, 16, v68
	v_fmac_f32_e32 v67, 0, v71
	v_lshlrev_b32_e32 v71, 16, v69
	v_add_f32_e32 v74, v72, v70
	v_exp_f32_e32 v76, v70
	v_add_f32_e32 v75, v73, v71
	v_exp_f32_e32 v77, v71
	ds_read2_b64 v[70:73], v237 offset0:36 offset1:54
	v_and_b32_e32 v68, 0xffff0000, v68
	v_fmac_f32_e32 v68, v76, v66
	v_and_b32_e32 v66, 0xffff0000, v69
	v_fmac_f32_e32 v66, v77, v67
	s_waitcnt lgkmcnt(0)
	v_lshlrev_b32_e32 v69, 16, v71
	v_lshlrev_b32_e32 v67, 16, v70
	v_add_f32_e32 v75, v75, v69
	v_add_f32_e32 v74, v74, v67
	v_exp_f32_e32 v69, v69
	v_exp_f32_e32 v67, v67
	v_and_b32_e32 v71, 0xffff0000, v71
	v_and_b32_e32 v70, 0xffff0000, v70
	v_fmac_f32_e32 v71, v69, v66
	v_lshlrev_b32_e32 v66, 16, v72
	v_fmac_f32_e32 v70, v67, v68
	v_lshlrev_b32_e32 v67, 16, v73
	v_add_f32_e32 v74, v74, v66
	v_exp_f32_e32 v76, v66
	v_add_f32_e32 v75, v75, v67
	v_exp_f32_e32 v77, v67
	ds_read2_b64 v[66:69], v237 offset0:72 offset1:90
	v_and_b32_e32 v72, 0xffff0000, v72
	v_fmac_f32_e32 v72, v76, v70
	v_and_b32_e32 v70, 0xffff0000, v73
	v_fmac_f32_e32 v70, v77, v71
	s_waitcnt lgkmcnt(0)
	v_lshlrev_b32_e32 v73, 16, v67
	v_lshlrev_b32_e32 v71, 16, v66
	v_add_f32_e32 v75, v75, v73
	v_add_f32_e32 v74, v74, v71
	v_exp_f32_e32 v73, v73
	v_exp_f32_e32 v71, v71
	v_and_b32_e32 v67, 0xffff0000, v67
	v_and_b32_e32 v66, 0xffff0000, v66
	v_fmac_f32_e32 v67, v73, v70
	v_lshlrev_b32_e32 v70, 16, v68
	v_fmac_f32_e32 v66, v71, v72
	v_lshlrev_b32_e32 v71, 16, v69
	v_add_f32_e32 v74, v74, v70
	v_exp_f32_e32 v76, v70
	v_add_f32_e32 v75, v75, v71
	v_exp_f32_e32 v77, v71
	ds_read2_b64 v[70:73], v237 offset0:108 offset1:126
	v_and_b32_e32 v68, 0xffff0000, v68
	v_fmac_f32_e32 v68, v76, v66
	v_and_b32_e32 v66, 0xffff0000, v69
	v_fmac_f32_e32 v66, v77, v67
	s_waitcnt lgkmcnt(0)
	v_lshlrev_b32_e32 v69, 16, v71
	v_lshlrev_b32_e32 v67, 16, v70
	v_add_f32_e32 v75, v75, v69
	v_add_f32_e32 v74, v74, v67
	v_exp_f32_e32 v69, v69
	v_exp_f32_e32 v67, v67
	v_and_b32_e32 v71, 0xffff0000, v71
	v_and_b32_e32 v70, 0xffff0000, v70
	v_fmac_f32_e32 v71, v69, v66
	v_lshlrev_b32_e32 v66, 16, v72
	v_fmac_f32_e32 v70, v67, v68
	v_lshlrev_b32_e32 v67, 16, v73
	v_add_f32_e32 v74, v74, v66
	v_exp_f32_e32 v76, v66
	v_add_f32_e32 v75, v75, v67
	v_exp_f32_e32 v77, v67
	ds_read2_b64 v[66:69], v237 offset0:144 offset1:162
	v_and_b32_e32 v72, 0xffff0000, v72
	v_fmac_f32_e32 v72, v76, v70
	v_and_b32_e32 v70, 0xffff0000, v73
	v_fmac_f32_e32 v70, v77, v71
	s_waitcnt lgkmcnt(0)
	v_lshlrev_b32_e32 v73, 16, v67
	v_lshlrev_b32_e32 v71, 16, v66
	v_add_f32_e32 v75, v75, v73
	v_add_f32_e32 v74, v74, v71
	v_exp_f32_e32 v73, v73
	v_exp_f32_e32 v71, v71
	v_and_b32_e32 v67, 0xffff0000, v67
	v_and_b32_e32 v66, 0xffff0000, v66
	v_fmac_f32_e32 v67, v73, v70
	v_lshlrev_b32_e32 v70, 16, v68
	v_fmac_f32_e32 v66, v71, v72
	v_lshlrev_b32_e32 v71, 16, v69
	v_add_f32_e32 v74, v74, v70
	v_exp_f32_e32 v76, v70
	v_add_f32_e32 v75, v75, v71
	v_exp_f32_e32 v77, v71
	ds_read2_b64 v[70:73], v237 offset0:180 offset1:198
	v_and_b32_e32 v68, 0xffff0000, v68
	v_fmac_f32_e32 v68, v76, v66
	v_and_b32_e32 v66, 0xffff0000, v69
	v_fmac_f32_e32 v66, v77, v67
	s_waitcnt lgkmcnt(0)
	v_lshlrev_b32_e32 v69, 16, v71
	v_lshlrev_b32_e32 v67, 16, v70
	v_add_f32_e32 v75, v75, v69
	v_add_f32_e32 v74, v74, v67
	v_exp_f32_e32 v69, v69
	v_exp_f32_e32 v67, v67
	v_and_b32_e32 v71, 0xffff0000, v71
	v_and_b32_e32 v70, 0xffff0000, v70
	v_fmac_f32_e32 v71, v69, v66
	v_lshlrev_b32_e32 v66, 16, v72
	v_fmac_f32_e32 v70, v67, v68
	v_lshlrev_b32_e32 v67, 16, v73
	v_add_f32_e32 v74, v74, v66
	v_exp_f32_e32 v76, v66
	v_add_f32_e32 v75, v75, v67
	v_exp_f32_e32 v77, v67
	ds_read2_b64 v[66:69], v237 offset0:216 offset1:234
	v_and_b32_e32 v72, 0xffff0000, v72
	v_fmac_f32_e32 v72, v76, v70
	v_and_b32_e32 v70, 0xffff0000, v73
	v_fmac_f32_e32 v70, v77, v71
	s_waitcnt lgkmcnt(0)
	v_lshlrev_b32_e32 v71, 16, v66
	v_lshlrev_b32_e32 v73, 16, v67
	v_add_f32_e32 v74, v74, v71
	v_add_f32_e32 v75, v75, v73
	v_exp_f32_e32 v71, v71
	v_exp_f32_e32 v73, v73
	v_and_b32_e32 v76, 0xffff0000, v66
	v_fmac_f32_e32 v76, v71, v72
	v_and_b32_e32 v71, 0xffff0000, v67
	v_lshlrev_b32_e32 v66, 16, v68
	v_fmac_f32_e32 v71, v73, v70
	v_lshlrev_b32_e32 v67, 16, v69
	v_add_f32_e32 v70, v74, v66
	v_exp_f32_e32 v73, v66
	v_add_f32_e32 v72, v75, v67
	v_and_b32_e32 v74, 0xffff0000, v68
	v_exp_f32_e32 v68, v67
	ds_read_b64 v[66:67], v237 offset:2016
	v_fmac_f32_e32 v74, v73, v76
	v_and_b32_e32 v73, 0xffff0000, v69
	v_fmac_f32_e32 v73, v68, v71
	ds_read_b64 v[68:69], v238
	s_waitcnt lgkmcnt(1)
	v_lshlrev_b32_e32 v71, 16, v66
	v_add_f32_e32 v70, v70, v71
	v_exp_f32_e32 v71, v71
	v_lshlrev_b32_e32 v75, 16, v67
	v_and_b32_e32 v66, 0xffff0000, v66
	v_add_f32_e32 v72, v72, v75
	v_fmac_f32_e32 v66, v71, v74
	s_waitcnt lgkmcnt(0)
	v_lshlrev_b32_e32 v71, 16, v68
	v_exp_f32_e32 v75, v75
	v_exp_f32_e32 v74, v71
	v_and_b32_e32 v67, 0xffff0000, v67
	v_fmac_f32_e32 v67, v75, v73
	v_lshlrev_b32_e32 v73, 16, v69
	v_add_f32_e32 v70, v70, v71
	v_and_b32_e32 v80, 0xffff0000, v68
	v_add_f32_e32 v71, v72, v73
	v_fmac_f32_e32 v80, v74, v66
	v_exp_f32_e32 v66, v73
	v_exp_f32_e32 v78, v70
	v_exp_f32_e32 v79, v71
	v_and_b32_e32 v81, 0xffff0000, v69
	v_fmac_f32_e32 v81, v66, v67
	ds_bpermute_b32 v66, v239, v78
	ds_bpermute_b32 v67, v239, v79
	ds_bpermute_b32 v68, v239, v80
	ds_bpermute_b32 v69, v239, v81
	ds_bpermute_b32 v70, v239, v78 offset:64
	ds_bpermute_b32 v71, v239, v79 offset:64
	ds_bpermute_b32 v72, v239, v80 offset:64
	ds_bpermute_b32 v73, v239, v81 offset:64
	ds_bpermute_b32 v74, v239, v78 offset:128
	ds_bpermute_b32 v75, v239, v79 offset:128
	ds_bpermute_b32 v76, v239, v80 offset:128
	ds_bpermute_b32 v77, v239, v81 offset:128
	ds_bpermute_b32 v78, v239, v78 offset:192
	ds_bpermute_b32 v79, v239, v79 offset:192
	ds_bpermute_b32 v80, v239, v80 offset:192
	ds_bpermute_b32 v81, v239, v81 offset:192
	s_and_saveexec_b64 s[48:49], s[0:1]
	s_cbranch_execz .LBB0_1280
	s_waitcnt lgkmcnt(10)
	v_pk_mul_f32 v[82:83], v[66:67], v[70:71]
	v_pk_fma_f32 v[66:67], v[66:67], 0, v[68:69] op_sel_hi:[1,0,1]
	v_mad_i64_i32 v[68:69], s[52:53], s81, v240, v[94:95]
	s_waitcnt lgkmcnt(8)
	v_pk_fma_f32 v[66:67], v[66:67], v[70:71], v[72:73]
	s_waitcnt lgkmcnt(6)
	v_pk_mul_f32 v[82:83], v[82:83], v[74:75]
	s_waitcnt lgkmcnt(4)
	v_pk_fma_f32 v[66:67], v[66:67], v[74:75], v[76:77]
	v_lshlrev_b64 v[68:69], 2, v[68:69]
	s_waitcnt lgkmcnt(2)
	v_pk_mul_f32 v[82:83], v[82:83], v[78:79]
	s_waitcnt lgkmcnt(0)
	v_pk_fma_f32 v[66:67], v[66:67], v[78:79], v[80:81]
	v_lshl_add_u64 v[70:71], s[8:9], 0, v[68:69]
	v_lshl_add_u64 v[68:69], s[10:11], 0, v[68:69]
	global_store_dwordx2 v[70:71], v[82:83], off
	global_store_dwordx2 v[68:69], v[66:67], off

.LBB0_1282:
	s_waitcnt lgkmcnt(12)
	ds_read_b128 v[66:69], v242
	s_waitcnt lgkmcnt(9)
	ds_read_b128 v[70:73], v242 offset:4096
	ds_read_b128 v[100:103], v242 offset:8192
	ds_read_b128 v[104:107], v242 offset:12288
	s_waitcnt vmcnt(15) lgkmcnt(3)
	v_mfma_f32_16x16x32_bf16 v[74:77], v[46:49], v[66:69], 0
	s_waitcnt vmcnt(9)
	v_mfma_f32_16x16x32_bf16 v[78:81], v[54:57], v[66:69], 0
	s_waitcnt vmcnt(8)
	v_mfma_f32_16x16x32_bf16 v[82:85], v[58:61], v[66:69], 0
	s_waitcnt vmcnt(3)
	v_mfma_f32_16x16x32_bf16 v[66:69], v[62:65], v[66:69], 0
	s_waitcnt lgkmcnt(2)
	v_mfma_f32_16x16x32_bf16 v[86:89], v[46:49], v[70:73], 0
	v_mfma_f32_16x16x32_bf16 v[90:93], v[54:57], v[70:73], 0
	v_mfma_f32_16x16x32_bf16 v[96:99], v[58:61], v[70:73], 0
	v_mfma_f32_16x16x32_bf16 v[70:73], v[62:65], v[70:73], 0
	s_waitcnt lgkmcnt(1)
	v_mfma_f32_16x16x32_bf16 v[108:111], v[46:49], v[100:103], 0
	v_mfma_f32_16x16x32_bf16 v[112:115], v[54:57], v[100:103], 0
	v_mfma_f32_16x16x32_bf16 v[120:123], v[58:61], v[100:103], 0
	v_mfma_f32_16x16x32_bf16 v[100:103], v[62:65], v[100:103], 0
	s_waitcnt lgkmcnt(0)
	v_mfma_f32_16x16x32_bf16 v[46:49], v[46:49], v[104:107], 0
	v_mfma_f32_16x16x32_bf16 v[54:57], v[54:57], v[104:107], 0
	v_mfma_f32_16x16x32_bf16 v[58:61], v[58:61], v[104:107], 0
	v_mfma_f32_16x16x32_bf16 v[62:65], v[62:65], v[104:107], 0
	ds_read_b128 v[104:107], v243
	ds_read_b128 v[124:127], v243 offset:4096
	s_waitcnt lgkmcnt(1)
	v_mfma_f32_16x16x32_bf16 v[74:77], v[30:33], v[104:107], v[74:77]
	v_mfma_f32_16x16x32_bf16 v[78:81], v[38:41], v[104:107], v[78:81]
	v_mfma_f32_16x16x32_bf16 v[82:85], v[42:45], v[104:107], v[82:85]
	s_waitcnt vmcnt(2)
	v_mfma_f32_16x16x32_bf16 v[66:69], v[50:53], v[104:107], v[66:69]
	s_waitcnt lgkmcnt(0)
	v_mfma_f32_16x16x32_bf16 v[86:89], v[30:33], v[124:127], v[86:89]
	v_mfma_f32_16x16x32_bf16 v[90:93], v[38:41], v[124:127], v[90:93]
	v_mfma_f32_16x16x32_bf16 v[96:99], v[42:45], v[124:127], v[96:99]
	v_mfma_f32_16x16x32_bf16 v[70:73], v[50:53], v[124:127], v[70:73]
	ds_read_b128 v[104:107], v243 offset:8192
	ds_read_b128 v[124:127], v243 offset:12288
	s_waitcnt lgkmcnt(1)
	v_mfma_f32_16x16x32_bf16 v[108:111], v[30:33], v[104:107], v[108:111]
	v_mfma_f32_16x16x32_bf16 v[112:115], v[38:41], v[104:107], v[112:115]
	v_mfma_f32_16x16x32_bf16 v[100:103], v[50:53], v[104:107], v[100:103]
	s_waitcnt lgkmcnt(0)
	v_mfma_f32_16x16x32_bf16 v[30:33], v[30:33], v[124:127], v[46:49]
	v_mfma_f32_16x16x32_bf16 v[38:41], v[38:41], v[124:127], v[54:57]
	v_mfma_f32_16x16x32_bf16 v[46:49], v[50:53], v[124:127], v[62:65]
	ds_read_b128 v[50:53], v244
	s_nop 0
	ds_read_b128 v[54:57], v244 offset:4096
	v_mfma_f32_16x16x32_bf16 v[120:123], v[42:45], v[104:107], v[120:123]
	v_mfma_f32_16x16x32_bf16 v[42:45], v[42:45], v[124:127], v[58:61]
	s_waitcnt lgkmcnt(1)
	v_mfma_f32_16x16x32_bf16 v[58:61], v[18:21], v[50:53], v[74:77]
	v_mfma_f32_16x16x32_bf16 v[62:65], v[22:25], v[50:53], v[78:81]
	v_mfma_f32_16x16x32_bf16 v[74:77], v[26:29], v[50:53], v[82:85]
	s_waitcnt vmcnt(1)
	v_mfma_f32_16x16x32_bf16 v[66:69], v[34:37], v[50:53], v[66:69]
	s_waitcnt lgkmcnt(0)
	v_mfma_f32_16x16x32_bf16 v[78:81], v[18:21], v[54:57], v[86:89]
	v_mfma_f32_16x16x32_bf16 v[104:107], v[22:25], v[54:57], v[90:93]
	v_mfma_f32_16x16x32_bf16 v[96:99], v[26:29], v[54:57], v[96:99]
	v_mfma_f32_16x16x32_bf16 v[70:73], v[34:37], v[54:57], v[70:73]
	ds_read_b128 v[50:53], v244 offset:8192
	ds_read_b128 v[54:57], v244 offset:12288
	s_waitcnt lgkmcnt(1)
	v_mfma_f32_16x16x32_bf16 v[108:111], v[18:21], v[50:53], v[108:111]
	s_waitcnt lgkmcnt(0)
	v_mfma_f32_16x16x32_bf16 v[124:127], v[18:21], v[54:57], v[30:33]
	ds_read_b128 v[18:21], v241
	s_nop 1
	ds_read_b128 v[30:33], v241 offset:4096
	v_mfma_f32_16x16x32_bf16 v[112:115], v[22:25], v[50:53], v[112:115]
	v_mfma_f32_16x16x32_bf16 v[128:131], v[22:25], v[54:57], v[38:41]
	v_add_co_u32_e32 v22, vcc, 0x1000, v174
	s_nop 1
	v_addc_co_u32_e32 v23, vcc, 0, v175, vcc
	v_add_co_u32_e32 v24, vcc, 0x1000, v172
	s_waitcnt lgkmcnt(1)
	v_mfma_f32_16x16x32_bf16 v[90:93], v[2:5], v[18:21], v[58:61]
	v_addc_co_u32_e32 v25, vcc, 0, v173, vcc
	v_mfma_f32_16x16x32_bf16 v[86:89], v[14:17], v[18:21], v[62:65]
	s_nop 0
	global_load_dwordx4 v[58:61], v[22:23], off offset:1024
	s_nop 0
	global_load_dwordx4 v[62:65], v[24:25], off offset:1024
	v_mfma_f32_16x16x32_bf16 v[120:123], v[26:29], v[50:53], v[120:123]
	v_mfma_f32_16x16x32_bf16 v[100:103], v[34:37], v[50:53], v[100:103]
	v_mfma_f32_16x16x32_bf16 v[136:139], v[34:37], v[54:57], v[46:49]
	v_mfma_f32_16x16x32_bf16 v[50:53], v[6:9], v[18:21], v[74:77]
	s_waitcnt vmcnt(2)
	v_mfma_f32_16x16x32_bf16 v[46:49], v[10:13], v[18:21], v[66:69]
	v_add_co_u32_e32 v18, vcc, 0x1000, v168
	s_nop 1
	v_addc_co_u32_e32 v19, vcc, 0, v169, vcc
	v_mfma_f32_16x16x32_bf16 v[132:135], v[26:29], v[54:57], v[42:45]
	global_load_dwordx4 v[54:57], v[18:19], off offset:1024
	global_load_dwordx4 v[26:29], v[22:23], off offset:1088
	s_nop 0
	global_load_dwordx4 v[22:25], v[24:25], off offset:1088
	s_nop 0
	global_load_dwordx4 v[18:21], v[18:19], off offset:1088
	s_waitcnt lgkmcnt(0)
	v_mfma_f32_16x16x32_bf16 v[82:85], v[2:5], v[30:33], v[78:81]
	v_mfma_f32_16x16x32_bf16 v[78:81], v[14:17], v[30:33], v[104:107]
	ds_read_b128 v[34:37], v241 offset:8192
	s_nop 1
	ds_read_b128 v[104:107], v241 offset:12288
	v_mfma_f32_16x16x32_bf16 v[42:45], v[6:9], v[30:33], v[96:99]
	v_mfma_f32_16x16x32_bf16 v[38:41], v[10:13], v[30:33], v[70:73]
	s_waitcnt vmcnt(5)
	v_pk_add_f32 v[30:31], v[58:59], v[90:91]
	s_nop 0
	v_pk_mul_f32 v[30:31], v[30:31], s[44:45] op_sel_hi:[1,0]
	s_waitcnt lgkmcnt(1)
	v_mfma_f32_16x16x32_bf16 v[70:73], v[2:5], v[34:37], v[108:111]
	s_waitcnt vmcnt(4)
	v_pk_add_f32 v[32:33], v[62:63], v[86:87]
	v_exp_f32_e32 v68, v30
	v_pk_mul_f32 v[66:67], v[32:33], s[44:45] op_sel_hi:[1,0]
	v_exp_f32_e32 v69, v31
	v_exp_f32_e32 v66, v66
	v_exp_f32_e32 v67, v67
	v_mfma_f32_16x16x32_bf16 v[74:77], v[14:17], v[34:37], v[112:115]
	v_add_f32_e64 v90, v68, 1.0
	v_add_f32_e64 v91, v69, 1.0
	ds_read_b64 v[86:87], v154
	v_pk_add_f32 v[96:97], v[66:67], 1.0 op_sel_hi:[1,0]
	v_mfma_f32_16x16x32_bf16 v[30:33], v[6:9], v[34:37], v[120:123]
	v_mul_f32_e64 v66, v90, v96
	v_mul_f32_e64 v67, v91, v97
	v_rcp_f32_e32 v98, v66
	v_rcp_f32_e32 v99, v67
	s_waitcnt lgkmcnt(1)
	v_mfma_f32_16x16x32_bf16 v[66:69], v[2:5], v[104:107], v[124:127]
	v_mul_f32_e64 v2, v96, v98
	v_mul_f32_e64 v3, v97, v99
	v_mfma_f32_16x16x32_bf16 v[34:37], v[10:13], v[34:37], v[100:103]
	s_waitcnt vmcnt(3)
	v_pk_mul_f32 v[96:97], v[54:55], v[2:3]
	s_nop 0
	v_pk_mul_f32 v[102:103], v[96:97], s[98:99] op_sel_hi:[1,0]
	v_mfma_f32_16x16x32_bf16 v[14:17], v[14:17], v[104:107], v[128:131]
	v_fma_f32 v2, v102, s46, v164
	v_fma_f32 v3, v103, s46, v164
	v_pk_fma_f32 v[100:101], v[102:103], v[2:3], 0.5 op_sel_hi:[1,1,0]
	v_mfma_f32_16x16x32_bf16 v[2:5], v[6:9], v[104:107], v[132:135]
	v_fma_f32 v6, v102, v100, 1.0
	v_fma_f32 v7, v103, v101, 1.0
	v_pk_mul_f32 v[100:101], v[6:7], v[102:103] neg_lo:[0,1] neg_hi:[0,1]
	v_min_f32_e32 v6, v102, v103
	v_cmp_ge_f32_e32 vcc, s66, v6
	v_mfma_f32_16x16x32_bf16 v[6:9], v[10:13], v[104:107], v[136:139]
	s_and_saveexec_b64 s[52:53], vcc
	s_cbranch_execnz .LBB0_1324
.LBB0_1283:
	s_or_b64 exec, exec, s[52:53]
	v_pk_add_f32 v[10:11], v[60:61], v[92:93]
	v_pk_add_f32 v[12:13], v[64:65], v[88:89]
	v_pk_mul_f32 v[10:11], v[10:11], s[44:45] op_sel_hi:[1,0]
	v_pk_mul_f32 v[12:13], v[12:13], s[44:45] op_sel_hi:[1,0]
	v_sqrt_f32_e32 v88, v100
	v_sqrt_f32_e32 v89, v101
	v_exp_f32_e32 v10, v10
	v_exp_f32_e32 v11, v11
	v_exp_f32_e32 v12, v12
	v_exp_f32_e32 v13, v13
	v_pk_mul_f32 v[90:91], v[90:91], v[98:99]
	s_waitcnt lgkmcnt(0)
	v_lshlrev_b32_e32 v92, 16, v86
	v_pk_mul_f32 v[98:99], v[90:91], v[88:89]
	v_pk_add_f32 v[88:89], v[10:11], 1.0 op_sel_hi:[1,0]
	v_pk_add_f32 v[12:13], v[12:13], 1.0 op_sel_hi:[1,0]
	v_and_b32_e32 v93, 0xffff0000, v86
	v_pk_mul_f32 v[10:11], v[88:89], v[12:13]
	s_nop 0
	v_rcp_f32_e32 v90, v10
	v_rcp_f32_e32 v91, v11
	v_pk_mul_f32 v[10:11], v[98:99], v[92:93]
	v_pk_mul_f32 v[12:13], v[12:13], v[90:91]
	s_nop 0
	v_pk_mul_f32 v[12:13], v[56:57], v[12:13]
	v_cvt_pk_bf16_f32 v10, v96, v10
	v_cvt_pk_bf16_f32 v11, v97, v11
	s_nop 0
	v_pk_mul_f32 v[96:97], v[12:13], s[98:99] op_sel_hi:[1,0]
	s_nop 0
	v_pk_fma_f32 v[92:93], v[96:97], s[46:47], v[164:165] op_sel_hi:[1,0,0]
	v_min_f32_e32 v86, v96, v97
	v_pk_fma_f32 v[92:93], v[96:97], v[92:93], 0.5 op_sel_hi:[1,1,0]
	v_cmp_ge_f32_e32 vcc, s66, v86
	v_pk_fma_f32 v[92:93], v[96:97], v[92:93], 1.0 op_sel_hi:[1,1,0]
	s_nop 0
	v_pk_mul_f32 v[92:93], v[92:93], v[96:97] neg_lo:[0,1] neg_hi:[0,1]
	s_and_saveexec_b64 s[52:53], vcc
	s_cbranch_execnz .LBB0_1325
.LBB0_1284:
	s_or_b64 exec, exec, s[52:53]
	v_pk_add_f32 v[82:83], v[58:59], v[82:83]
	v_pk_add_f32 v[78:79], v[62:63], v[78:79]
	v_sqrt_f32_e32 v92, v92
	v_sqrt_f32_e32 v93, v93
	v_pk_mul_f32 v[82:83], v[82:83], s[44:45] op_sel_hi:[1,0]
	v_pk_mul_f32 v[78:79], v[78:79], s[44:45] op_sel_hi:[1,0]
	v_pk_mul_f32 v[88:89], v[88:89], v[90:91]
	v_exp_f32_e32 v82, v82
	v_exp_f32_e32 v83, v83
	v_exp_f32_e32 v90, v78
	v_exp_f32_e32 v91, v79
	v_lshlrev_b32_e32 v86, 16, v87
	v_and_b32_e32 v87, 0xffff0000, v87
	v_pk_mul_f32 v[88:89], v[88:89], v[92:93]
	v_pk_add_f32 v[78:79], v[82:83], 1.0 op_sel_hi:[1,0]
	v_pk_mul_f32 v[86:87], v[88:89], v[86:87]
	v_pk_add_f32 v[88:89], v[90:91], 1.0 op_sel_hi:[1,0]
	v_cvt_pk_bf16_f32 v12, v12, v86
	v_cvt_pk_bf16_f32 v13, v13, v87
	ds_write_b128 v236, v[10:13]
	v_pk_mul_f32 v[82:83], v[78:79], v[88:89]
	ds_read_b64 v[12:13], v154 offset:4096
	v_rcp_f32_e32 v82, v82
	v_rcp_f32_e32 v83, v83
	s_nop 0
	v_pk_mul_f32 v[10:11], v[88:89], v[82:83]
	s_nop 0
	v_pk_mul_f32 v[10:11], v[54:55], v[10:11]
	s_nop 0
	v_pk_mul_f32 v[88:89], v[10:11], s[98:99] op_sel_hi:[1,0]
	s_nop 0
	v_pk_fma_f32 v[86:87], v[88:89], s[46:47], v[164:165] op_sel_hi:[1,0,0]
	v_min_f32_e32 v90, v88, v89
	v_pk_fma_f32 v[86:87], v[88:89], v[86:87], 0.5 op_sel_hi:[1,1,0]
	v_cmp_ge_f32_e32 vcc, s66, v90
	v_pk_fma_f32 v[86:87], v[88:89], v[86:87], 1.0 op_sel_hi:[1,1,0]
	s_nop 0
	v_pk_mul_f32 v[86:87], v[86:87], v[88:89] neg_lo:[0,1] neg_hi:[0,1]
	s_and_saveexec_b64 s[52:53], vcc
	s_cbranch_execnz .LBB0_1326
.LBB0_1285:
	s_or_b64 exec, exec, s[52:53]
	v_pk_add_f32 v[84:85], v[60:61], v[84:85]
	v_pk_add_f32 v[80:81], v[64:65], v[80:81]
	v_pk_mul_f32 v[84:85], v[84:85], s[44:45] op_sel_hi:[1,0]
	v_pk_mul_f32 v[80:81], v[80:81], s[44:45] op_sel_hi:[1,0]
	v_exp_f32_e32 v84, v84
	v_exp_f32_e32 v85, v85
	v_exp_f32_e32 v90, v80
	v_exp_f32_e32 v91, v81
	v_sqrt_f32_e32 v86, v86
	v_sqrt_f32_e32 v87, v87
	v_pk_add_f32 v[80:81], v[84:85], 1.0 op_sel_hi:[1,0]
	v_pk_add_f32 v[84:85], v[90:91], 1.0 op_sel_hi:[1,0]
	v_pk_mul_f32 v[78:79], v[78:79], v[82:83]
	v_pk_mul_f32 v[82:83], v[80:81], v[84:85]
	s_waitcnt lgkmcnt(0)
	v_lshlrev_b32_e32 v88, 16, v12
	v_rcp_f32_e32 v82, v82
	v_rcp_f32_e32 v83, v83
	v_and_b32_e32 v89, 0xffff0000, v12
	v_pk_mul_f32 v[78:79], v[78:79], v[86:87]
	s_nop 0
	v_pk_mul_f32 v[78:79], v[78:79], v[88:89]
	s_nop 0
	v_cvt_pk_bf16_f32 v10, v10, v78
	v_cvt_pk_bf16_f32 v11, v11, v79
	v_pk_mul_f32 v[78:79], v[84:85], v[82:83]
	s_nop 0
	v_pk_mul_f32 v[78:79], v[56:57], v[78:79]
	s_nop 0
	v_pk_mul_f32 v[84:85], v[78:79], s[98:99] op_sel_hi:[1,0]
	s_nop 0
	v_pk_fma_f32 v[86:87], v[84:85], s[46:47], v[164:165] op_sel_hi:[1,0,0]
	v_min_f32_e32 v12, v84, v85
	v_pk_fma_f32 v[86:87], v[84:85], v[86:87], 0.5 op_sel_hi:[1,1,0]
	v_cmp_ge_f32_e32 vcc, s66, v12
	v_pk_fma_f32 v[86:87], v[84:85], v[86:87], 1.0 op_sel_hi:[1,1,0]
	s_nop 0
	v_pk_mul_f32 v[86:87], v[86:87], v[84:85] neg_lo:[0,1] neg_hi:[0,1]
	s_and_saveexec_b64 s[52:53], vcc
	s_cbranch_execnz .LBB0_1327
.LBB0_1286:
	s_or_b64 exec, exec, s[52:53]
	v_pk_add_f32 v[70:71], v[58:59], v[70:71]
	v_pk_add_f32 v[74:75], v[62:63], v[74:75]
	v_sqrt_f32_e32 v84, v86
	v_sqrt_f32_e32 v85, v87
	v_pk_mul_f32 v[70:71], v[70:71], s[44:45] op_sel_hi:[1,0]
	v_pk_mul_f32 v[74:75], v[74:75], s[44:45] op_sel_hi:[1,0]
	v_exp_f32_e32 v70, v70
	v_exp_f32_e32 v71, v71
	v_exp_f32_e32 v74, v74
	v_exp_f32_e32 v75, v75
	v_pk_mul_f32 v[80:81], v[80:81], v[82:83]
	v_lshlrev_b32_e32 v12, 16, v13
	v_and_b32_e32 v13, 0xffff0000, v13
	v_pk_mul_f32 v[80:81], v[80:81], v[84:85]
	v_pk_add_f32 v[70:71], v[70:71], 1.0 op_sel_hi:[1,0]
	v_pk_mul_f32 v[12:13], v[80:81], v[12:13]
	v_pk_add_f32 v[80:81], v[74:75], 1.0 op_sel_hi:[1,0]
	v_cvt_pk_bf16_f32 v12, v78, v12
	v_cvt_pk_bf16_f32 v13, v79, v13
	ds_write_b128 v236, v[10:13] offset:2432
	v_pk_mul_f32 v[74:75], v[70:71], v[80:81]
	ds_read_b64 v[12:13], v154 offset:8192
	v_rcp_f32_e32 v74, v74
	v_rcp_f32_e32 v75, v75
	s_nop 0
	v_pk_mul_f32 v[10:11], v[80:81], v[74:75]
	s_nop 0
	v_pk_mul_f32 v[10:11], v[54:55], v[10:11]
	s_nop 0
	v_pk_mul_f32 v[80:81], v[10:11], s[98:99] op_sel_hi:[1,0]
	s_nop 0
	v_pk_fma_f32 v[78:79], v[80:81], s[46:47], v[164:165] op_sel_hi:[1,0,0]
	v_min_f32_e32 v82, v80, v81
	v_pk_fma_f32 v[78:79], v[80:81], v[78:79], 0.5 op_sel_hi:[1,1,0]
	v_cmp_ge_f32_e32 vcc, s66, v82
	v_pk_fma_f32 v[78:79], v[80:81], v[78:79], 1.0 op_sel_hi:[1,1,0]
	s_nop 0
	v_pk_mul_f32 v[78:79], v[78:79], v[80:81] neg_lo:[0,1] neg_hi:[0,1]
	s_and_saveexec_b64 s[52:53], vcc
	s_cbranch_execnz .LBB0_1328
.LBB0_1287:
	s_or_b64 exec, exec, s[52:53]
	v_pk_add_f32 v[72:73], v[60:61], v[72:73]
	v_pk_add_f32 v[76:77], v[64:65], v[76:77]
	v_pk_mul_f32 v[72:73], v[72:73], s[44:45] op_sel_hi:[1,0]
	v_pk_mul_f32 v[76:77], v[76:77], s[44:45] op_sel_hi:[1,0]
	v_exp_f32_e32 v72, v72
	v_exp_f32_e32 v73, v73
	v_exp_f32_e32 v76, v76
	v_exp_f32_e32 v77, v77
	v_sqrt_f32_e32 v78, v78
	v_sqrt_f32_e32 v79, v79
	v_pk_add_f32 v[72:73], v[72:73], 1.0 op_sel_hi:[1,0]
	v_pk_add_f32 v[76:77], v[76:77], 1.0 op_sel_hi:[1,0]
	v_pk_mul_f32 v[70:71], v[70:71], v[74:75]
	v_pk_mul_f32 v[74:75], v[72:73], v[76:77]
	s_waitcnt lgkmcnt(0)
	v_lshlrev_b32_e32 v80, 16, v12
	v_rcp_f32_e32 v74, v74
	v_rcp_f32_e32 v75, v75
	v_and_b32_e32 v81, 0xffff0000, v12
	v_pk_mul_f32 v[70:71], v[70:71], v[78:79]
	s_nop 0
	v_pk_mul_f32 v[70:71], v[70:71], v[80:81]
	s_nop 0
	v_cvt_pk_bf16_f32 v10, v10, v70
	v_cvt_pk_bf16_f32 v11, v11, v71
	v_pk_mul_f32 v[70:71], v[76:77], v[74:75]
	s_nop 0
	v_pk_mul_f32 v[70:71], v[56:57], v[70:71]
	s_nop 0
	v_pk_mul_f32 v[76:77], v[70:71], s[98:99] op_sel_hi:[1,0]
	s_nop 0
	v_pk_fma_f32 v[78:79], v[76:77], s[46:47], v[164:165] op_sel_hi:[1,0,0]
	v_min_f32_e32 v12, v76, v77
	v_pk_fma_f32 v[78:79], v[76:77], v[78:79], 0.5 op_sel_hi:[1,1,0]
	v_cmp_ge_f32_e32 vcc, s66, v12
	v_pk_fma_f32 v[78:79], v[76:77], v[78:79], 1.0 op_sel_hi:[1,1,0]
	s_nop 0
	v_pk_mul_f32 v[78:79], v[78:79], v[76:77] neg_lo:[0,1] neg_hi:[0,1]
	s_and_saveexec_b64 s[52:53], vcc
	s_cbranch_execnz .LBB0_1329
.LBB0_1288:
	s_or_b64 exec, exec, s[52:53]
	v_pk_add_f32 v[58:59], v[58:59], v[66:67]
	v_pk_add_f32 v[14:15], v[62:63], v[14:15]
	v_pk_mul_f32 v[58:59], v[58:59], s[44:45] op_sel_hi:[1,0]
	v_pk_mul_f32 v[14:15], v[14:15], s[44:45] op_sel_hi:[1,0]
	v_exp_f32_e32 v58, v58
	v_exp_f32_e32 v59, v59
	v_exp_f32_e32 v62, v14
	v_exp_f32_e32 v63, v15
	v_sqrt_f32_e32 v76, v78
	v_sqrt_f32_e32 v77, v79
	v_pk_add_f32 v[14:15], v[58:59], 1.0 op_sel_hi:[1,0]
	v_pk_add_f32 v[62:63], v[62:63], 1.0 op_sel_hi:[1,0]
	v_pk_mul_f32 v[72:73], v[72:73], v[74:75]
	v_pk_mul_f32 v[58:59], v[14:15], v[62:63]
	v_lshlrev_b32_e32 v12, 16, v13
	v_rcp_f32_e32 v58, v58
	v_rcp_f32_e32 v59, v59
	v_and_b32_e32 v13, 0xffff0000, v13
	v_pk_mul_f32 v[72:73], v[72:73], v[76:77]
	s_nop 0
	v_pk_mul_f32 v[12:13], v[72:73], v[12:13]
	s_nop 0
	v_cvt_pk_bf16_f32 v12, v70, v12
	v_cvt_pk_bf16_f32 v13, v71, v13
	ds_write_b128 v236, v[10:13] offset:4864
	v_pk_mul_f32 v[10:11], v[62:63], v[58:59]
	ds_read_b64 v[12:13], v154 offset:12288
	v_pk_mul_f32 v[10:11], v[54:55], v[10:11]
	s_nop 0
	v_pk_mul_f32 v[62:63], v[10:11], s[98:99] op_sel_hi:[1,0]
	s_nop 0
	v_pk_fma_f32 v[54:55], v[62:63], s[46:47], v[164:165] op_sel_hi:[1,0,0]
	v_min_f32_e32 v66, v62, v63
	v_pk_fma_f32 v[54:55], v[62:63], v[54:55], 0.5 op_sel_hi:[1,1,0]
	v_cmp_ge_f32_e32 vcc, s66, v66
	v_pk_fma_f32 v[54:55], v[62:63], v[54:55], 1.0 op_sel_hi:[1,1,0]
	s_nop 0
	v_pk_mul_f32 v[54:55], v[54:55], v[62:63] neg_lo:[0,1] neg_hi:[0,1]
	s_and_saveexec_b64 s[52:53], vcc
	s_cbranch_execnz .LBB0_1330
.LBB0_1289:
	s_or_b64 exec, exec, s[52:53]
	v_pk_add_f32 v[60:61], v[60:61], v[68:69]
	v_pk_add_f32 v[16:17], v[64:65], v[16:17]
	v_pk_mul_f32 v[60:61], v[60:61], s[44:45] op_sel_hi:[1,0]
	v_pk_mul_f32 v[16:17], v[16:17], s[44:45] op_sel_hi:[1,0]
	v_sqrt_f32_e32 v54, v54
	v_sqrt_f32_e32 v55, v55
	v_exp_f32_e32 v60, v60
	v_exp_f32_e32 v61, v61
	v_exp_f32_e32 v16, v16
	v_exp_f32_e32 v17, v17
	v_pk_mul_f32 v[14:15], v[14:15], v[58:59]
	s_waitcnt lgkmcnt(0)
	v_lshlrev_b32_e32 v62, 16, v12
	v_pk_mul_f32 v[54:55], v[14:15], v[54:55]
	v_pk_add_f32 v[14:15], v[60:61], 1.0 op_sel_hi:[1,0]
	v_pk_add_f32 v[58:59], v[16:17], 1.0 op_sel_hi:[1,0]
	v_and_b32_e32 v63, 0xffff0000, v12
	v_pk_mul_f32 v[16:17], v[14:15], v[58:59]
	v_pk_mul_f32 v[54:55], v[54:55], v[62:63]
	v_rcp_f32_e32 v16, v16
	v_rcp_f32_e32 v17, v17
	v_cvt_pk_bf16_f32 v10, v10, v54
	v_cvt_pk_bf16_f32 v11, v11, v55
	s_nop 0
	v_pk_mul_f32 v[54:55], v[58:59], v[16:17]
	s_nop 0
	v_pk_mul_f32 v[54:55], v[56:57], v[54:55]
	s_nop 0
	v_pk_mul_f32 v[56:57], v[54:55], s[98:99] op_sel_hi:[1,0]
	s_nop 0
	v_pk_fma_f32 v[58:59], v[56:57], s[46:47], v[164:165] op_sel_hi:[1,0,0]
	v_min_f32_e32 v12, v56, v57
	v_pk_fma_f32 v[58:59], v[56:57], v[58:59], 0.5 op_sel_hi:[1,1,0]
	v_cmp_ge_f32_e32 vcc, s66, v12
	v_pk_fma_f32 v[58:59], v[56:57], v[58:59], 1.0 op_sel_hi:[1,1,0]
	s_nop 0
	v_pk_mul_f32 v[58:59], v[58:59], v[56:57] neg_lo:[0,1] neg_hi:[0,1]
	s_and_saveexec_b64 s[52:53], vcc
	s_cbranch_execnz .LBB0_1331
.LBB0_1290:
	s_or_b64 exec, exec, s[52:53]
	v_pk_mul_f32 v[14:15], v[14:15], v[16:17]
	s_waitcnt vmcnt(2)
	v_pk_add_f32 v[16:17], v[26:27], v[50:51]
	s_waitcnt vmcnt(1)
	v_pk_add_f32 v[46:47], v[22:23], v[46:47]
	v_sqrt_f32_e32 v56, v58
	v_sqrt_f32_e32 v57, v59
	v_pk_mul_f32 v[16:17], v[16:17], s[44:45] op_sel_hi:[1,0]
	v_pk_mul_f32 v[46:47], v[46:47], s[44:45] op_sel_hi:[1,0]
	v_exp_f32_e32 v16, v16
	v_exp_f32_e32 v17, v17
	v_exp_f32_e32 v46, v46
	v_exp_f32_e32 v47, v47
	v_lshlrev_b32_e32 v12, 16, v13
	v_and_b32_e32 v13, 0xffff0000, v13
	v_pk_mul_f32 v[14:15], v[14:15], v[56:57]
	v_pk_add_f32 v[46:47], v[46:47], 1.0 op_sel_hi:[1,0]
	v_pk_mul_f32 v[12:13], v[14:15], v[12:13]
	v_pk_add_f32 v[14:15], v[16:17], 1.0 op_sel_hi:[1,0]
	v_cvt_pk_bf16_f32 v12, v54, v12
	v_cvt_pk_bf16_f32 v13, v55, v13
	ds_write_b128 v236, v[10:13] offset:7296
	v_pk_mul_f32 v[16:17], v[14:15], v[46:47]
	ds_read_b64 v[12:13], v118
	v_rcp_f32_e32 v16, v16
	v_rcp_f32_e32 v17, v17
	s_nop 0
	v_pk_mul_f32 v[10:11], v[46:47], v[16:17]
	s_waitcnt vmcnt(0)
	v_pk_mul_f32 v[10:11], v[18:19], v[10:11]
	s_nop 0
	v_pk_mul_f32 v[50:51], v[10:11], s[98:99] op_sel_hi:[1,0]
	s_nop 0
	v_pk_fma_f32 v[46:47], v[50:51], s[46:47], v[164:165] op_sel_hi:[1,0,0]
	v_min_f32_e32 v54, v50, v51
	v_pk_fma_f32 v[46:47], v[50:51], v[46:47], 0.5 op_sel_hi:[1,1,0]
	v_cmp_ge_f32_e32 vcc, s66, v54
	v_pk_fma_f32 v[46:47], v[50:51], v[46:47], 1.0 op_sel_hi:[1,1,0]
	s_nop 0
	v_pk_mul_f32 v[46:47], v[46:47], v[50:51] neg_lo:[0,1] neg_hi:[0,1]
	s_and_saveexec_b64 s[52:53], vcc
	s_cbranch_execnz .LBB0_1332
.LBB0_1291:
	s_or_b64 exec, exec, s[52:53]
	v_pk_add_f32 v[50:51], v[28:29], v[52:53]
	v_pk_add_f32 v[48:49], v[24:25], v[48:49]
	v_pk_mul_f32 v[50:51], v[50:51], s[44:45] op_sel_hi:[1,0]
	v_pk_mul_f32 v[48:49], v[48:49], s[44:45] op_sel_hi:[1,0]
	v_sqrt_f32_e32 v46, v46
	v_sqrt_f32_e32 v47, v47
	v_exp_f32_e32 v50, v50
	v_exp_f32_e32 v51, v51
	v_exp_f32_e32 v48, v48
	v_exp_f32_e32 v49, v49
	v_pk_mul_f32 v[14:15], v[14:15], v[16:17]
	s_waitcnt lgkmcnt(0)
	v_lshlrev_b32_e32 v52, 16, v12
	v_pk_mul_f32 v[16:17], v[14:15], v[46:47]
	v_pk_add_f32 v[14:15], v[50:51], 1.0 op_sel_hi:[1,0]
	v_pk_add_f32 v[48:49], v[48:49], 1.0 op_sel_hi:[1,0]
	v_and_b32_e32 v53, 0xffff0000, v12
	v_pk_mul_f32 v[46:47], v[14:15], v[48:49]
	v_pk_mul_f32 v[16:17], v[16:17], v[52:53]
	v_rcp_f32_e32 v46, v46
	v_rcp_f32_e32 v47, v47
	v_cvt_pk_bf16_f32 v10, v10, v16
	v_cvt_pk_bf16_f32 v11, v11, v17
	s_nop 0
	v_pk_mul_f32 v[16:17], v[48:49], v[46:47]
	s_nop 0
	v_pk_mul_f32 v[16:17], v[20:21], v[16:17]
	s_nop 0
	v_pk_mul_f32 v[50:51], v[16:17], s[98:99] op_sel_hi:[1,0]
	s_nop 0
	v_pk_fma_f32 v[48:49], v[50:51], s[46:47], v[164:165] op_sel_hi:[1,0,0]
	v_min_f32_e32 v12, v50, v51
	v_pk_fma_f32 v[48:49], v[50:51], v[48:49], 0.5 op_sel_hi:[1,1,0]
	v_cmp_ge_f32_e32 vcc, s66, v12
	v_pk_fma_f32 v[48:49], v[50:51], v[48:49], 1.0 op_sel_hi:[1,1,0]
	s_nop 0
	v_pk_mul_f32 v[48:49], v[48:49], v[50:51] neg_lo:[0,1] neg_hi:[0,1]
	s_and_saveexec_b64 s[52:53], vcc
	s_cbranch_execnz .LBB0_1333
.LBB0_1292:
	s_or_b64 exec, exec, s[52:53]
	v_pk_add_f32 v[42:43], v[26:27], v[42:43]
	v_pk_add_f32 v[38:39], v[22:23], v[38:39]
	v_sqrt_f32_e32 v48, v48
	v_sqrt_f32_e32 v49, v49
	v_pk_mul_f32 v[42:43], v[42:43], s[44:45] op_sel_hi:[1,0]
	v_pk_mul_f32 v[38:39], v[38:39], s[44:45] op_sel_hi:[1,0]
	v_exp_f32_e32 v42, v42
	v_exp_f32_e32 v43, v43
	v_exp_f32_e32 v38, v38
	v_exp_f32_e32 v39, v39
	v_pk_mul_f32 v[14:15], v[14:15], v[46:47]
	v_lshlrev_b32_e32 v12, 16, v13
	v_and_b32_e32 v13, 0xffff0000, v13
	v_pk_mul_f32 v[14:15], v[14:15], v[48:49]
	s_nop 0
	v_pk_mul_f32 v[12:13], v[14:15], v[12:13]
	v_pk_add_f32 v[14:15], v[42:43], 1.0 op_sel_hi:[1,0]
	v_pk_add_f32 v[42:43], v[38:39], 1.0 op_sel_hi:[1,0]
	v_cvt_pk_bf16_f32 v12, v16, v12
	v_cvt_pk_bf16_f32 v13, v17, v13
	ds_write_b128 v236, v[10:13] offset:64
	v_pk_mul_f32 v[38:39], v[14:15], v[42:43]
	ds_read_b64 v[12:13], v118 offset:4096
	v_rcp_f32_e32 v38, v38
	v_rcp_f32_e32 v39, v39
	s_nop 0
	v_pk_mul_f32 v[10:11], v[42:43], v[38:39]
	s_nop 0
	v_pk_mul_f32 v[10:11], v[18:19], v[10:11]
	s_nop 0
	v_pk_mul_f32 v[42:43], v[10:11], s[98:99] op_sel_hi:[1,0]
	s_nop 0
	v_pk_fma_f32 v[16:17], v[42:43], s[46:47], v[164:165] op_sel_hi:[1,0,0]
	v_min_f32_e32 v46, v42, v43
	v_pk_fma_f32 v[16:17], v[42:43], v[16:17], 0.5 op_sel_hi:[1,1,0]
	v_cmp_ge_f32_e32 vcc, s66, v46
	v_pk_fma_f32 v[16:17], v[42:43], v[16:17], 1.0 op_sel_hi:[1,1,0]
	s_nop 0
	v_pk_mul_f32 v[16:17], v[16:17], v[42:43] neg_lo:[0,1] neg_hi:[0,1]
	s_and_saveexec_b64 s[52:53], vcc
	s_cbranch_execnz .LBB0_1334
.LBB0_1293:
	s_or_b64 exec, exec, s[52:53]
	v_pk_add_f32 v[42:43], v[28:29], v[44:45]
	v_pk_add_f32 v[40:41], v[24:25], v[40:41]
	v_pk_mul_f32 v[42:43], v[42:43], s[44:45] op_sel_hi:[1,0]
	v_pk_mul_f32 v[40:41], v[40:41], s[44:45] op_sel_hi:[1,0]
	v_sqrt_f32_e32 v16, v16
	v_sqrt_f32_e32 v17, v17
	v_exp_f32_e32 v42, v42
	v_exp_f32_e32 v43, v43
	v_exp_f32_e32 v40, v40
	v_exp_f32_e32 v41, v41
	v_pk_mul_f32 v[14:15], v[14:15], v[38:39]
	s_waitcnt lgkmcnt(0)
	v_lshlrev_b32_e32 v44, 16, v12
	v_pk_mul_f32 v[38:39], v[14:15], v[16:17]
	v_pk_add_f32 v[14:15], v[42:43], 1.0 op_sel_hi:[1,0]
	v_pk_add_f32 v[40:41], v[40:41], 1.0 op_sel_hi:[1,0]
	v_and_b32_e32 v45, 0xffff0000, v12
	v_pk_mul_f32 v[16:17], v[14:15], v[40:41]
	v_pk_mul_f32 v[38:39], v[38:39], v[44:45]
	v_rcp_f32_e32 v16, v16
	v_rcp_f32_e32 v17, v17
	v_cvt_pk_bf16_f32 v10, v10, v38
	v_cvt_pk_bf16_f32 v11, v11, v39
	s_nop 0
	v_pk_mul_f32 v[38:39], v[40:41], v[16:17]
	s_nop 0
	v_pk_mul_f32 v[38:39], v[20:21], v[38:39]
	s_nop 0
	v_pk_mul_f32 v[40:41], v[38:39], s[98:99] op_sel_hi:[1,0]
	s_nop 0
	v_pk_fma_f32 v[42:43], v[40:41], s[46:47], v[164:165] op_sel_hi:[1,0,0]
	v_min_f32_e32 v12, v40, v41
	v_pk_fma_f32 v[42:43], v[40:41], v[42:43], 0.5 op_sel_hi:[1,1,0]
	v_cmp_ge_f32_e32 vcc, s66, v12
	v_pk_fma_f32 v[42:43], v[40:41], v[42:43], 1.0 op_sel_hi:[1,1,0]
	s_nop 0
	v_pk_mul_f32 v[42:43], v[42:43], v[40:41] neg_lo:[0,1] neg_hi:[0,1]
	s_and_saveexec_b64 s[52:53], vcc
	s_cbranch_execnz .LBB0_1335
.LBB0_1294:
	s_or_b64 exec, exec, s[52:53]
	v_pk_mul_f32 v[14:15], v[14:15], v[16:17]
	v_pk_add_f32 v[16:17], v[26:27], v[30:31]
	v_pk_add_f32 v[30:31], v[22:23], v[34:35]
	v_sqrt_f32_e32 v40, v42
	v_sqrt_f32_e32 v41, v43
	v_pk_mul_f32 v[16:17], v[16:17], s[44:45] op_sel_hi:[1,0]
	v_pk_mul_f32 v[30:31], v[30:31], s[44:45] op_sel_hi:[1,0]
	v_exp_f32_e32 v16, v16
	v_exp_f32_e32 v17, v17
	v_exp_f32_e32 v30, v30
	v_exp_f32_e32 v31, v31
	v_lshlrev_b32_e32 v12, 16, v13
	v_and_b32_e32 v13, 0xffff0000, v13
	v_pk_mul_f32 v[14:15], v[14:15], v[40:41]
	v_pk_add_f32 v[30:31], v[30:31], 1.0 op_sel_hi:[1,0]
	v_pk_mul_f32 v[12:13], v[14:15], v[12:13]
	v_pk_add_f32 v[14:15], v[16:17], 1.0 op_sel_hi:[1,0]
	v_cvt_pk_bf16_f32 v12, v38, v12
	v_cvt_pk_bf16_f32 v13, v39, v13
	ds_write_b128 v236, v[10:13] offset:2496
	v_pk_mul_f32 v[16:17], v[14:15], v[30:31]
	ds_read_b64 v[12:13], v118 offset:8192
	v_rcp_f32_e32 v16, v16
	v_rcp_f32_e32 v17, v17
	s_nop 0
	v_pk_mul_f32 v[10:11], v[30:31], v[16:17]
	s_nop 0
	v_pk_mul_f32 v[10:11], v[18:19], v[10:11]
	s_nop 0
	v_pk_mul_f32 v[34:35], v[10:11], s[98:99] op_sel_hi:[1,0]
	s_nop 0
	v_pk_fma_f32 v[30:31], v[34:35], s[46:47], v[164:165] op_sel_hi:[1,0,0]
	v_min_f32_e32 v38, v34, v35
	v_pk_fma_f32 v[30:31], v[34:35], v[30:31], 0.5 op_sel_hi:[1,1,0]
	v_cmp_ge_f32_e32 vcc, s66, v38
	v_pk_fma_f32 v[30:31], v[34:35], v[30:31], 1.0 op_sel_hi:[1,1,0]
	s_nop 0
	v_pk_mul_f32 v[30:31], v[30:31], v[34:35] neg_lo:[0,1] neg_hi:[0,1]
	s_and_saveexec_b64 s[52:53], vcc
	s_cbranch_execnz .LBB0_1336
.LBB0_1295:
	s_or_b64 exec, exec, s[52:53]
	v_pk_add_f32 v[32:33], v[28:29], v[32:33]
	v_pk_add_f32 v[34:35], v[24:25], v[36:37]
	v_pk_mul_f32 v[32:33], v[32:33], s[44:45] op_sel_hi:[1,0]
	v_pk_mul_f32 v[34:35], v[34:35], s[44:45] op_sel_hi:[1,0]
	v_sqrt_f32_e32 v30, v30
	v_sqrt_f32_e32 v31, v31
	v_exp_f32_e32 v32, v32
	v_exp_f32_e32 v33, v33
	v_exp_f32_e32 v34, v34
	v_exp_f32_e32 v35, v35
	v_pk_mul_f32 v[14:15], v[14:15], v[16:17]
	s_waitcnt lgkmcnt(0)
	v_lshlrev_b32_e32 v36, 16, v12
	v_pk_mul_f32 v[16:17], v[14:15], v[30:31]
	v_pk_add_f32 v[14:15], v[32:33], 1.0 op_sel_hi:[1,0]
	v_pk_add_f32 v[32:33], v[34:35], 1.0 op_sel_hi:[1,0]
	v_and_b32_e32 v37, 0xffff0000, v12
	v_pk_mul_f32 v[30:31], v[14:15], v[32:33]
	v_pk_mul_f32 v[16:17], v[16:17], v[36:37]
	v_rcp_f32_e32 v30, v30
	v_rcp_f32_e32 v31, v31
	v_cvt_pk_bf16_f32 v10, v10, v16
	v_cvt_pk_bf16_f32 v11, v11, v17
	s_nop 0
	v_pk_mul_f32 v[16:17], v[32:33], v[30:31]
	s_nop 0
	v_pk_mul_f32 v[16:17], v[20:21], v[16:17]
	s_nop 0
	v_pk_mul_f32 v[32:33], v[16:17], s[98:99] op_sel_hi:[1,0]
	s_nop 0
	v_pk_fma_f32 v[34:35], v[32:33], s[46:47], v[164:165] op_sel_hi:[1,0,0]
	v_min_f32_e32 v12, v32, v33
	v_pk_fma_f32 v[34:35], v[32:33], v[34:35], 0.5 op_sel_hi:[1,1,0]
	v_cmp_ge_f32_e32 vcc, s66, v12
	v_pk_fma_f32 v[34:35], v[32:33], v[34:35], 1.0 op_sel_hi:[1,1,0]
	s_nop 0
	v_pk_mul_f32 v[34:35], v[34:35], v[32:33] neg_lo:[0,1] neg_hi:[0,1]
	s_and_saveexec_b64 s[52:53], vcc
	s_cbranch_execnz .LBB0_1337
.LBB0_1296:
	s_or_b64 exec, exec, s[52:53]
	v_pk_add_f32 v[2:3], v[26:27], v[2:3]
	v_pk_add_f32 v[6:7], v[22:23], v[6:7]
	v_pk_mul_f32 v[2:3], v[2:3], s[44:45] op_sel_hi:[1,0]
	v_pk_mul_f32 v[6:7], v[6:7], s[44:45] op_sel_hi:[1,0]
	v_exp_f32_e32 v2, v2
	v_exp_f32_e32 v3, v3
	v_exp_f32_e32 v6, v6
	v_exp_f32_e32 v7, v7
	v_sqrt_f32_e32 v32, v34
	v_sqrt_f32_e32 v33, v35
	v_pk_mul_f32 v[14:15], v[14:15], v[30:31]
	v_pk_add_f32 v[2:3], v[2:3], 1.0 op_sel_hi:[1,0]
	v_pk_add_f32 v[22:23], v[6:7], 1.0 op_sel_hi:[1,0]
	v_lshlrev_b32_e32 v12, 16, v13
	v_and_b32_e32 v13, 0xffff0000, v13
	v_pk_mul_f32 v[14:15], v[14:15], v[32:33]
	v_pk_mul_f32 v[6:7], v[2:3], v[22:23]
	v_pk_mul_f32 v[12:13], v[14:15], v[12:13]
	v_rcp_f32_e32 v14, v6
	v_rcp_f32_e32 v15, v7
	v_cvt_pk_bf16_f32 v12, v16, v12
	v_cvt_pk_bf16_f32 v13, v17, v13
	ds_write_b128 v236, v[10:13] offset:4928
	v_pk_mul_f32 v[10:11], v[22:23], v[14:15]
	ds_read_b64 v[6:7], v118 offset:12288
	v_pk_mul_f32 v[10:11], v[18:19], v[10:11]
	s_nop 0
	v_pk_mul_f32 v[16:17], v[10:11], s[98:99] op_sel_hi:[1,0]
	s_nop 0
	v_pk_fma_f32 v[12:13], v[16:17], s[46:47], v[164:165] op_sel_hi:[1,0,0]
	v_min_f32_e32 v18, v16, v17
	v_pk_fma_f32 v[12:13], v[16:17], v[12:13], 0.5 op_sel_hi:[1,1,0]
	v_cmp_ge_f32_e32 vcc, s66, v18
	v_pk_fma_f32 v[12:13], v[16:17], v[12:13], 1.0 op_sel_hi:[1,1,0]
	s_nop 0
	v_pk_mul_f32 v[12:13], v[12:13], v[16:17] neg_lo:[0,1] neg_hi:[0,1]
	s_and_saveexec_b64 s[52:53], vcc
	s_cbranch_execnz .LBB0_1338
.LBB0_1297:
	s_or_b64 exec, exec, s[52:53]
	v_pk_add_f32 v[4:5], v[28:29], v[4:5]
	v_pk_add_f32 v[8:9], v[24:25], v[8:9]
	v_pk_mul_f32 v[4:5], v[4:5], s[44:45] op_sel_hi:[1,0]
	v_pk_mul_f32 v[8:9], v[8:9], s[44:45] op_sel_hi:[1,0]
	v_exp_f32_e32 v4, v4
	v_exp_f32_e32 v5, v5
	v_exp_f32_e32 v18, v8
	v_exp_f32_e32 v19, v9
	v_sqrt_f32_e32 v12, v12
	v_sqrt_f32_e32 v13, v13
	v_pk_mul_f32 v[2:3], v[2:3], v[14:15]
	v_pk_add_f32 v[8:9], v[4:5], 1.0 op_sel_hi:[1,0]
	v_pk_add_f32 v[4:5], v[18:19], 1.0 op_sel_hi:[1,0]
	v_pk_mul_f32 v[2:3], v[2:3], v[12:13]
	v_pk_mul_f32 v[12:13], v[8:9], v[4:5]
	s_waitcnt lgkmcnt(0)
	v_lshlrev_b32_e32 v16, 16, v6
	v_rcp_f32_e32 v12, v12
	v_rcp_f32_e32 v13, v13
	v_and_b32_e32 v17, 0xffff0000, v6
	v_pk_mul_f32 v[2:3], v[2:3], v[16:17]
	v_pk_mul_f32 v[4:5], v[4:5], v[12:13]
	s_nop 0
	v_pk_mul_f32 v[4:5], v[20:21], v[4:5]
	v_cvt_pk_bf16_f32 v2, v10, v2
	v_cvt_pk_bf16_f32 v3, v11, v3
	s_nop 0
	v_pk_mul_f32 v[14:15], v[4:5], s[98:99] op_sel_hi:[1,0]
	s_nop 0
	v_pk_fma_f32 v[10:11], v[14:15], s[46:47], v[164:165] op_sel_hi:[1,0,0]
	v_min_f32_e32 v6, v14, v15
	v_pk_fma_f32 v[10:11], v[14:15], v[10:11], 0.5 op_sel_hi:[1,1,0]
	v_cmp_ge_f32_e32 vcc, s66, v6
	v_pk_fma_f32 v[10:11], v[14:15], v[10:11], 1.0 op_sel_hi:[1,1,0]
	s_nop 0
	v_pk_mul_f32 v[10:11], v[10:11], v[14:15] neg_lo:[0,1] neg_hi:[0,1]
	s_and_saveexec_b64 s[52:53], vcc
	s_cbranch_execnz .LBB0_1339

.LBB0_1304:
	ds_read_b64 v[2:3], v238
	ds_read_b64 v[6:7], v237 offset:2016
	ds_read2_b64 v[14:17], v237 offset0:216 offset1:234
	v_or_b32_e32 v13, 64, v239
	v_or_b32_e32 v9, 0x80, v239
	s_waitcnt lgkmcnt(2)
	v_lshlrev_b32_e32 v4, 16, v2
	v_lshlrev_b32_e32 v8, 16, v3
	v_add_f32_e32 v10, 0, v4
	v_exp_f32_e32 v4, v4
	v_exp_f32_e32 v11, v8
	v_and_b32_e32 v2, 0xffff0000, v2
	v_fmac_f32_e32 v2, 0, v4
	v_and_b32_e32 v3, 0xffff0000, v3
	s_waitcnt lgkmcnt(1)
	v_lshlrev_b32_e32 v4, 16, v6
	v_add_f32_e32 v8, 0, v8
	v_fmac_f32_e32 v3, 0, v11
	v_lshlrev_b32_e32 v11, 16, v7
	v_add_f32_e32 v10, v10, v4
	v_add_f32_e32 v8, v8, v11
	v_exp_f32_e32 v4, v4
	v_exp_f32_e32 v11, v11
	v_and_b32_e32 v6, 0xffff0000, v6
	v_fmac_f32_e32 v6, v4, v2
	v_and_b32_e32 v2, 0xffff0000, v7
	v_fmac_f32_e32 v2, v11, v3
	s_waitcnt lgkmcnt(0)
	v_lshlrev_b32_e32 v3, 16, v16
	v_lshlrev_b32_e32 v4, 16, v17
	v_add_f32_e32 v7, v10, v3
	v_add_f32_e32 v8, v8, v4
	v_exp_f32_e32 v3, v3
	v_exp_f32_e32 v4, v4
	v_and_b32_e32 v10, 0xffff0000, v16
	v_fmac_f32_e32 v10, v3, v6
	v_and_b32_e32 v3, 0xffff0000, v17
	v_fmac_f32_e32 v3, v4, v2
	v_lshlrev_b32_e32 v2, 16, v14
	v_lshlrev_b32_e32 v4, 16, v15
	v_add_f32_e32 v6, v7, v2
	v_add_f32_e32 v7, v8, v4
	v_exp_f32_e32 v2, v2
	ds_read2_b64 v[16:19], v237 offset0:180 offset1:198
	v_exp_f32_e32 v4, v4
	v_and_b32_e32 v8, 0xffff0000, v14
	v_fmac_f32_e32 v8, v2, v10
	v_and_b32_e32 v2, 0xffff0000, v15
	v_fmac_f32_e32 v2, v4, v3
	s_waitcnt lgkmcnt(0)
	v_lshlrev_b32_e32 v3, 16, v18
	v_lshlrev_b32_e32 v4, 16, v19
	v_add_f32_e32 v6, v6, v3
	v_add_f32_e32 v7, v7, v4
	v_exp_f32_e32 v3, v3
	v_exp_f32_e32 v4, v4
	v_and_b32_e32 v10, 0xffff0000, v18
	v_fmac_f32_e32 v10, v3, v8
	v_and_b32_e32 v3, 0xffff0000, v19
	v_fmac_f32_e32 v3, v4, v2
	v_lshlrev_b32_e32 v2, 16, v16
	v_lshlrev_b32_e32 v4, 16, v17
	v_add_f32_e32 v6, v6, v2
	v_add_f32_e32 v7, v7, v4
	v_exp_f32_e32 v2, v2
	ds_read2_b64 v[18:21], v237 offset0:144 offset1:162
	v_exp_f32_e32 v4, v4
	v_and_b32_e32 v8, 0xffff0000, v16
	v_fmac_f32_e32 v8, v2, v10
	v_and_b32_e32 v2, 0xffff0000, v17
	v_fmac_f32_e32 v2, v4, v3
	s_waitcnt lgkmcnt(0)
	v_lshlrev_b32_e32 v3, 16, v20
	v_lshlrev_b32_e32 v4, 16, v21
	v_add_f32_e32 v6, v6, v3
	v_add_f32_e32 v7, v7, v4
	v_exp_f32_e32 v3, v3
	v_exp_f32_e32 v4, v4
	v_and_b32_e32 v10, 0xffff0000, v20
	v_fmac_f32_e32 v10, v3, v8
	v_and_b32_e32 v3, 0xffff0000, v21
	v_fmac_f32_e32 v3, v4, v2
	v_lshlrev_b32_e32 v2, 16, v18
	v_lshlrev_b32_e32 v4, 16, v19
	v_add_f32_e32 v6, v6, v2
	v_add_f32_e32 v7, v7, v4
	v_exp_f32_e32 v2, v2
	ds_read2_b64 v[14:17], v237 offset0:108 offset1:126
	v_exp_f32_e32 v4, v4
	v_and_b32_e32 v8, 0xffff0000, v18
	v_fmac_f32_e32 v8, v2, v10
	v_and_b32_e32 v2, 0xffff0000, v19
	v_fmac_f32_e32 v2, v4, v3
	s_waitcnt lgkmcnt(0)
	v_lshlrev_b32_e32 v3, 16, v16
	v_lshlrev_b32_e32 v4, 16, v17
	v_add_f32_e32 v6, v6, v3
	v_add_f32_e32 v7, v7, v4
	v_exp_f32_e32 v3, v3
	v_exp_f32_e32 v4, v4
	v_and_b32_e32 v10, 0xffff0000, v16
	v_fmac_f32_e32 v10, v3, v8
	v_and_b32_e32 v3, 0xffff0000, v17
	v_fmac_f32_e32 v3, v4, v2
	v_lshlrev_b32_e32 v2, 16, v14
	v_lshlrev_b32_e32 v4, 16, v15
	v_add_f32_e32 v6, v6, v2
	v_add_f32_e32 v7, v7, v4
	v_exp_f32_e32 v2, v2
	ds_read2_b64 v[16:19], v237 offset0:72 offset1:90
	v_exp_f32_e32 v4, v4
	v_and_b32_e32 v8, 0xffff0000, v14
	v_fmac_f32_e32 v8, v2, v10
	v_and_b32_e32 v2, 0xffff0000, v15
	v_fmac_f32_e32 v2, v4, v3
	s_waitcnt lgkmcnt(0)
	v_lshlrev_b32_e32 v3, 16, v18
	v_lshlrev_b32_e32 v4, 16, v19
	v_add_f32_e32 v6, v6, v3
	v_add_f32_e32 v7, v7, v4
	v_exp_f32_e32 v3, v3
	v_exp_f32_e32 v4, v4
	v_and_b32_e32 v10, 0xffff0000, v18
	v_fmac_f32_e32 v10, v3, v8
	v_and_b32_e32 v3, 0xffff0000, v19
	v_fmac_f32_e32 v3, v4, v2
	v_lshlrev_b32_e32 v2, 16, v16
	v_lshlrev_b32_e32 v4, 16, v17
	v_add_f32_e32 v6, v6, v2
	v_add_f32_e32 v7, v7, v4
	v_exp_f32_e32 v2, v2
	ds_read2_b64 v[18:21], v237 offset0:36 offset1:54
	v_exp_f32_e32 v4, v4
	v_and_b32_e32 v8, 0xffff0000, v16
	v_fmac_f32_e32 v8, v2, v10
	v_and_b32_e32 v2, 0xffff0000, v17
	v_fmac_f32_e32 v2, v4, v3
	s_waitcnt lgkmcnt(0)
	v_lshlrev_b32_e32 v3, 16, v20
	v_lshlrev_b32_e32 v4, 16, v21
	v_add_f32_e32 v6, v6, v3
	v_add_f32_e32 v7, v7, v4
	v_exp_f32_e32 v3, v3
	v_exp_f32_e32 v4, v4
	v_and_b32_e32 v10, 0xffff0000, v20
	v_fmac_f32_e32 v10, v3, v8
	v_and_b32_e32 v3, 0xffff0000, v21
	v_fmac_f32_e32 v3, v4, v2
	v_lshlrev_b32_e32 v2, 16, v18
	v_lshlrev_b32_e32 v4, 16, v19
	v_add_f32_e32 v6, v6, v2
	v_add_f32_e32 v7, v7, v4
	v_exp_f32_e32 v2, v2
	ds_read2_b64 v[14:17], v237 offset1:18
	v_exp_f32_e32 v4, v4
	v_and_b32_e32 v8, 0xffff0000, v18
	v_fmac_f32_e32 v8, v2, v10
	v_and_b32_e32 v2, 0xffff0000, v19
	v_fmac_f32_e32 v2, v4, v3
	s_waitcnt lgkmcnt(0)
	v_lshlrev_b32_e32 v3, 16, v16
	v_lshlrev_b32_e32 v4, 16, v17
	v_add_f32_e32 v6, v6, v3
	v_add_f32_e32 v7, v7, v4
	v_exp_f32_e32 v3, v3
	v_exp_f32_e32 v4, v4
	v_and_b32_e32 v10, 0xffff0000, v16
	v_fmac_f32_e32 v10, v3, v8
	v_and_b32_e32 v3, 0xffff0000, v17
	v_fmac_f32_e32 v3, v4, v2
	v_lshlrev_b32_e32 v2, 16, v14
	v_lshlrev_b32_e32 v4, 16, v15
	v_mov_b32_e32 v8, v2
	v_add_f32_e32 v2, v6, v2
	v_add_f32_e32 v6, v7, v4
	v_exp_f32_e32 v8, v8
	v_and_b32_e32 v16, 0xffff0000, v14
	v_exp_f32_e32 v4, v4
	v_exp_f32_e32 v14, v2
	v_exp_f32_e32 v17, v6
	v_and_b32_e32 v18, 0xffff0000, v15
	v_or_b32_e32 v5, 0xc0, v239
	v_fmac_f32_e32 v16, v8, v10
	v_fmac_f32_e32 v18, v4, v3
	ds_bpermute_b32 v2, v5, v14
	ds_bpermute_b32 v3, v5, v17
	ds_bpermute_b32 v4, v5, v16
	ds_bpermute_b32 v5, v5, v18
	ds_bpermute_b32 v6, v9, v14
	ds_bpermute_b32 v7, v9, v17
	ds_bpermute_b32 v8, v9, v16
	ds_bpermute_b32 v9, v9, v18
	ds_bpermute_b32 v10, v13, v14
	ds_bpermute_b32 v11, v13, v17
	ds_bpermute_b32 v12, v13, v16
	ds_bpermute_b32 v13, v13, v18
	ds_bpermute_b32 v14, v239, v14
	ds_bpermute_b32 v15, v239, v17
	ds_bpermute_b32 v16, v239, v16
	ds_bpermute_b32 v17, v239, v18
	s_and_b64 vcc, exec, s[52:53]
	s_cbranch_vccnz .Lp8_nomask
	s_waitcnt vmcnt(0)
	v_add_u32_e32 v67, -1, v66
	v_cmp_gt_u32_e32 vcc, s99, v67
	s_nop 1
	v_cndmask_b32_e32 v201, 0, v38, vcc
	v_cndmask_b32_e32 v202, 0, v39, vcc
	v_cndmask_b32_e32 v203, 0, v40, vcc
	v_cndmask_b32_e32 v205, 0, v41, vcc
	v_cndmask_b32_e32 v206, 0, v42, vcc
	v_cndmask_b32_e32 v207, 0, v43, vcc
	v_cndmask_b32_e32 v209, 0, v44, vcc
	v_cndmask_b32_e32 v210, 0, v45, vcc
	v_cmp_gt_u32_e32 vcc, s99, v66
	s_nop 1
	v_cndmask_b32_e32 v212, 0, v46, vcc
	v_cndmask_b32_e32 v213, 0, v47, vcc
	v_cndmask_b32_e32 v215, 0, v48, vcc
	v_cndmask_b32_e32 v216, 0, v49, vcc
	v_or_b32_e32 v67, 1, v66
	v_cmp_gt_u32_e32 vcc, s99, v67
	s_nop 1
	v_cndmask_b32_e32 v218, 0, v50, vcc
	v_cndmask_b32_e32 v219, 0, v51, vcc
	v_cndmask_b32_e32 v221, 0, v52, vcc
	v_cndmask_b32_e32 v222, 0, v53, vcc
	v_or_b32_e32 v67, 2, v66
	v_cmp_gt_u32_e32 vcc, s99, v67
	s_nop 1
	v_cndmask_b32_e32 v224, 0, v54, vcc
	v_cndmask_b32_e32 v225, 0, v55, vcc
	v_cndmask_b32_e32 v226, 0, v56, vcc
	v_cndmask_b32_e32 v227, 0, v57, vcc
	v_or_b32_e32 v67, 3, v66
	v_cmp_gt_u32_e32 vcc, s99, v67
	s_nop 1
	v_cndmask_b32_e32 v228, 0, v58, vcc
	v_cndmask_b32_e32 v229, 0, v59, vcc
	v_cndmask_b32_e32 v230, 0, v60, vcc
	v_cndmask_b32_e32 v231, 0, v61, vcc
	v_add_u32_e32 v67, 4, v66
	v_cmp_gt_u32_e32 vcc, s99, v67
	s_nop 1
	v_cndmask_b32_e32 v232, 0, v62, vcc
	v_cndmask_b32_e32 v233, 0, v63, vcc
	v_cndmask_b32_e32 v234, 0, v64, vcc
	v_cndmask_b32_e32 v235, 0, v65, vcc

.LBB0_1466:
	v_add_u32_e32 v116, v171, v69
	v_add_u32_e32 v119, 0x800, v116
	ds_read2_b64 v[120:123], v119 offset0:224 offset1:240
	s_waitcnt lgkmcnt(0)
	v_pk_fma_f32 v[112:113], v[112:113], 0, v[114:115] op_sel_hi:[1,0,1]
	s_ashr_i32 s43, s42, 31
	v_pk_fma_f32 v[100:101], v[112:113], v[100:101], v[102:103]
	s_andn2_b64 vcc, exec, s[46:47]
	v_lshlrev_b32_e32 v114, 16, v122
	v_lshlrev_b32_e32 v124, 16, v123
	v_and_b32_e32 v115, 0xffff0000, v122
	v_add_f32_e32 v122, 0, v114
	v_exp_f32_e32 v117, v114
	v_exp_f32_e32 v118, v124
	v_and_b32_e32 v114, 0xffff0000, v123
	v_lshlrev_b32_e32 v123, 16, v120
	v_lshlrev_b32_e32 v125, 16, v121
	v_add_f32_e32 v128, v122, v123
	v_add_f32_e32 v124, 0, v124
	v_exp_f32_e32 v130, v123
	v_add_f32_e32 v129, v124, v125
	v_exp_f32_e32 v131, v125
	ds_read2_b64 v[122:125], v119 offset0:192 offset1:208
	v_fma_f32 v126, 0, v117, v115
	v_and_b32_e32 v120, 0xffff0000, v120
	v_fma_f32 v127, 0, v118, v114
	v_fmac_f32_e32 v120, v130, v126
	v_and_b32_e32 v121, 0xffff0000, v121
	s_waitcnt lgkmcnt(0)
	v_lshlrev_b32_e32 v126, 16, v124
	v_fmac_f32_e32 v121, v131, v127
	v_lshlrev_b32_e32 v127, 16, v125
	v_add_f32_e32 v128, v128, v126
	v_add_f32_e32 v129, v129, v127
	v_exp_f32_e32 v126, v126
	v_exp_f32_e32 v127, v127
	v_and_b32_e32 v130, 0xffff0000, v124
	v_fmac_f32_e32 v130, v126, v120
	v_and_b32_e32 v120, 0xffff0000, v125
	v_fmac_f32_e32 v120, v127, v121
	v_lshlrev_b32_e32 v121, 16, v122
	v_lshlrev_b32_e32 v124, 16, v123
	v_add_f32_e32 v128, v128, v121
	v_add_f32_e32 v129, v129, v124
	v_exp_f32_e32 v121, v121
	v_exp_f32_e32 v131, v124
	ds_read2_b64 v[124:127], v119 offset0:160 offset1:176
	v_and_b32_e32 v122, 0xffff0000, v122
	v_fmac_f32_e32 v122, v121, v130
	v_and_b32_e32 v121, 0xffff0000, v123
	v_fmac_f32_e32 v121, v131, v120
	s_waitcnt lgkmcnt(0)
	v_lshlrev_b32_e32 v120, 16, v126
	v_lshlrev_b32_e32 v123, 16, v127
	v_add_f32_e32 v128, v128, v120
	v_add_f32_e32 v129, v129, v123
	v_exp_f32_e32 v120, v120
	v_exp_f32_e32 v123, v123
	v_and_b32_e32 v126, 0xffff0000, v126
	v_fmac_f32_e32 v126, v120, v122
	v_and_b32_e32 v127, 0xffff0000, v127
	v_lshlrev_b32_e32 v120, 16, v124
	v_fmac_f32_e32 v127, v123, v121
	v_lshlrev_b32_e32 v121, 16, v125
	v_add_f32_e32 v128, v128, v120
	v_exp_f32_e32 v130, v120
	v_add_f32_e32 v129, v129, v121
	v_exp_f32_e32 v131, v121
	ds_read2_b64 v[120:123], v119 offset0:128 offset1:144
	v_and_b32_e32 v124, 0xffff0000, v124
	v_fmac_f32_e32 v124, v130, v126
	v_and_b32_e32 v125, 0xffff0000, v125
	v_fmac_f32_e32 v125, v131, v127
	s_waitcnt lgkmcnt(0)
	v_lshlrev_b32_e32 v126, 16, v122
	v_lshlrev_b32_e32 v127, 16, v123
	v_add_f32_e32 v128, v128, v126
	v_add_f32_e32 v129, v129, v127
	v_exp_f32_e32 v126, v126
	v_exp_f32_e32 v127, v127
	v_and_b32_e32 v130, 0xffff0000, v122
	v_fmac_f32_e32 v130, v126, v124
	v_and_b32_e32 v126, 0xffff0000, v123
	v_lshlrev_b32_e32 v122, 16, v120
	v_fmac_f32_e32 v126, v127, v125
	v_lshlrev_b32_e32 v123, 16, v121
	v_add_f32_e32 v127, v128, v122
	v_add_f32_e32 v128, v129, v123
	v_exp_f32_e32 v129, v122
	v_exp_f32_e32 v131, v123
	ds_read2_b64 v[122:125], v119 offset0:96 offset1:112
	v_and_b32_e32 v121, 0xffff0000, v121
	v_and_b32_e32 v120, 0xffff0000, v120
	v_fmac_f32_e32 v121, v131, v126
	v_fmac_f32_e32 v120, v129, v130
	s_waitcnt lgkmcnt(0)
	v_lshlrev_b32_e32 v126, 16, v124
	v_lshlrev_b32_e32 v129, 16, v125
	v_add_f32_e32 v127, v127, v126
	v_add_f32_e32 v128, v128, v129
	v_exp_f32_e32 v126, v126
	v_exp_f32_e32 v129, v129
	v_and_b32_e32 v130, 0xffff0000, v124
	v_fmac_f32_e32 v130, v126, v120
	v_and_b32_e32 v120, 0xffff0000, v125
	v_fmac_f32_e32 v120, v129, v121
	v_lshlrev_b32_e32 v121, 16, v122
	v_lshlrev_b32_e32 v124, 16, v123
	v_add_f32_e32 v129, v127, v121
	v_add_f32_e32 v128, v128, v124
	v_exp_f32_e32 v121, v121
	v_exp_f32_e32 v131, v124
	ds_read2_b64 v[124:127], v119 offset0:64 offset1:80
	v_and_b32_e32 v122, 0xffff0000, v122
	v_fmac_f32_e32 v122, v121, v130
	v_and_b32_e32 v121, 0xffff0000, v123
	v_fmac_f32_e32 v121, v131, v120
	s_waitcnt lgkmcnt(0)
	v_lshlrev_b32_e32 v120, 16, v126
	v_lshlrev_b32_e32 v123, 16, v127
	v_add_f32_e32 v129, v129, v120
	v_add_f32_e32 v128, v128, v123
	v_exp_f32_e32 v120, v120
	v_exp_f32_e32 v123, v123
	v_and_b32_e32 v126, 0xffff0000, v126
	v_fmac_f32_e32 v126, v120, v122
	v_and_b32_e32 v127, 0xffff0000, v127
	v_lshlrev_b32_e32 v120, 16, v124
	v_fmac_f32_e32 v127, v123, v121
	v_lshlrev_b32_e32 v121, 16, v125
	v_add_f32_e32 v129, v129, v120
	v_exp_f32_e32 v130, v120
	v_add_f32_e32 v128, v128, v121
	v_exp_f32_e32 v131, v121
	ds_read2_b64 v[120:123], v119 offset0:32 offset1:48
	v_and_b32_e32 v124, 0xffff0000, v124
	v_fmac_f32_e32 v124, v130, v126
	v_and_b32_e32 v125, 0xffff0000, v125
	v_fmac_f32_e32 v125, v131, v127
	s_waitcnt lgkmcnt(0)
	v_lshlrev_b32_e32 v126, 16, v122
	v_lshlrev_b32_e32 v127, 16, v123
	v_add_f32_e32 v129, v129, v126
	v_add_f32_e32 v128, v128, v127
	v_exp_f32_e32 v126, v126
	v_exp_f32_e32 v127, v127
	v_and_b32_e32 v130, 0xffff0000, v122
	v_fmac_f32_e32 v130, v126, v124
	v_and_b32_e32 v126, 0xffff0000, v123
	v_lshlrev_b32_e32 v122, 16, v120
	v_fmac_f32_e32 v126, v127, v125
	v_lshlrev_b32_e32 v123, 16, v121
	v_add_f32_e32 v127, v129, v122
	v_exp_f32_e32 v129, v122
	v_add_f32_e32 v128, v128, v123
	v_exp_f32_e32 v131, v123
	ds_read2_b64 v[122:125], v119 offset1:16
	v_and_b32_e32 v119, 0xffff0000, v120
	v_and_b32_e32 v120, 0xffff0000, v121
	v_fmac_f32_e32 v120, v131, v126
	v_fmac_f32_e32 v119, v129, v130
	s_waitcnt lgkmcnt(0)
	v_lshlrev_b32_e32 v121, 16, v124
	v_lshlrev_b32_e32 v126, 16, v125
	v_add_f32_e32 v127, v127, v121
	v_add_f32_e32 v128, v128, v126
	v_exp_f32_e32 v121, v121
	v_exp_f32_e32 v126, v126
	v_and_b32_e32 v129, 0xffff0000, v124
	v_fmac_f32_e32 v129, v121, v119
	v_and_b32_e32 v119, 0xffff0000, v125
	v_fmac_f32_e32 v119, v126, v120
	v_lshlrev_b32_e32 v120, 16, v122
	v_lshlrev_b32_e32 v121, 16, v123
	v_add_f32_e32 v130, v127, v120
	v_add_f32_e32 v128, v128, v121
	v_exp_f32_e32 v120, v120
	ds_read2_b64 v[124:127], v116 offset0:224 offset1:240
	v_exp_f32_e32 v121, v121
	v_and_b32_e32 v122, 0xffff0000, v122
	v_fmac_f32_e32 v122, v120, v129
	v_and_b32_e32 v120, 0xffff0000, v123
	v_fmac_f32_e32 v120, v121, v119
	s_waitcnt lgkmcnt(0)
	v_lshlrev_b32_e32 v119, 16, v126
	v_lshlrev_b32_e32 v121, 16, v127
	v_add_f32_e32 v123, v130, v119
	v_add_f32_e32 v128, v128, v121
	v_exp_f32_e32 v119, v119
	v_exp_f32_e32 v121, v121
	v_and_b32_e32 v126, 0xffff0000, v126
	v_fmac_f32_e32 v126, v119, v122
	v_and_b32_e32 v119, 0xffff0000, v127
	v_fmac_f32_e32 v119, v121, v120
	v_lshlrev_b32_e32 v120, 16, v124
	v_lshlrev_b32_e32 v121, 16, v125
	v_add_f32_e32 v127, v123, v120
	v_exp_f32_e32 v129, v120
	v_add_f32_e32 v128, v128, v121
	v_exp_f32_e32 v130, v121
	ds_read2_b64 v[120:123], v116 offset0:192 offset1:208
	v_and_b32_e32 v125, 0xffff0000, v125
	v_and_b32_e32 v124, 0xffff0000, v124
	v_fmac_f32_e32 v125, v130, v119
	v_fmac_f32_e32 v124, v129, v126
	s_waitcnt lgkmcnt(0)
	v_lshlrev_b32_e32 v119, 16, v122
	v_lshlrev_b32_e32 v126, 16, v123
	v_add_f32_e32 v127, v127, v119
	v_add_f32_e32 v128, v128, v126
	v_exp_f32_e32 v119, v119
	v_exp_f32_e32 v126, v126
	v_and_b32_e32 v129, 0xffff0000, v122
	v_fmac_f32_e32 v129, v119, v124
	v_and_b32_e32 v119, 0xffff0000, v123
	v_lshlrev_b32_e32 v122, 16, v120
	v_fmac_f32_e32 v119, v126, v125
	v_lshlrev_b32_e32 v123, 16, v121
	v_add_f32_e32 v126, v127, v122
	v_add_f32_e32 v127, v128, v123
	v_exp_f32_e32 v128, v122
	v_exp_f32_e32 v130, v123
	ds_read2_b64 v[122:125], v116 offset0:160 offset1:176
	v_and_b32_e32 v121, 0xffff0000, v121
	v_and_b32_e32 v120, 0xffff0000, v120
	v_fmac_f32_e32 v121, v130, v119
	v_fmac_f32_e32 v120, v128, v129
	s_waitcnt lgkmcnt(0)
	v_lshlrev_b32_e32 v119, 16, v124
	v_lshlrev_b32_e32 v128, 16, v125
	v_add_f32_e32 v126, v126, v119
	v_add_f32_e32 v127, v127, v128
	v_exp_f32_e32 v119, v119
	v_exp_f32_e32 v128, v128
	v_and_b32_e32 v129, 0xffff0000, v124
	v_fmac_f32_e32 v129, v119, v120
	v_and_b32_e32 v119, 0xffff0000, v125
	v_lshlrev_b32_e32 v120, 16, v122
	v_fmac_f32_e32 v119, v128, v121
	v_lshlrev_b32_e32 v121, 16, v123
	v_add_f32_e32 v128, v126, v120
	v_add_f32_e32 v130, v127, v121
	v_exp_f32_e32 v120, v120
	ds_read2_b64 v[124:127], v116 offset0:128 offset1:144
	v_exp_f32_e32 v121, v121
	v_and_b32_e32 v122, 0xffff0000, v122
	v_fmac_f32_e32 v122, v120, v129
	v_and_b32_e32 v120, 0xffff0000, v123
	v_fmac_f32_e32 v120, v121, v119
	s_waitcnt lgkmcnt(0)
	v_lshlrev_b32_e32 v119, 16, v126
	v_lshlrev_b32_e32 v121, 16, v127
	v_add_f32_e32 v123, v128, v119
	v_add_f32_e32 v128, v130, v121
	v_exp_f32_e32 v119, v119
	v_exp_f32_e32 v121, v121
	v_and_b32_e32 v126, 0xffff0000, v126
	v_fmac_f32_e32 v126, v119, v122
	v_and_b32_e32 v119, 0xffff0000, v127
	v_fmac_f32_e32 v119, v121, v120
	v_lshlrev_b32_e32 v120, 16, v124
	v_lshlrev_b32_e32 v121, 16, v125
	v_add_f32_e32 v127, v123, v120
	v_exp_f32_e32 v129, v120
	v_add_f32_e32 v128, v128, v121
	v_exp_f32_e32 v130, v121
	ds_read2_b64 v[120:123], v116 offset0:96 offset1:112
	v_and_b32_e32 v125, 0xffff0000, v125
	v_and_b32_e32 v124, 0xffff0000, v124
	v_fmac_f32_e32 v125, v130, v119
	v_fmac_f32_e32 v124, v129, v126
	s_waitcnt lgkmcnt(0)
	v_lshlrev_b32_e32 v119, 16, v122
	v_lshlrev_b32_e32 v126, 16, v123
	v_add_f32_e32 v127, v127, v119
	v_add_f32_e32 v128, v128, v126
	v_exp_f32_e32 v119, v119
	v_exp_f32_e32 v126, v126
	v_and_b32_e32 v129, 0xffff0000, v122
	v_fmac_f32_e32 v129, v119, v124
	v_and_b32_e32 v119, 0xffff0000, v123
	v_lshlrev_b32_e32 v122, 16, v120
	v_fmac_f32_e32 v119, v126, v125
	v_lshlrev_b32_e32 v123, 16, v121
	v_add_f32_e32 v126, v127, v122
	v_add_f32_e32 v127, v128, v123
	v_exp_f32_e32 v128, v122
	v_exp_f32_e32 v130, v123
	ds_read2_b64 v[122:125], v116 offset0:64 offset1:80
	v_and_b32_e32 v121, 0xffff0000, v121
	v_and_b32_e32 v120, 0xffff0000, v120
	v_fmac_f32_e32 v121, v130, v119
	v_fmac_f32_e32 v120, v128, v129
	s_waitcnt lgkmcnt(0)
	v_lshlrev_b32_e32 v119, 16, v124
	v_lshlrev_b32_e32 v128, 16, v125
	v_add_f32_e32 v126, v126, v119
	v_add_f32_e32 v127, v127, v128
	v_exp_f32_e32 v119, v119
	v_exp_f32_e32 v128, v128
	v_and_b32_e32 v129, 0xffff0000, v124
	v_fmac_f32_e32 v129, v119, v120
	v_and_b32_e32 v119, 0xffff0000, v125
	v_lshlrev_b32_e32 v120, 16, v122
	v_fmac_f32_e32 v119, v128, v121
	v_lshlrev_b32_e32 v121, 16, v123
	v_add_f32_e32 v128, v126, v120
	v_add_f32_e32 v130, v127, v121
	v_exp_f32_e32 v120, v120
	ds_read2_b64 v[124:127], v116 offset0:32 offset1:48
	v_exp_f32_e32 v121, v121
	v_and_b32_e32 v122, 0xffff0000, v122
	v_fmac_f32_e32 v122, v120, v129
	v_and_b32_e32 v120, 0xffff0000, v123
	v_fmac_f32_e32 v120, v121, v119
	s_waitcnt lgkmcnt(0)
	v_lshlrev_b32_e32 v119, 16, v126
	v_lshlrev_b32_e32 v121, 16, v127
	v_add_f32_e32 v123, v128, v119
	v_add_f32_e32 v128, v130, v121
	v_exp_f32_e32 v119, v119
	v_exp_f32_e32 v121, v121
	v_and_b32_e32 v126, 0xffff0000, v126
	v_fmac_f32_e32 v126, v119, v122
	v_and_b32_e32 v119, 0xffff0000, v127
	v_fmac_f32_e32 v119, v121, v120
	v_lshlrev_b32_e32 v120, 16, v124
	v_lshlrev_b32_e32 v121, 16, v125
	v_add_f32_e32 v127, v123, v120
	v_exp_f32_e32 v129, v120
	v_add_f32_e32 v128, v128, v121
	v_exp_f32_e32 v130, v121
	ds_read2_b64 v[120:123], v116 offset1:16
	v_and_b32_e32 v125, 0xffff0000, v125
	v_and_b32_e32 v124, 0xffff0000, v124
	v_fmac_f32_e32 v125, v130, v119
	v_fmac_f32_e32 v124, v129, v126
	s_waitcnt lgkmcnt(0)
	v_lshlrev_b32_e32 v119, 16, v122
	v_lshlrev_b32_e32 v126, 16, v123
	v_add_f32_e32 v127, v127, v119
	v_add_f32_e32 v128, v128, v126
	v_exp_f32_e32 v119, v119
	v_exp_f32_e32 v126, v126
	v_and_b32_e32 v122, 0xffff0000, v122
	v_fmac_f32_e32 v122, v119, v124
	v_and_b32_e32 v119, 0xffff0000, v123
	v_lshlrev_b32_e32 v123, 16, v120
	v_fmac_f32_e32 v119, v126, v125
	v_exp_f32_e32 v125, v123
	v_lshlrev_b32_e32 v124, 16, v121
	v_add_f32_e32 v123, v127, v123
	v_and_b32_e32 v120, 0xffff0000, v120
	v_fmac_f32_e32 v120, v125, v122
	v_exp_f32_e32 v122, v124
	v_exp_f32_e32 v123, v123
	v_and_b32_e32 v121, 0xffff0000, v121
	ds_bpermute_b32 v125, v168, v120
	v_fmac_f32_e32 v121, v122, v119
	ds_bpermute_b32 v119, v168, v123
	ds_bpermute_b32 v102, v167, v123
	ds_bpermute_b32 v103, v167, v120
	v_pk_fma_f32 v[100:101], v[100:101], v[104:105], v[106:107]
	ds_bpermute_b32 v107, v166, v120
	v_pk_fma_f32 v[100:101], v[100:101], v[108:109], v[110:111]
	v_add_f32_e32 v126, v128, v124
	s_waitcnt lgkmcnt(3)
	v_fmac_f32_e32 v125, v100, v119
	v_cndmask_b32_e64 v100, v125, v100, s[6:7]
	s_waitcnt lgkmcnt(1)
	v_fmac_f32_e32 v103, v100, v102
	ds_bpermute_b32 v102, v166, v123
	v_cndmask_b32_e64 v100, v100, v103, s[8:9]
	v_exp_f32_e32 v124, v126
	ds_bpermute_b32 v126, v168, v121
	s_waitcnt lgkmcnt(1)
	v_fmac_f32_e32 v107, v100, v102
	s_waitcnt vmcnt(16)
	v_lshlrev_b32_e32 v102, 16, v236
	v_mul_f32_e32 v103, 0x3d372713, v102
	v_mul_f32_e32 v103, v103, v102
	v_fma_f32 v103, v103, v102, v102
	v_mul_f32_e32 v103, 0x3f4c422a, v103
	ds_bpermute_b32 v122, v168, v124
	v_add_f32_e32 v103, v103, v103
	v_mul_f32_e32 v103, 0x3fb8aa3b, v103
	ds_bpermute_b32 v104, v167, v124
	ds_bpermute_b32 v105, v167, v121
	v_exp_f32_e32 v103, v103
	s_waitcnt lgkmcnt(2)
	v_fmac_f32_e32 v126, v101, v122
	v_cndmask_b32_e64 v100, v100, v107, s[0:1]
	v_cndmask_b32_e64 v101, v126, v101, s[6:7]
	v_fmac_f32_e32 v115, v117, v100
	v_add_f32_e32 v100, 1.0, v103
	v_and_b32_e32 v103, 0xffff0000, v236
	s_waitcnt lgkmcnt(0)
	v_fmac_f32_e32 v105, v101, v104
	v_mul_f32_e32 v104, 0x3d372713, v103
	v_mul_f32_e32 v104, v104, v103
	v_fma_f32 v104, v104, v103, v103
	v_mul_f32_e32 v104, 0x3f4c422a, v104
	v_rcp_f32_e32 v100, v100
	v_add_f32_e32 v104, v104, v104
	v_mul_f32_e32 v104, 0x3fb8aa3b, v104
	v_exp_f32_e32 v104, v104
	ds_bpermute_b32 v106, v166, v124
	ds_bpermute_b32 v108, v166, v121
	v_fma_f32 v100, v100, -2.0, 1.0
	v_mul_f32_e32 v102, 0.5, v102
	v_add_f32_e32 v100, 1.0, v100
	v_mul_f32_e32 v100, v102, v100
	v_add_f32_e32 v102, 1.0, v104
	v_cndmask_b32_e64 v101, v101, v105, s[8:9]
	v_rcp_f32_e32 v102, v102
	s_waitcnt lgkmcnt(0)
	v_fmac_f32_e32 v108, v101, v106
	v_cndmask_b32_e64 v101, v101, v108, s[0:1]
	v_fmac_f32_e32 v114, v118, v101
	v_lshlrev_b32_e32 v101, 16, v233
	v_add_f32_e32 v101, v115, v101
	v_fma_f32 v102, v102, -2.0, 1.0
	v_mul_f32_e32 v100, v100, v101
	v_and_b32_e32 v101, 0xffff0000, v233
	v_mul_f32_e32 v103, 0.5, v103
	v_add_f32_e32 v102, 1.0, v102
	v_add_f32_e32 v101, v114, v101
	v_mul_f32_e32 v102, v103, v102
	v_mul_f32_e32 v101, v102, v101
	v_cvt_pk_bf16_f32 v102, v100, v101
	ds_read_b64 v[100:101], v116 offset:3840
	ds_write_b32 v190, v102 offset:3968
	s_add_i32 s34, s34, s35
	s_waitcnt lgkmcnt(1)
	v_lshlrev_b32_e32 v103, 16, v100
	v_exp_f32_e32 v103, v103
	v_and_b32_e32 v102, 0xffff0000, v100
	v_lshlrev_b32_e32 v100, 16, v101
	v_and_b32_e32 v105, 0xffff0000, v101
	v_fmac_f32_e32 v102, v115, v103
	v_lshlrev_b32_e32 v103, 16, v235
	v_mul_f32_e32 v104, 0x3d372713, v103
	v_mul_f32_e32 v104, v104, v103
	v_fma_f32 v104, v104, v103, v103
	v_mul_f32_e32 v104, 0x3f4c422a, v104
	v_add_f32_e32 v104, v104, v104
	v_mul_f32_e32 v104, 0x3fb8aa3b, v104
	v_exp_f32_e32 v104, v104
	v_mul_f32_e32 v103, 0.5, v103
	v_exp_f32_e32 v100, v100
	v_add_f32_e32 v101, 1.0, v104
	v_and_b32_e32 v104, 0xffff0000, v235
	v_mul_f32_e32 v106, 0x3d372713, v104
	v_mul_f32_e32 v106, v106, v104
	v_fma_f32 v106, v106, v104, v104
	v_mul_f32_e32 v106, 0x3f4c422a, v106
	v_rcp_f32_e32 v101, v101
	v_add_f32_e32 v106, v106, v106
	v_mul_f32_e32 v106, 0x3fb8aa3b, v106
	v_exp_f32_e32 v106, v106
	v_fma_f32 v101, v101, -2.0, 1.0
	v_add_f32_e32 v101, 1.0, v101
	v_mul_f32_e32 v101, v103, v101
	v_add_f32_e32 v103, 1.0, v106
	v_rcp_f32_e32 v103, v103
	v_fmac_f32_e32 v105, v114, v100
	v_lshlrev_b32_e32 v100, 16, v231
	v_add_f32_e32 v100, v102, v100
	v_fma_f32 v103, v103, -2.0, 1.0
	v_mul_f32_e32 v100, v101, v100
	v_and_b32_e32 v101, 0xffff0000, v231
	v_mul_f32_e32 v104, 0.5, v104
	v_add_f32_e32 v103, 1.0, v103
	v_add_f32_e32 v101, v105, v101
	v_mul_f32_e32 v103, v104, v103
	v_mul_f32_e32 v101, v103, v101
	v_cvt_pk_bf16_f32 v103, v100, v101
	ds_read_b64 v[100:101], v116 offset:3712
	ds_write_b32 v190, v103 offset:3840
	s_waitcnt lgkmcnt(1)
	v_lshlrev_b32_e32 v104, 16, v100
	v_exp_f32_e32 v104, v104
	v_and_b32_e32 v103, 0xffff0000, v100
	v_lshlrev_b32_e32 v100, 16, v101
	v_fmac_f32_e32 v103, v102, v104
	v_lshlrev_b32_e32 v102, 16, v234
	v_mul_f32_e32 v104, 0x3d372713, v102
	v_mul_f32_e32 v104, v104, v102
	v_fma_f32 v104, v104, v102, v102
	v_mul_f32_e32 v104, 0x3f4c422a, v104
	v_add_f32_e32 v104, v104, v104
	v_mul_f32_e32 v104, 0x3fb8aa3b, v104
	v_exp_f32_e32 v104, v104
	v_exp_f32_e32 v100, v100
	v_and_b32_e32 v106, 0xffff0000, v101
	v_mul_f32_e32 v102, 0.5, v102
	v_add_f32_e32 v101, 1.0, v104
	v_and_b32_e32 v104, 0xffff0000, v234
	v_fmac_f32_e32 v106, v105, v100
	v_mul_f32_e32 v105, 0x3d372713, v104
	v_mul_f32_e32 v105, v105, v104
	v_fma_f32 v105, v105, v104, v104
	v_mul_f32_e32 v105, 0x3f4c422a, v105
	v_rcp_f32_e32 v101, v101
	v_add_f32_e32 v105, v105, v105
	v_mul_f32_e32 v105, 0x3fb8aa3b, v105
	v_exp_f32_e32 v105, v105
	v_fma_f32 v101, v101, -2.0, 1.0
	v_add_f32_e32 v101, 1.0, v101
	v_mul_f32_e32 v101, v102, v101
	v_add_f32_e32 v102, 1.0, v105
	v_rcp_f32_e32 v102, v102
	v_lshlrev_b32_e32 v100, 16, v229
	v_add_f32_e32 v100, v103, v100
	v_mul_f32_e32 v100, v101, v100
	v_fma_f32 v102, v102, -2.0, 1.0
	v_and_b32_e32 v101, 0xffff0000, v229
	v_mul_f32_e32 v104, 0.5, v104
	v_add_f32_e32 v102, 1.0, v102
	v_add_f32_e32 v101, v106, v101
	v_mul_f32_e32 v102, v104, v102
	v_mul_f32_e32 v101, v102, v101
	v_cvt_pk_bf16_f32 v102, v100, v101
	ds_read_b64 v[100:101], v116 offset:3584
	ds_write_b32 v190, v102 offset:3712
	s_waitcnt lgkmcnt(1)
	v_lshlrev_b32_e32 v104, 16, v100
	v_exp_f32_e32 v104, v104
	v_and_b32_e32 v102, 0xffff0000, v100
	v_lshlrev_b32_e32 v100, 16, v101
	v_fmac_f32_e32 v102, v103, v104
	v_lshlrev_b32_e32 v103, 16, v232
	v_mul_f32_e32 v104, 0x3d372713, v103
	v_mul_f32_e32 v104, v104, v103
	v_fma_f32 v104, v104, v103, v103
	v_mul_f32_e32 v104, 0x3f4c422a, v104
	v_add_f32_e32 v104, v104, v104
	v_mul_f32_e32 v104, 0x3fb8aa3b, v104
	v_exp_f32_e32 v104, v104
	v_exp_f32_e32 v100, v100
	v_and_b32_e32 v105, 0xffff0000, v101
	v_mul_f32_e32 v103, 0.5, v103
	v_add_f32_e32 v101, 1.0, v104
	v_and_b32_e32 v104, 0xffff0000, v232
	v_fmac_f32_e32 v105, v106, v100
	v_mul_f32_e32 v106, 0x3d372713, v104
	v_mul_f32_e32 v106, v106, v104
	v_fma_f32 v106, v106, v104, v104
	v_mul_f32_e32 v106, 0x3f4c422a, v106
	v_rcp_f32_e32 v101, v101
	v_add_f32_e32 v106, v106, v106
	v_mul_f32_e32 v106, 0x3fb8aa3b, v106
	v_exp_f32_e32 v106, v106
	v_fma_f32 v101, v101, -2.0, 1.0
	v_add_f32_e32 v101, 1.0, v101
	v_mul_f32_e32 v101, v103, v101
	v_add_f32_e32 v103, 1.0, v106
	v_rcp_f32_e32 v103, v103
	v_lshlrev_b32_e32 v100, 16, v227
	v_add_f32_e32 v100, v102, v100
	v_mul_f32_e32 v100, v101, v100
	v_fma_f32 v103, v103, -2.0, 1.0
	v_and_b32_e32 v101, 0xffff0000, v227
	v_mul_f32_e32 v104, 0.5, v104
	v_add_f32_e32 v103, 1.0, v103
	v_add_f32_e32 v101, v105, v101
	v_mul_f32_e32 v103, v104, v103
	v_mul_f32_e32 v101, v103, v101
	v_cvt_pk_bf16_f32 v103, v100, v101
	ds_read_b64 v[100:101], v116 offset:3456
	ds_write_b32 v190, v103 offset:3584
	s_waitcnt lgkmcnt(1)
	v_lshlrev_b32_e32 v104, 16, v100
	v_exp_f32_e32 v104, v104
	v_and_b32_e32 v103, 0xffff0000, v100
	v_lshlrev_b32_e32 v100, 16, v101
	v_fmac_f32_e32 v103, v102, v104
	v_lshlrev_b32_e32 v102, 16, v230
	v_mul_f32_e32 v104, 0x3d372713, v102
	v_mul_f32_e32 v104, v104, v102
	v_fma_f32 v104, v104, v102, v102
	v_mul_f32_e32 v104, 0x3f4c422a, v104
	v_add_f32_e32 v104, v104, v104
	v_mul_f32_e32 v104, 0x3fb8aa3b, v104
	v_exp_f32_e32 v104, v104
	v_exp_f32_e32 v100, v100
	v_and_b32_e32 v106, 0xffff0000, v101
	v_mul_f32_e32 v102, 0.5, v102
	v_add_f32_e32 v101, 1.0, v104
	v_and_b32_e32 v104, 0xffff0000, v230
	v_fmac_f32_e32 v106, v105, v100
	v_mul_f32_e32 v105, 0x3d372713, v104
	v_mul_f32_e32 v105, v105, v104
	v_fma_f32 v105, v105, v104, v104
	v_mul_f32_e32 v105, 0x3f4c422a, v105
	v_rcp_f32_e32 v101, v101
	v_add_f32_e32 v105, v105, v105
	v_mul_f32_e32 v105, 0x3fb8aa3b, v105
	v_exp_f32_e32 v105, v105
	v_fma_f32 v101, v101, -2.0, 1.0
	v_add_f32_e32 v101, 1.0, v101
	v_mul_f32_e32 v101, v102, v101
	v_add_f32_e32 v102, 1.0, v105
	v_rcp_f32_e32 v102, v102
	v_lshlrev_b32_e32 v100, 16, v225
	v_add_f32_e32 v100, v103, v100
	v_mul_f32_e32 v100, v101, v100
	v_fma_f32 v102, v102, -2.0, 1.0
	v_and_b32_e32 v101, 0xffff0000, v225
	v_mul_f32_e32 v104, 0.5, v104
	v_add_f32_e32 v102, 1.0, v102
	v_add_f32_e32 v101, v106, v101
	v_mul_f32_e32 v102, v104, v102
	v_mul_f32_e32 v101, v102, v101
	v_cvt_pk_bf16_f32 v102, v100, v101
	ds_read_b64 v[100:101], v116 offset:3328
	ds_write_b32 v190, v102 offset:3456
	s_waitcnt lgkmcnt(1)
	v_lshlrev_b32_e32 v104, 16, v100
	v_exp_f32_e32 v104, v104
	v_and_b32_e32 v102, 0xffff0000, v100
	v_lshlrev_b32_e32 v100, 16, v101
	v_fmac_f32_e32 v102, v103, v104
	v_lshlrev_b32_e32 v103, 16, v228
	v_mul_f32_e32 v104, 0x3d372713, v103
	v_mul_f32_e32 v104, v104, v103
	v_fma_f32 v104, v104, v103, v103
	v_mul_f32_e32 v104, 0x3f4c422a, v104
	v_add_f32_e32 v104, v104, v104
	v_mul_f32_e32 v104, 0x3fb8aa3b, v104
	v_exp_f32_e32 v104, v104
	v_exp_f32_e32 v100, v100
	v_and_b32_e32 v105, 0xffff0000, v101
	v_mul_f32_e32 v103, 0.5, v103
	v_add_f32_e32 v101, 1.0, v104
	v_and_b32_e32 v104, 0xffff0000, v228
	v_fmac_f32_e32 v105, v106, v100
	v_mul_f32_e32 v106, 0x3d372713, v104
	v_mul_f32_e32 v106, v106, v104
	v_fma_f32 v106, v106, v104, v104
	v_mul_f32_e32 v106, 0x3f4c422a, v106
	v_rcp_f32_e32 v101, v101
	v_add_f32_e32 v106, v106, v106
	v_mul_f32_e32 v106, 0x3fb8aa3b, v106
	v_exp_f32_e32 v106, v106
	v_fma_f32 v101, v101, -2.0, 1.0
	v_add_f32_e32 v101, 1.0, v101
	v_mul_f32_e32 v101, v103, v101
	v_add_f32_e32 v103, 1.0, v106
	v_rcp_f32_e32 v103, v103
	v_lshlrev_b32_e32 v100, 16, v222
	v_add_f32_e32 v100, v102, v100
	v_mul_f32_e32 v100, v101, v100
	v_fma_f32 v103, v103, -2.0, 1.0
	v_and_b32_e32 v101, 0xffff0000, v222
	v_mul_f32_e32 v104, 0.5, v104
	v_add_f32_e32 v103, 1.0, v103
	v_add_f32_e32 v101, v105, v101
	v_mul_f32_e32 v103, v104, v103
	v_mul_f32_e32 v101, v103, v101
	v_cvt_pk_bf16_f32 v103, v100, v101
	ds_read_b64 v[100:101], v116 offset:3200
	ds_write_b32 v190, v103 offset:3328
	s_waitcnt lgkmcnt(1)
	v_lshlrev_b32_e32 v104, 16, v100
	v_exp_f32_e32 v104, v104
	v_and_b32_e32 v103, 0xffff0000, v100
	v_lshlrev_b32_e32 v100, 16, v101
	v_fmac_f32_e32 v103, v102, v104
	v_lshlrev_b32_e32 v102, 16, v226
	v_mul_f32_e32 v104, 0x3d372713, v102
	v_mul_f32_e32 v104, v104, v102
	v_fma_f32 v104, v104, v102, v102
	v_mul_f32_e32 v104, 0x3f4c422a, v104
	v_add_f32_e32 v104, v104, v104
	v_mul_f32_e32 v104, 0x3fb8aa3b, v104
	v_exp_f32_e32 v104, v104
	v_exp_f32_e32 v100, v100
	v_and_b32_e32 v106, 0xffff0000, v101
	v_mul_f32_e32 v102, 0.5, v102
	v_add_f32_e32 v101, 1.0, v104
	v_and_b32_e32 v104, 0xffff0000, v226
	v_fmac_f32_e32 v106, v105, v100
	v_mul_f32_e32 v105, 0x3d372713, v104
	v_mul_f32_e32 v105, v105, v104
	v_fma_f32 v105, v105, v104, v104
	v_mul_f32_e32 v105, 0x3f4c422a, v105
	v_rcp_f32_e32 v101, v101
	v_add_f32_e32 v105, v105, v105
	v_mul_f32_e32 v105, 0x3fb8aa3b, v105
	v_exp_f32_e32 v105, v105
	v_fma_f32 v101, v101, -2.0, 1.0
	v_add_f32_e32 v101, 1.0, v101
	v_mul_f32_e32 v101, v102, v101
	v_add_f32_e32 v102, 1.0, v105
	v_rcp_f32_e32 v102, v102
	v_lshlrev_b32_e32 v100, 16, v220
	v_add_f32_e32 v100, v103, v100
	v_mul_f32_e32 v100, v101, v100
	v_fma_f32 v102, v102, -2.0, 1.0
	v_and_b32_e32 v101, 0xffff0000, v220
	v_mul_f32_e32 v104, 0.5, v104
	v_add_f32_e32 v102, 1.0, v102
	v_add_f32_e32 v101, v106, v101
	v_mul_f32_e32 v102, v104, v102
	v_mul_f32_e32 v101, v102, v101
	v_cvt_pk_bf16_f32 v102, v100, v101
	ds_read_b64 v[100:101], v116 offset:3072
	ds_write_b32 v190, v102 offset:3200
	s_waitcnt lgkmcnt(1)
	v_lshlrev_b32_e32 v104, 16, v100
	v_exp_f32_e32 v104, v104
	v_and_b32_e32 v102, 0xffff0000, v100
	v_lshlrev_b32_e32 v100, 16, v101
	v_fmac_f32_e32 v102, v103, v104
	v_lshlrev_b32_e32 v103, 16, v224
	v_mul_f32_e32 v104, 0x3d372713, v103
	v_mul_f32_e32 v104, v104, v103
	v_fma_f32 v104, v104, v103, v103
	v_mul_f32_e32 v104, 0x3f4c422a, v104
	v_add_f32_e32 v104, v104, v104
	v_mul_f32_e32 v104, 0x3fb8aa3b, v104
	v_exp_f32_e32 v104, v104
	v_exp_f32_e32 v100, v100
	v_and_b32_e32 v105, 0xffff0000, v101
	v_mul_f32_e32 v103, 0.5, v103
	v_add_f32_e32 v101, 1.0, v104
	v_and_b32_e32 v104, 0xffff0000, v224
	v_fmac_f32_e32 v105, v106, v100
	v_mul_f32_e32 v106, 0x3d372713, v104
	v_mul_f32_e32 v106, v106, v104
	v_fma_f32 v106, v106, v104, v104
	v_mul_f32_e32 v106, 0x3f4c422a, v106
	v_rcp_f32_e32 v101, v101
	v_add_f32_e32 v106, v106, v106
	v_mul_f32_e32 v106, 0x3fb8aa3b, v106
	v_exp_f32_e32 v106, v106
	v_fma_f32 v101, v101, -2.0, 1.0
	v_add_f32_e32 v101, 1.0, v101
	v_mul_f32_e32 v101, v103, v101
	v_add_f32_e32 v103, 1.0, v106
	v_rcp_f32_e32 v103, v103
	v_lshlrev_b32_e32 v100, 16, v218
	v_add_f32_e32 v100, v102, v100
	v_mul_f32_e32 v100, v101, v100
	v_fma_f32 v103, v103, -2.0, 1.0
	v_and_b32_e32 v101, 0xffff0000, v218
	v_mul_f32_e32 v104, 0.5, v104
	v_add_f32_e32 v103, 1.0, v103
	v_add_f32_e32 v101, v105, v101
	v_mul_f32_e32 v103, v104, v103
	v_mul_f32_e32 v101, v103, v101
	v_cvt_pk_bf16_f32 v103, v100, v101
	ds_read_b64 v[100:101], v116 offset:2944
	ds_write_b32 v190, v103 offset:3072
	s_waitcnt lgkmcnt(1)
	v_lshlrev_b32_e32 v104, 16, v100
	v_exp_f32_e32 v104, v104
	v_and_b32_e32 v103, 0xffff0000, v100
	v_lshlrev_b32_e32 v100, 16, v101
	v_fmac_f32_e32 v103, v102, v104
	v_lshlrev_b32_e32 v102, 16, v223
	v_mul_f32_e32 v104, 0x3d372713, v102
	v_mul_f32_e32 v104, v104, v102
	v_fma_f32 v104, v104, v102, v102
	v_mul_f32_e32 v104, 0x3f4c422a, v104
	v_add_f32_e32 v104, v104, v104
	v_mul_f32_e32 v104, 0x3fb8aa3b, v104
	v_exp_f32_e32 v104, v104
	v_exp_f32_e32 v100, v100
	v_and_b32_e32 v106, 0xffff0000, v101
	v_mul_f32_e32 v102, 0.5, v102
	v_add_f32_e32 v101, 1.0, v104
	v_and_b32_e32 v104, 0xffff0000, v223
	v_fmac_f32_e32 v106, v105, v100
	v_mul_f32_e32 v105, 0x3d372713, v104
	v_mul_f32_e32 v105, v105, v104
	v_fma_f32 v105, v105, v104, v104
	v_mul_f32_e32 v105, 0x3f4c422a, v105
	v_rcp_f32_e32 v101, v101
	v_add_f32_e32 v105, v105, v105
	v_mul_f32_e32 v105, 0x3fb8aa3b, v105
	v_exp_f32_e32 v105, v105
	v_fma_f32 v101, v101, -2.0, 1.0
	v_add_f32_e32 v101, 1.0, v101
	v_mul_f32_e32 v101, v102, v101
	v_add_f32_e32 v102, 1.0, v105
	v_rcp_f32_e32 v102, v102
	v_lshlrev_b32_e32 v100, 16, v216
	v_add_f32_e32 v100, v103, v100
	v_mul_f32_e32 v100, v101, v100
	v_fma_f32 v102, v102, -2.0, 1.0
	v_and_b32_e32 v101, 0xffff0000, v216
	v_mul_f32_e32 v104, 0.5, v104
	v_add_f32_e32 v102, 1.0, v102
	v_add_f32_e32 v101, v106, v101
	v_mul_f32_e32 v102, v104, v102
	v_mul_f32_e32 v101, v102, v101
	v_cvt_pk_bf16_f32 v102, v100, v101
	ds_read_b64 v[100:101], v116 offset:2816
	ds_write_b32 v190, v102 offset:2944
	s_waitcnt lgkmcnt(1)
	v_lshlrev_b32_e32 v104, 16, v100
	v_exp_f32_e32 v104, v104
	v_and_b32_e32 v102, 0xffff0000, v100
	v_lshlrev_b32_e32 v100, 16, v101
	v_fmac_f32_e32 v102, v103, v104
	v_lshlrev_b32_e32 v103, 16, v221
	v_mul_f32_e32 v104, 0x3d372713, v103
	v_mul_f32_e32 v104, v104, v103
	v_fma_f32 v104, v104, v103, v103
	v_mul_f32_e32 v104, 0x3f4c422a, v104
	v_add_f32_e32 v104, v104, v104
	v_mul_f32_e32 v104, 0x3fb8aa3b, v104
	v_exp_f32_e32 v104, v104
	v_exp_f32_e32 v100, v100
	v_and_b32_e32 v105, 0xffff0000, v101
	v_mul_f32_e32 v103, 0.5, v103
	v_add_f32_e32 v101, 1.0, v104
	v_and_b32_e32 v104, 0xffff0000, v221
	v_fmac_f32_e32 v105, v106, v100
	v_mul_f32_e32 v106, 0x3d372713, v104
	v_mul_f32_e32 v106, v106, v104
	v_fma_f32 v106, v106, v104, v104
	v_mul_f32_e32 v106, 0x3f4c422a, v106
	v_rcp_f32_e32 v101, v101
	v_add_f32_e32 v106, v106, v106
	v_mul_f32_e32 v106, 0x3fb8aa3b, v106
	v_exp_f32_e32 v106, v106
	v_fma_f32 v101, v101, -2.0, 1.0
	v_add_f32_e32 v101, 1.0, v101
	v_mul_f32_e32 v101, v103, v101
	v_add_f32_e32 v103, 1.0, v106
	v_rcp_f32_e32 v103, v103
	v_lshlrev_b32_e32 v100, 16, v214
	v_add_f32_e32 v100, v102, v100
	v_mul_f32_e32 v100, v101, v100
	v_fma_f32 v103, v103, -2.0, 1.0
	v_and_b32_e32 v101, 0xffff0000, v214
	v_mul_f32_e32 v104, 0.5, v104
	v_add_f32_e32 v103, 1.0, v103
	v_add_f32_e32 v101, v105, v101
	v_mul_f32_e32 v103, v104, v103
	v_mul_f32_e32 v101, v103, v101
	v_cvt_pk_bf16_f32 v103, v100, v101
	ds_read_b64 v[100:101], v116 offset:2688
	ds_write_b32 v190, v103 offset:2816
	s_waitcnt lgkmcnt(1)
	v_lshlrev_b32_e32 v104, 16, v100
	v_exp_f32_e32 v104, v104
	v_and_b32_e32 v103, 0xffff0000, v100
	v_lshlrev_b32_e32 v100, 16, v101
	v_fmac_f32_e32 v103, v102, v104
	v_lshlrev_b32_e32 v102, 16, v219
	v_mul_f32_e32 v104, 0x3d372713, v102
	v_mul_f32_e32 v104, v104, v102
	v_fma_f32 v104, v104, v102, v102
	v_mul_f32_e32 v104, 0x3f4c422a, v104
	v_add_f32_e32 v104, v104, v104
	v_mul_f32_e32 v104, 0x3fb8aa3b, v104
	v_exp_f32_e32 v104, v104
	v_exp_f32_e32 v100, v100
	v_and_b32_e32 v106, 0xffff0000, v101
	v_mul_f32_e32 v102, 0.5, v102
	v_add_f32_e32 v101, 1.0, v104
	v_and_b32_e32 v104, 0xffff0000, v219
	v_fmac_f32_e32 v106, v105, v100
	v_mul_f32_e32 v105, 0x3d372713, v104
	v_mul_f32_e32 v105, v105, v104
	v_fma_f32 v105, v105, v104, v104
	v_mul_f32_e32 v105, 0x3f4c422a, v105
	v_rcp_f32_e32 v101, v101
	v_add_f32_e32 v105, v105, v105
	v_mul_f32_e32 v105, 0x3fb8aa3b, v105
	v_exp_f32_e32 v105, v105
	v_fma_f32 v101, v101, -2.0, 1.0
	v_add_f32_e32 v101, 1.0, v101
	v_mul_f32_e32 v101, v102, v101
	v_add_f32_e32 v102, 1.0, v105
	v_rcp_f32_e32 v102, v102
	v_lshlrev_b32_e32 v100, 16, v211
	v_add_f32_e32 v100, v103, v100
	v_mul_f32_e32 v100, v101, v100
	v_fma_f32 v102, v102, -2.0, 1.0
	v_and_b32_e32 v101, 0xffff0000, v211
	v_mul_f32_e32 v104, 0.5, v104
	v_add_f32_e32 v102, 1.0, v102
	v_add_f32_e32 v101, v106, v101
	v_mul_f32_e32 v102, v104, v102
	v_mul_f32_e32 v101, v102, v101
	v_cvt_pk_bf16_f32 v102, v100, v101
	ds_read_b64 v[100:101], v116 offset:2560
	ds_write_b32 v190, v102 offset:2688
	s_waitcnt lgkmcnt(1)
	v_lshlrev_b32_e32 v104, 16, v100
	v_exp_f32_e32 v104, v104
	v_and_b32_e32 v102, 0xffff0000, v100
	v_lshlrev_b32_e32 v100, 16, v101
	v_fmac_f32_e32 v102, v103, v104
	v_lshlrev_b32_e32 v103, 16, v217
	v_mul_f32_e32 v104, 0x3d372713, v103
	v_mul_f32_e32 v104, v104, v103
	v_fma_f32 v104, v104, v103, v103
	v_mul_f32_e32 v104, 0x3f4c422a, v104
	v_add_f32_e32 v104, v104, v104
	v_mul_f32_e32 v104, 0x3fb8aa3b, v104
	v_exp_f32_e32 v104, v104
	v_exp_f32_e32 v100, v100
	v_and_b32_e32 v105, 0xffff0000, v101
	v_mul_f32_e32 v103, 0.5, v103
	v_add_f32_e32 v101, 1.0, v104
	v_and_b32_e32 v104, 0xffff0000, v217
	v_fmac_f32_e32 v105, v106, v100
	v_mul_f32_e32 v106, 0x3d372713, v104
	v_mul_f32_e32 v106, v106, v104
	v_fma_f32 v106, v106, v104, v104
	v_mul_f32_e32 v106, 0x3f4c422a, v106
	v_rcp_f32_e32 v101, v101
	v_add_f32_e32 v106, v106, v106
	v_mul_f32_e32 v106, 0x3fb8aa3b, v106
	v_exp_f32_e32 v106, v106
	v_fma_f32 v101, v101, -2.0, 1.0
	v_add_f32_e32 v101, 1.0, v101
	v_mul_f32_e32 v101, v103, v101
	v_add_f32_e32 v103, 1.0, v106
	v_rcp_f32_e32 v103, v103
	v_lshlrev_b32_e32 v100, 16, v209
	v_add_f32_e32 v100, v102, v100
	v_mul_f32_e32 v100, v101, v100
	v_fma_f32 v103, v103, -2.0, 1.0
	v_and_b32_e32 v101, 0xffff0000, v209
	v_mul_f32_e32 v104, 0.5, v104
	v_add_f32_e32 v103, 1.0, v103
	v_add_f32_e32 v101, v105, v101
	v_mul_f32_e32 v103, v104, v103
	v_mul_f32_e32 v101, v103, v101
	v_cvt_pk_bf16_f32 v103, v100, v101
	ds_read_b64 v[100:101], v116 offset:2432
	ds_write_b32 v190, v103 offset:2560
	s_waitcnt lgkmcnt(1)
	v_lshlrev_b32_e32 v104, 16, v100
	v_exp_f32_e32 v104, v104
	v_and_b32_e32 v103, 0xffff0000, v100
	v_lshlrev_b32_e32 v100, 16, v101
	v_fmac_f32_e32 v103, v102, v104
	v_lshlrev_b32_e32 v102, 16, v215
	v_mul_f32_e32 v104, 0x3d372713, v102
	v_mul_f32_e32 v104, v104, v102
	v_fma_f32 v104, v104, v102, v102
	v_mul_f32_e32 v104, 0x3f4c422a, v104
	v_add_f32_e32 v104, v104, v104
	v_mul_f32_e32 v104, 0x3fb8aa3b, v104
	v_exp_f32_e32 v104, v104
	v_exp_f32_e32 v100, v100
	v_and_b32_e32 v106, 0xffff0000, v101
	v_mul_f32_e32 v102, 0.5, v102
	v_add_f32_e32 v101, 1.0, v104
	v_and_b32_e32 v104, 0xffff0000, v215
	v_fmac_f32_e32 v106, v105, v100
	v_mul_f32_e32 v105, 0x3d372713, v104
	v_mul_f32_e32 v105, v105, v104
	v_fma_f32 v105, v105, v104, v104
	v_mul_f32_e32 v105, 0x3f4c422a, v105
	v_rcp_f32_e32 v101, v101
	v_add_f32_e32 v105, v105, v105
	v_mul_f32_e32 v105, 0x3fb8aa3b, v105
	v_exp_f32_e32 v105, v105
	v_fma_f32 v101, v101, -2.0, 1.0
	v_add_f32_e32 v101, 1.0, v101
	v_mul_f32_e32 v101, v102, v101
	v_add_f32_e32 v102, 1.0, v105
	v_rcp_f32_e32 v102, v102
	v_lshlrev_b32_e32 v100, 16, v207
	v_add_f32_e32 v100, v103, v100
	v_mul_f32_e32 v100, v101, v100
	v_fma_f32 v102, v102, -2.0, 1.0
	v_and_b32_e32 v101, 0xffff0000, v207
	v_mul_f32_e32 v104, 0.5, v104
	v_add_f32_e32 v102, 1.0, v102
	v_add_f32_e32 v101, v106, v101
	v_mul_f32_e32 v102, v104, v102
	v_mul_f32_e32 v101, v102, v101
	v_cvt_pk_bf16_f32 v102, v100, v101
	ds_read_b64 v[100:101], v116 offset:2304
	ds_write_b32 v190, v102 offset:2432
	s_waitcnt lgkmcnt(1)
	v_lshlrev_b32_e32 v104, 16, v100
	v_exp_f32_e32 v104, v104
	v_and_b32_e32 v102, 0xffff0000, v100
	v_lshlrev_b32_e32 v100, 16, v101
	v_fmac_f32_e32 v102, v103, v104
	v_lshlrev_b32_e32 v103, 16, v213
	v_mul_f32_e32 v104, 0x3d372713, v103
	v_mul_f32_e32 v104, v104, v103
	v_fma_f32 v104, v104, v103, v103
	v_mul_f32_e32 v104, 0x3f4c422a, v104
	v_add_f32_e32 v104, v104, v104
	v_mul_f32_e32 v104, 0x3fb8aa3b, v104
	v_exp_f32_e32 v104, v104
	v_exp_f32_e32 v100, v100
	v_and_b32_e32 v105, 0xffff0000, v101
	v_mul_f32_e32 v103, 0.5, v103
	v_add_f32_e32 v101, 1.0, v104
	v_and_b32_e32 v104, 0xffff0000, v213
	v_fmac_f32_e32 v105, v106, v100
	v_mul_f32_e32 v106, 0x3d372713, v104
	v_mul_f32_e32 v106, v106, v104
	v_fma_f32 v106, v106, v104, v104
	v_mul_f32_e32 v106, 0x3f4c422a, v106
	v_rcp_f32_e32 v101, v101
	v_add_f32_e32 v106, v106, v106
	v_mul_f32_e32 v106, 0x3fb8aa3b, v106
	v_exp_f32_e32 v106, v106
	v_fma_f32 v101, v101, -2.0, 1.0
	v_add_f32_e32 v101, 1.0, v101
	v_mul_f32_e32 v101, v103, v101
	v_add_f32_e32 v103, 1.0, v106
	v_rcp_f32_e32 v103, v103
	v_lshlrev_b32_e32 v100, 16, v205
	v_add_f32_e32 v100, v102, v100
	v_mul_f32_e32 v100, v101, v100
	v_fma_f32 v103, v103, -2.0, 1.0
	v_and_b32_e32 v101, 0xffff0000, v205
	v_mul_f32_e32 v104, 0.5, v104
	v_add_f32_e32 v103, 1.0, v103
	v_add_f32_e32 v101, v105, v101
	v_mul_f32_e32 v103, v104, v103
	v_mul_f32_e32 v101, v103, v101
	v_cvt_pk_bf16_f32 v103, v100, v101
	ds_read_b64 v[100:101], v116 offset:2176
	ds_write_b32 v190, v103 offset:2304
	s_waitcnt lgkmcnt(1)
	v_lshlrev_b32_e32 v104, 16, v100
	v_exp_f32_e32 v104, v104
	v_and_b32_e32 v103, 0xffff0000, v100
	v_lshlrev_b32_e32 v100, 16, v101
	v_fmac_f32_e32 v103, v102, v104
	v_lshlrev_b32_e32 v102, 16, v212
	v_mul_f32_e32 v104, 0x3d372713, v102
	v_mul_f32_e32 v104, v104, v102
	v_fma_f32 v104, v104, v102, v102
	v_mul_f32_e32 v104, 0x3f4c422a, v104
	v_add_f32_e32 v104, v104, v104
	v_mul_f32_e32 v104, 0x3fb8aa3b, v104
	v_exp_f32_e32 v104, v104
	v_exp_f32_e32 v100, v100
	v_and_b32_e32 v106, 0xffff0000, v101
	v_mul_f32_e32 v102, 0.5, v102
	v_add_f32_e32 v101, 1.0, v104
	v_and_b32_e32 v104, 0xffff0000, v212
	v_fmac_f32_e32 v106, v105, v100
	v_mul_f32_e32 v105, 0x3d372713, v104
	v_mul_f32_e32 v105, v105, v104
	v_fma_f32 v105, v105, v104, v104
	v_mul_f32_e32 v105, 0x3f4c422a, v105
	v_rcp_f32_e32 v101, v101
	v_add_f32_e32 v105, v105, v105
	v_mul_f32_e32 v105, 0x3fb8aa3b, v105
	v_exp_f32_e32 v105, v105
	v_fma_f32 v101, v101, -2.0, 1.0
	v_add_f32_e32 v101, 1.0, v101
	v_mul_f32_e32 v101, v102, v101
	v_add_f32_e32 v102, 1.0, v105
	v_rcp_f32_e32 v102, v102
	v_lshlrev_b32_e32 v100, 16, v203
	v_add_f32_e32 v100, v103, v100
	v_mul_f32_e32 v100, v101, v100
	v_fma_f32 v102, v102, -2.0, 1.0
	v_and_b32_e32 v101, 0xffff0000, v203
	v_mul_f32_e32 v104, 0.5, v104
	v_add_f32_e32 v102, 1.0, v102
	v_add_f32_e32 v101, v106, v101
	v_mul_f32_e32 v102, v104, v102
	v_mul_f32_e32 v101, v102, v101
	v_cvt_pk_bf16_f32 v102, v100, v101
	ds_read_b64 v[100:101], v116 offset:2048
	ds_write_b32 v190, v102 offset:2176
	s_waitcnt lgkmcnt(1)
	v_lshlrev_b32_e32 v104, 16, v100
	v_exp_f32_e32 v104, v104
	v_and_b32_e32 v102, 0xffff0000, v100
	v_lshlrev_b32_e32 v100, 16, v101
	v_fmac_f32_e32 v102, v103, v104
	v_lshlrev_b32_e32 v103, 16, v210
	v_mul_f32_e32 v104, 0x3d372713, v103
	v_mul_f32_e32 v104, v104, v103
	v_fma_f32 v104, v104, v103, v103
	v_mul_f32_e32 v104, 0x3f4c422a, v104
	v_add_f32_e32 v104, v104, v104
	v_mul_f32_e32 v104, 0x3fb8aa3b, v104
	v_exp_f32_e32 v104, v104
	v_exp_f32_e32 v100, v100
	v_and_b32_e32 v105, 0xffff0000, v101
	v_mul_f32_e32 v103, 0.5, v103
	v_add_f32_e32 v101, 1.0, v104
	v_and_b32_e32 v104, 0xffff0000, v210
	v_fmac_f32_e32 v105, v106, v100
	v_mul_f32_e32 v106, 0x3d372713, v104
	v_mul_f32_e32 v106, v106, v104
	v_fma_f32 v106, v106, v104, v104
	v_mul_f32_e32 v106, 0x3f4c422a, v106
	v_rcp_f32_e32 v101, v101
	v_add_f32_e32 v106, v106, v106
	v_mul_f32_e32 v106, 0x3fb8aa3b, v106
	v_exp_f32_e32 v106, v106
	v_fma_f32 v101, v101, -2.0, 1.0
	v_add_f32_e32 v101, 1.0, v101
	v_mul_f32_e32 v101, v103, v101
	v_add_f32_e32 v103, 1.0, v106
	v_rcp_f32_e32 v103, v103
	v_lshlrev_b32_e32 v100, 16, v201
	v_add_f32_e32 v100, v102, v100
	v_mul_f32_e32 v100, v101, v100
	v_fma_f32 v103, v103, -2.0, 1.0
	v_and_b32_e32 v101, 0xffff0000, v201
	v_mul_f32_e32 v104, 0.5, v104
	v_add_f32_e32 v103, 1.0, v103
	v_add_f32_e32 v101, v105, v101
	v_mul_f32_e32 v103, v104, v103
	v_mul_f32_e32 v101, v103, v101
	v_cvt_pk_bf16_f32 v103, v100, v101
	ds_read_b64 v[100:101], v116 offset:1920
	ds_write_b32 v190, v103 offset:2048
	s_waitcnt lgkmcnt(1)
	v_lshlrev_b32_e32 v104, 16, v100
	v_exp_f32_e32 v104, v104
	v_and_b32_e32 v103, 0xffff0000, v100
	v_lshlrev_b32_e32 v100, 16, v101
	v_fmac_f32_e32 v103, v102, v104
	v_lshlrev_b32_e32 v102, 16, v208
	v_mul_f32_e32 v104, 0x3d372713, v102
	v_mul_f32_e32 v104, v104, v102
	v_fma_f32 v104, v104, v102, v102
	v_mul_f32_e32 v104, 0x3f4c422a, v104
	v_add_f32_e32 v104, v104, v104
	v_mul_f32_e32 v104, 0x3fb8aa3b, v104
	v_exp_f32_e32 v104, v104
	v_exp_f32_e32 v100, v100
	v_and_b32_e32 v106, 0xffff0000, v101
	v_mul_f32_e32 v102, 0.5, v102
	v_add_f32_e32 v101, 1.0, v104
	v_and_b32_e32 v104, 0xffff0000, v208
	v_fmac_f32_e32 v106, v105, v100
	v_mul_f32_e32 v105, 0x3d372713, v104
	v_mul_f32_e32 v105, v105, v104
	v_fma_f32 v105, v105, v104, v104
	v_mul_f32_e32 v105, 0x3f4c422a, v105
	v_rcp_f32_e32 v101, v101
	v_add_f32_e32 v105, v105, v105
	v_mul_f32_e32 v105, 0x3fb8aa3b, v105
	v_exp_f32_e32 v105, v105
	v_fma_f32 v101, v101, -2.0, 1.0
	v_add_f32_e32 v101, 1.0, v101
	v_mul_f32_e32 v101, v102, v101
	v_add_f32_e32 v102, 1.0, v105
	v_rcp_f32_e32 v102, v102
	v_lshlrev_b32_e32 v100, 16, v198
	v_add_f32_e32 v100, v103, v100
	v_mul_f32_e32 v100, v101, v100
	v_fma_f32 v102, v102, -2.0, 1.0
	v_and_b32_e32 v101, 0xffff0000, v198
	v_mul_f32_e32 v104, 0.5, v104
	v_add_f32_e32 v102, 1.0, v102
	v_add_f32_e32 v101, v106, v101
	v_mul_f32_e32 v102, v104, v102
	v_mul_f32_e32 v101, v102, v101
	v_cvt_pk_bf16_f32 v102, v100, v101
	ds_read_b64 v[100:101], v116 offset:1792
	ds_write_b32 v190, v102 offset:1920
	s_waitcnt lgkmcnt(1)
	v_lshlrev_b32_e32 v104, 16, v100
	v_exp_f32_e32 v104, v104
	v_and_b32_e32 v102, 0xffff0000, v100
	v_lshlrev_b32_e32 v100, 16, v101
	v_fmac_f32_e32 v102, v103, v104
	v_lshlrev_b32_e32 v103, 16, v206
	v_mul_f32_e32 v104, 0x3d372713, v103
	v_mul_f32_e32 v104, v104, v103
	v_fma_f32 v104, v104, v103, v103
	v_mul_f32_e32 v104, 0x3f4c422a, v104
	v_add_f32_e32 v104, v104, v104
	v_mul_f32_e32 v104, 0x3fb8aa3b, v104
	v_exp_f32_e32 v104, v104
	v_exp_f32_e32 v100, v100
	v_and_b32_e32 v105, 0xffff0000, v101
	v_mul_f32_e32 v103, 0.5, v103
	v_add_f32_e32 v101, 1.0, v104
	v_and_b32_e32 v104, 0xffff0000, v206
	v_fmac_f32_e32 v105, v106, v100
	v_mul_f32_e32 v106, 0x3d372713, v104
	v_mul_f32_e32 v106, v106, v104
	v_fma_f32 v106, v106, v104, v104
	v_mul_f32_e32 v106, 0x3f4c422a, v106
	v_rcp_f32_e32 v101, v101
	v_add_f32_e32 v106, v106, v106
	v_mul_f32_e32 v106, 0x3fb8aa3b, v106
	v_exp_f32_e32 v106, v106
	v_fma_f32 v101, v101, -2.0, 1.0
	v_add_f32_e32 v101, 1.0, v101
	v_mul_f32_e32 v101, v103, v101
	v_add_f32_e32 v103, 1.0, v106
	v_rcp_f32_e32 v103, v103
	v_lshlrev_b32_e32 v100, 16, v196
	v_add_f32_e32 v100, v102, v100
	v_mul_f32_e32 v100, v101, v100
	v_fma_f32 v103, v103, -2.0, 1.0
	v_and_b32_e32 v101, 0xffff0000, v196
	v_mul_f32_e32 v104, 0.5, v104
	v_add_f32_e32 v103, 1.0, v103
	v_add_f32_e32 v101, v105, v101
	v_mul_f32_e32 v103, v104, v103
	v_mul_f32_e32 v101, v103, v101
	v_cvt_pk_bf16_f32 v103, v100, v101
	ds_read_b64 v[100:101], v116 offset:1664
	ds_write_b32 v190, v103 offset:1792
	s_waitcnt lgkmcnt(1)
	v_lshlrev_b32_e32 v104, 16, v100
	v_exp_f32_e32 v104, v104
	v_and_b32_e32 v103, 0xffff0000, v100
	v_lshlrev_b32_e32 v100, 16, v101
	v_fmac_f32_e32 v103, v102, v104
	v_lshlrev_b32_e32 v102, 16, v204
	v_mul_f32_e32 v104, 0x3d372713, v102
	v_mul_f32_e32 v104, v104, v102
	v_fma_f32 v104, v104, v102, v102
	v_mul_f32_e32 v104, 0x3f4c422a, v104
	v_add_f32_e32 v104, v104, v104
	v_mul_f32_e32 v104, 0x3fb8aa3b, v104
	v_exp_f32_e32 v104, v104
	v_exp_f32_e32 v100, v100
	v_and_b32_e32 v106, 0xffff0000, v101
	v_mul_f32_e32 v102, 0.5, v102
	v_add_f32_e32 v101, 1.0, v104
	v_and_b32_e32 v104, 0xffff0000, v204
	v_fmac_f32_e32 v106, v105, v100
	v_mul_f32_e32 v105, 0x3d372713, v104
	v_mul_f32_e32 v105, v105, v104
	v_fma_f32 v105, v105, v104, v104
	v_mul_f32_e32 v105, 0x3f4c422a, v105
	v_rcp_f32_e32 v101, v101
	v_add_f32_e32 v105, v105, v105
	v_mul_f32_e32 v105, 0x3fb8aa3b, v105
	v_exp_f32_e32 v105, v105
	v_fma_f32 v101, v101, -2.0, 1.0
	v_add_f32_e32 v101, 1.0, v101
	v_mul_f32_e32 v101, v102, v101
	v_add_f32_e32 v102, 1.0, v105
	v_rcp_f32_e32 v102, v102
	v_lshlrev_b32_e32 v100, 16, v194
	v_add_f32_e32 v100, v103, v100
	v_mul_f32_e32 v100, v101, v100
	v_fma_f32 v102, v102, -2.0, 1.0
	v_and_b32_e32 v101, 0xffff0000, v194
	v_mul_f32_e32 v104, 0.5, v104
	v_add_f32_e32 v102, 1.0, v102
	v_add_f32_e32 v101, v106, v101
	v_mul_f32_e32 v102, v104, v102
	v_mul_f32_e32 v101, v102, v101
	v_cvt_pk_bf16_f32 v102, v100, v101
	ds_read_b64 v[100:101], v116 offset:1536
	ds_write_b32 v190, v102 offset:1664
	s_waitcnt lgkmcnt(1)
	v_lshlrev_b32_e32 v104, 16, v100
	v_exp_f32_e32 v104, v104
	v_and_b32_e32 v102, 0xffff0000, v100
	v_lshlrev_b32_e32 v100, 16, v101
	v_fmac_f32_e32 v102, v103, v104
	v_lshlrev_b32_e32 v103, 16, v202
	v_mul_f32_e32 v104, 0x3d372713, v103
	v_mul_f32_e32 v104, v104, v103
	v_fma_f32 v104, v104, v103, v103
	v_mul_f32_e32 v104, 0x3f4c422a, v104
	v_add_f32_e32 v104, v104, v104
	v_mul_f32_e32 v104, 0x3fb8aa3b, v104
	v_exp_f32_e32 v104, v104
	v_exp_f32_e32 v100, v100
	v_and_b32_e32 v105, 0xffff0000, v101
	v_mul_f32_e32 v103, 0.5, v103
	v_add_f32_e32 v101, 1.0, v104
	v_and_b32_e32 v104, 0xffff0000, v202
	v_fmac_f32_e32 v105, v106, v100
	v_mul_f32_e32 v106, 0x3d372713, v104
	v_mul_f32_e32 v106, v106, v104
	v_fma_f32 v106, v106, v104, v104
	v_mul_f32_e32 v106, 0x3f4c422a, v106
	v_rcp_f32_e32 v101, v101
	v_add_f32_e32 v106, v106, v106
	v_mul_f32_e32 v106, 0x3fb8aa3b, v106
	v_exp_f32_e32 v106, v106
	v_fma_f32 v101, v101, -2.0, 1.0
	v_add_f32_e32 v101, 1.0, v101
	v_mul_f32_e32 v101, v103, v101
	v_add_f32_e32 v103, 1.0, v106
	v_rcp_f32_e32 v103, v103
	v_lshlrev_b32_e32 v100, 16, v157
	v_add_f32_e32 v100, v102, v100
	v_mul_f32_e32 v100, v101, v100
	v_fma_f32 v103, v103, -2.0, 1.0
	v_and_b32_e32 v101, 0xffff0000, v157
	v_mul_f32_e32 v104, 0.5, v104
	v_add_f32_e32 v103, 1.0, v103
	v_add_f32_e32 v101, v105, v101
	v_mul_f32_e32 v103, v104, v103
	v_mul_f32_e32 v101, v103, v101
	v_cvt_pk_bf16_f32 v103, v100, v101
	ds_read_b64 v[100:101], v116 offset:1408
	ds_write_b32 v190, v103 offset:1536
	s_waitcnt lgkmcnt(1)
	v_lshlrev_b32_e32 v104, 16, v100
	v_exp_f32_e32 v104, v104
	v_and_b32_e32 v103, 0xffff0000, v100
	v_lshlrev_b32_e32 v100, 16, v101
	v_fmac_f32_e32 v103, v102, v104
	v_lshlrev_b32_e32 v102, 16, v200
	v_mul_f32_e32 v104, 0x3d372713, v102
	v_mul_f32_e32 v104, v104, v102
	v_fma_f32 v104, v104, v102, v102
	v_mul_f32_e32 v104, 0x3f4c422a, v104
	v_add_f32_e32 v104, v104, v104
	v_mul_f32_e32 v104, 0x3fb8aa3b, v104
	v_exp_f32_e32 v104, v104
	v_exp_f32_e32 v100, v100
	v_and_b32_e32 v106, 0xffff0000, v101
	v_mul_f32_e32 v102, 0.5, v102
	v_add_f32_e32 v101, 1.0, v104
	v_and_b32_e32 v104, 0xffff0000, v200
	v_fmac_f32_e32 v106, v105, v100
	v_mul_f32_e32 v105, 0x3d372713, v104
	v_mul_f32_e32 v105, v105, v104
	v_fma_f32 v105, v105, v104, v104
	v_mul_f32_e32 v105, 0x3f4c422a, v105
	v_rcp_f32_e32 v101, v101
	v_add_f32_e32 v105, v105, v105
	v_mul_f32_e32 v105, 0x3fb8aa3b, v105
	v_exp_f32_e32 v105, v105
	v_fma_f32 v101, v101, -2.0, 1.0
	v_add_f32_e32 v101, 1.0, v101
	v_mul_f32_e32 v101, v102, v101
	v_add_f32_e32 v102, 1.0, v105
	v_rcp_f32_e32 v102, v102
	v_lshlrev_b32_e32 v100, 16, v155
	v_add_f32_e32 v100, v103, v100
	v_mul_f32_e32 v100, v101, v100
	v_fma_f32 v102, v102, -2.0, 1.0
	v_and_b32_e32 v101, 0xffff0000, v155
	v_mul_f32_e32 v104, 0.5, v104
	v_add_f32_e32 v102, 1.0, v102
	v_add_f32_e32 v101, v106, v101
	v_mul_f32_e32 v102, v104, v102
	v_mul_f32_e32 v101, v102, v101
	v_cvt_pk_bf16_f32 v102, v100, v101
	ds_read_b64 v[100:101], v116 offset:1280
	ds_write_b32 v190, v102 offset:1408
	s_waitcnt lgkmcnt(1)
	v_lshlrev_b32_e32 v104, 16, v100
	v_exp_f32_e32 v104, v104
	v_and_b32_e32 v102, 0xffff0000, v100
	v_lshlrev_b32_e32 v100, 16, v101
	v_fmac_f32_e32 v102, v103, v104
	v_lshlrev_b32_e32 v103, 16, v199
	v_mul_f32_e32 v104, 0x3d372713, v103
	v_mul_f32_e32 v104, v104, v103
	v_fma_f32 v104, v104, v103, v103
	v_mul_f32_e32 v104, 0x3f4c422a, v104
	v_add_f32_e32 v104, v104, v104
	v_mul_f32_e32 v104, 0x3fb8aa3b, v104
	v_exp_f32_e32 v104, v104
	v_exp_f32_e32 v100, v100
	v_and_b32_e32 v105, 0xffff0000, v101
	v_mul_f32_e32 v103, 0.5, v103
	v_add_f32_e32 v101, 1.0, v104
	v_and_b32_e32 v104, 0xffff0000, v199
	v_fmac_f32_e32 v105, v106, v100
	v_mul_f32_e32 v106, 0x3d372713, v104
	v_mul_f32_e32 v106, v106, v104
	v_fma_f32 v106, v106, v104, v104
	v_mul_f32_e32 v106, 0x3f4c422a, v106
	v_rcp_f32_e32 v101, v101
	v_add_f32_e32 v106, v106, v106
	v_mul_f32_e32 v106, 0x3fb8aa3b, v106
	v_exp_f32_e32 v106, v106
	v_fma_f32 v101, v101, -2.0, 1.0
	v_add_f32_e32 v101, 1.0, v101
	v_mul_f32_e32 v101, v103, v101
	v_add_f32_e32 v103, 1.0, v106
	v_rcp_f32_e32 v103, v103
	v_lshlrev_b32_e32 v100, 16, v152
	v_add_f32_e32 v100, v102, v100
	v_mul_f32_e32 v100, v101, v100
	v_fma_f32 v103, v103, -2.0, 1.0
	v_and_b32_e32 v101, 0xffff0000, v152
	v_mul_f32_e32 v104, 0.5, v104
	v_add_f32_e32 v103, 1.0, v103
	v_add_f32_e32 v101, v105, v101
	v_mul_f32_e32 v103, v104, v103
	v_mul_f32_e32 v101, v103, v101
	v_cvt_pk_bf16_f32 v103, v100, v101
	ds_read_b64 v[100:101], v116 offset:1152
	ds_write_b32 v190, v103 offset:1280
	s_waitcnt lgkmcnt(1)
	v_lshlrev_b32_e32 v104, 16, v100
	v_exp_f32_e32 v104, v104
	v_and_b32_e32 v103, 0xffff0000, v100
	v_lshlrev_b32_e32 v100, 16, v101
	v_fmac_f32_e32 v103, v102, v104
	v_lshlrev_b32_e32 v102, 16, v197
	v_mul_f32_e32 v104, 0x3d372713, v102
	v_mul_f32_e32 v104, v104, v102
	v_fma_f32 v104, v104, v102, v102
	v_mul_f32_e32 v104, 0x3f4c422a, v104
	v_add_f32_e32 v104, v104, v104
	v_mul_f32_e32 v104, 0x3fb8aa3b, v104
	v_exp_f32_e32 v104, v104
	v_exp_f32_e32 v100, v100
	v_and_b32_e32 v106, 0xffff0000, v101
	v_mul_f32_e32 v102, 0.5, v102
	v_add_f32_e32 v101, 1.0, v104
	v_and_b32_e32 v104, 0xffff0000, v197
	v_fmac_f32_e32 v106, v105, v100
	v_mul_f32_e32 v105, 0x3d372713, v104
	v_mul_f32_e32 v105, v105, v104
	v_fma_f32 v105, v105, v104, v104
	v_mul_f32_e32 v105, 0x3f4c422a, v105
	v_rcp_f32_e32 v101, v101
	v_add_f32_e32 v105, v105, v105
	v_mul_f32_e32 v105, 0x3fb8aa3b, v105
	v_exp_f32_e32 v105, v105
	v_fma_f32 v101, v101, -2.0, 1.0
	v_add_f32_e32 v101, 1.0, v101
	v_mul_f32_e32 v101, v102, v101
	v_add_f32_e32 v102, 1.0, v105
	v_rcp_f32_e32 v102, v102
	v_lshlrev_b32_e32 v100, 16, v150
	v_add_f32_e32 v100, v103, v100
	v_mul_f32_e32 v100, v101, v100
	v_fma_f32 v102, v102, -2.0, 1.0
	v_and_b32_e32 v101, 0xffff0000, v150
	v_mul_f32_e32 v104, 0.5, v104
	v_add_f32_e32 v102, 1.0, v102
	v_add_f32_e32 v101, v106, v101
	v_mul_f32_e32 v102, v104, v102
	v_mul_f32_e32 v101, v102, v101
	v_cvt_pk_bf16_f32 v102, v100, v101
	ds_read_b64 v[100:101], v116 offset:1024
	ds_write_b32 v190, v102 offset:1152
	s_waitcnt lgkmcnt(1)
	v_lshlrev_b32_e32 v104, 16, v100
	v_exp_f32_e32 v104, v104
	v_and_b32_e32 v102, 0xffff0000, v100
	v_lshlrev_b32_e32 v100, 16, v101
	v_fmac_f32_e32 v102, v103, v104
	v_lshlrev_b32_e32 v103, 16, v195
	v_mul_f32_e32 v104, 0x3d372713, v103
	v_mul_f32_e32 v104, v104, v103
	v_fma_f32 v104, v104, v103, v103
	v_mul_f32_e32 v104, 0x3f4c422a, v104
	v_add_f32_e32 v104, v104, v104
	v_mul_f32_e32 v104, 0x3fb8aa3b, v104
	v_exp_f32_e32 v104, v104
	v_exp_f32_e32 v100, v100
	v_and_b32_e32 v105, 0xffff0000, v101
	v_mul_f32_e32 v103, 0.5, v103
	v_add_f32_e32 v101, 1.0, v104
	v_and_b32_e32 v104, 0xffff0000, v195
	v_fmac_f32_e32 v105, v106, v100
	v_mul_f32_e32 v106, 0x3d372713, v104
	v_mul_f32_e32 v106, v106, v104
	v_fma_f32 v106, v106, v104, v104
	v_mul_f32_e32 v106, 0x3f4c422a, v106
	v_rcp_f32_e32 v101, v101
	v_add_f32_e32 v106, v106, v106
	v_mul_f32_e32 v106, 0x3fb8aa3b, v106
	v_exp_f32_e32 v106, v106
	v_fma_f32 v101, v101, -2.0, 1.0
	v_add_f32_e32 v101, 1.0, v101
	v_mul_f32_e32 v101, v103, v101
	v_add_f32_e32 v103, 1.0, v106
	v_rcp_f32_e32 v103, v103
	v_lshlrev_b32_e32 v100, 16, v148
	v_add_f32_e32 v100, v102, v100
	v_mul_f32_e32 v100, v101, v100
	v_fma_f32 v103, v103, -2.0, 1.0
	v_and_b32_e32 v101, 0xffff0000, v148
	v_mul_f32_e32 v104, 0.5, v104
	v_add_f32_e32 v103, 1.0, v103
	v_add_f32_e32 v101, v105, v101
	v_mul_f32_e32 v103, v104, v103
	v_mul_f32_e32 v101, v103, v101
	v_cvt_pk_bf16_f32 v103, v100, v101
	ds_read_b64 v[100:101], v116 offset:896
	ds_write_b32 v190, v103 offset:1024
	s_waitcnt lgkmcnt(1)
	v_lshlrev_b32_e32 v104, 16, v100
	v_exp_f32_e32 v104, v104
	v_and_b32_e32 v103, 0xffff0000, v100
	v_lshlrev_b32_e32 v100, 16, v101
	v_fmac_f32_e32 v103, v102, v104
	v_lshlrev_b32_e32 v102, 16, v193
	v_mul_f32_e32 v104, 0x3d372713, v102
	v_mul_f32_e32 v104, v104, v102
	v_fma_f32 v104, v104, v102, v102
	v_mul_f32_e32 v104, 0x3f4c422a, v104
	v_add_f32_e32 v104, v104, v104
	v_mul_f32_e32 v104, 0x3fb8aa3b, v104
	v_exp_f32_e32 v104, v104
	v_exp_f32_e32 v100, v100
	v_and_b32_e32 v106, 0xffff0000, v101
	v_mul_f32_e32 v102, 0.5, v102
	v_add_f32_e32 v101, 1.0, v104
	v_and_b32_e32 v104, 0xffff0000, v193
	v_fmac_f32_e32 v106, v105, v100
	v_mul_f32_e32 v105, 0x3d372713, v104
	v_mul_f32_e32 v105, v105, v104
	v_fma_f32 v105, v105, v104, v104
	v_mul_f32_e32 v105, 0x3f4c422a, v105
	v_rcp_f32_e32 v101, v101
	v_add_f32_e32 v105, v105, v105
	v_mul_f32_e32 v105, 0x3fb8aa3b, v105
	v_exp_f32_e32 v105, v105
	v_fma_f32 v101, v101, -2.0, 1.0
	v_add_f32_e32 v101, 1.0, v101
	v_mul_f32_e32 v101, v102, v101
	v_add_f32_e32 v102, 1.0, v105
	v_rcp_f32_e32 v102, v102
	v_lshlrev_b32_e32 v100, 16, v146
	v_add_f32_e32 v100, v103, v100
	v_mul_f32_e32 v100, v101, v100
	v_fma_f32 v102, v102, -2.0, 1.0
	v_and_b32_e32 v101, 0xffff0000, v146
	v_mul_f32_e32 v104, 0.5, v104
	v_add_f32_e32 v102, 1.0, v102
	v_add_f32_e32 v101, v106, v101
	v_mul_f32_e32 v102, v104, v102
	v_mul_f32_e32 v101, v102, v101
	v_cvt_pk_bf16_f32 v102, v100, v101
	ds_read_b64 v[100:101], v116 offset:768
	ds_write_b32 v190, v102 offset:896
	s_waitcnt lgkmcnt(1)
	v_lshlrev_b32_e32 v104, 16, v100
	v_exp_f32_e32 v104, v104
	v_and_b32_e32 v102, 0xffff0000, v100
	v_lshlrev_b32_e32 v100, 16, v101
	v_fmac_f32_e32 v102, v103, v104
	v_lshlrev_b32_e32 v103, 16, v156
	v_mul_f32_e32 v104, 0x3d372713, v103
	v_mul_f32_e32 v104, v104, v103
	v_fma_f32 v104, v104, v103, v103
	v_mul_f32_e32 v104, 0x3f4c422a, v104
	v_add_f32_e32 v104, v104, v104
	v_mul_f32_e32 v104, 0x3fb8aa3b, v104
	v_exp_f32_e32 v104, v104
	v_exp_f32_e32 v100, v100
	v_and_b32_e32 v105, 0xffff0000, v101
	v_mul_f32_e32 v103, 0.5, v103
	v_add_f32_e32 v101, 1.0, v104
	v_and_b32_e32 v104, 0xffff0000, v156
	v_fmac_f32_e32 v105, v106, v100
	v_mul_f32_e32 v106, 0x3d372713, v104
	v_mul_f32_e32 v106, v106, v104
	v_fma_f32 v106, v106, v104, v104
	v_mul_f32_e32 v106, 0x3f4c422a, v106
	v_rcp_f32_e32 v101, v101
	v_add_f32_e32 v106, v106, v106
	v_mul_f32_e32 v106, 0x3fb8aa3b, v106
	v_exp_f32_e32 v106, v106
	v_fma_f32 v101, v101, -2.0, 1.0
	v_add_f32_e32 v101, 1.0, v101
	v_mul_f32_e32 v101, v103, v101
	v_add_f32_e32 v103, 1.0, v106
	v_rcp_f32_e32 v103, v103
	v_lshlrev_b32_e32 v100, 16, v144
	v_add_f32_e32 v100, v102, v100
	v_mul_f32_e32 v100, v101, v100
	v_fma_f32 v103, v103, -2.0, 1.0
	v_and_b32_e32 v101, 0xffff0000, v144
	v_mul_f32_e32 v104, 0.5, v104
	v_add_f32_e32 v103, 1.0, v103
	v_add_f32_e32 v101, v105, v101
	v_mul_f32_e32 v103, v104, v103
	v_mul_f32_e32 v101, v103, v101
	v_cvt_pk_bf16_f32 v103, v100, v101
	ds_read_b64 v[100:101], v116 offset:640
	ds_write_b32 v190, v103 offset:768
	s_waitcnt lgkmcnt(1)
	v_lshlrev_b32_e32 v104, 16, v100
	v_exp_f32_e32 v104, v104
	v_and_b32_e32 v103, 0xffff0000, v100
	v_lshlrev_b32_e32 v100, 16, v101
	v_fmac_f32_e32 v103, v102, v104
	v_lshlrev_b32_e32 v102, 16, v154
	v_mul_f32_e32 v104, 0x3d372713, v102
	v_mul_f32_e32 v104, v104, v102
	v_fma_f32 v104, v104, v102, v102
	v_mul_f32_e32 v104, 0x3f4c422a, v104
	v_add_f32_e32 v104, v104, v104
	v_mul_f32_e32 v104, 0x3fb8aa3b, v104
	v_exp_f32_e32 v104, v104
	v_exp_f32_e32 v100, v100
	v_and_b32_e32 v106, 0xffff0000, v101
	v_mul_f32_e32 v102, 0.5, v102
	v_add_f32_e32 v101, 1.0, v104
	v_and_b32_e32 v104, 0xffff0000, v154
	v_fmac_f32_e32 v106, v105, v100
	v_mul_f32_e32 v105, 0x3d372713, v104
	v_mul_f32_e32 v105, v105, v104
	v_fma_f32 v105, v105, v104, v104
	v_mul_f32_e32 v105, 0x3f4c422a, v105
	v_rcp_f32_e32 v101, v101
	v_add_f32_e32 v105, v105, v105
	v_mul_f32_e32 v105, 0x3fb8aa3b, v105
	v_exp_f32_e32 v105, v105
	v_fma_f32 v101, v101, -2.0, 1.0
	v_add_f32_e32 v101, 1.0, v101
	v_mul_f32_e32 v101, v102, v101
	v_add_f32_e32 v102, 1.0, v105
	v_rcp_f32_e32 v102, v102
	v_lshlrev_b32_e32 v100, 16, v143
	v_add_f32_e32 v100, v103, v100
	v_mul_f32_e32 v100, v101, v100
	v_fma_f32 v102, v102, -2.0, 1.0
	v_and_b32_e32 v101, 0xffff0000, v143
	v_mul_f32_e32 v104, 0.5, v104
	v_add_f32_e32 v102, 1.0, v102
	v_add_f32_e32 v101, v106, v101
	v_mul_f32_e32 v102, v104, v102
	v_mul_f32_e32 v101, v102, v101
	v_cvt_pk_bf16_f32 v102, v100, v101
	ds_read_b64 v[100:101], v116 offset:512
	ds_write_b32 v190, v102 offset:640
	s_waitcnt lgkmcnt(1)
	v_lshlrev_b32_e32 v104, 16, v100
	v_exp_f32_e32 v104, v104
	v_and_b32_e32 v102, 0xffff0000, v100
	v_lshlrev_b32_e32 v100, 16, v101
	v_fmac_f32_e32 v102, v103, v104
	v_lshlrev_b32_e32 v103, 16, v153
	v_mul_f32_e32 v104, 0x3d372713, v103
	v_mul_f32_e32 v104, v104, v103
	v_fma_f32 v104, v104, v103, v103
	v_mul_f32_e32 v104, 0x3f4c422a, v104
	v_add_f32_e32 v104, v104, v104
	v_mul_f32_e32 v104, 0x3fb8aa3b, v104
	v_exp_f32_e32 v104, v104
	v_exp_f32_e32 v100, v100
	v_and_b32_e32 v105, 0xffff0000, v101
	v_mul_f32_e32 v103, 0.5, v103
	v_add_f32_e32 v101, 1.0, v104
	v_and_b32_e32 v104, 0xffff0000, v153
	v_fmac_f32_e32 v105, v106, v100
	v_mul_f32_e32 v106, 0x3d372713, v104
	v_mul_f32_e32 v106, v106, v104
	v_fma_f32 v106, v106, v104, v104
	v_mul_f32_e32 v106, 0x3f4c422a, v106
	v_rcp_f32_e32 v101, v101
	v_add_f32_e32 v106, v106, v106
	v_mul_f32_e32 v106, 0x3fb8aa3b, v106
	v_exp_f32_e32 v106, v106
	v_fma_f32 v101, v101, -2.0, 1.0
	v_add_f32_e32 v101, 1.0, v101
	v_mul_f32_e32 v101, v103, v101
	v_add_f32_e32 v103, 1.0, v106
	v_rcp_f32_e32 v103, v103
	v_lshlrev_b32_e32 v100, 16, v142
	v_add_f32_e32 v100, v102, v100
	v_mul_f32_e32 v100, v101, v100
	v_fma_f32 v103, v103, -2.0, 1.0
	v_and_b32_e32 v101, 0xffff0000, v142
	v_mul_f32_e32 v104, 0.5, v104
	v_add_f32_e32 v103, 1.0, v103
	v_add_f32_e32 v101, v105, v101
	v_mul_f32_e32 v103, v104, v103
	v_mul_f32_e32 v101, v103, v101
	v_cvt_pk_bf16_f32 v103, v100, v101
	ds_read_b64 v[100:101], v116 offset:384
	ds_write_b32 v190, v103 offset:512
	s_waitcnt lgkmcnt(1)
	v_lshlrev_b32_e32 v104, 16, v100
	v_exp_f32_e32 v104, v104
	v_and_b32_e32 v103, 0xffff0000, v100
	v_lshlrev_b32_e32 v100, 16, v101
	v_fmac_f32_e32 v103, v102, v104
	v_lshlrev_b32_e32 v102, 16, v151
	v_mul_f32_e32 v104, 0x3d372713, v102
	v_mul_f32_e32 v104, v104, v102
	v_fma_f32 v104, v104, v102, v102
	v_mul_f32_e32 v104, 0x3f4c422a, v104
	v_add_f32_e32 v104, v104, v104
	v_mul_f32_e32 v104, 0x3fb8aa3b, v104
	v_exp_f32_e32 v104, v104
	v_exp_f32_e32 v100, v100
	v_and_b32_e32 v106, 0xffff0000, v101
	v_mul_f32_e32 v102, 0.5, v102
	v_add_f32_e32 v101, 1.0, v104
	v_and_b32_e32 v104, 0xffff0000, v151
	v_fmac_f32_e32 v106, v105, v100
	v_mul_f32_e32 v105, 0x3d372713, v104
	v_mul_f32_e32 v105, v105, v104
	v_fma_f32 v105, v105, v104, v104
	v_mul_f32_e32 v105, 0x3f4c422a, v105
	v_rcp_f32_e32 v101, v101
	v_add_f32_e32 v105, v105, v105
	v_mul_f32_e32 v105, 0x3fb8aa3b, v105
	v_exp_f32_e32 v105, v105
	v_fma_f32 v101, v101, -2.0, 1.0
	v_add_f32_e32 v101, 1.0, v101
	v_mul_f32_e32 v101, v102, v101
	v_add_f32_e32 v102, 1.0, v105
	v_rcp_f32_e32 v102, v102
	v_lshlrev_b32_e32 v100, 16, v141
	v_add_f32_e32 v100, v103, v100
	v_mul_f32_e32 v100, v101, v100
	v_fma_f32 v102, v102, -2.0, 1.0
	v_and_b32_e32 v101, 0xffff0000, v141
	v_mul_f32_e32 v104, 0.5, v104
	v_add_f32_e32 v102, 1.0, v102
	v_add_f32_e32 v101, v106, v101
	v_mul_f32_e32 v102, v104, v102
	v_mul_f32_e32 v101, v102, v101
	v_cvt_pk_bf16_f32 v102, v100, v101
	ds_read_b64 v[100:101], v116 offset:256
	ds_write_b32 v190, v102 offset:384
	s_waitcnt lgkmcnt(1)
	v_lshlrev_b32_e32 v104, 16, v100
	v_exp_f32_e32 v104, v104
	v_and_b32_e32 v102, 0xffff0000, v100
	v_lshlrev_b32_e32 v100, 16, v101
	v_fmac_f32_e32 v102, v103, v104
	v_lshlrev_b32_e32 v103, 16, v149
	v_mul_f32_e32 v104, 0x3d372713, v103
	v_mul_f32_e32 v104, v104, v103
	v_fma_f32 v104, v104, v103, v103
	v_mul_f32_e32 v104, 0x3f4c422a, v104
	v_add_f32_e32 v104, v104, v104
	v_mul_f32_e32 v104, 0x3fb8aa3b, v104
	v_exp_f32_e32 v104, v104
	v_exp_f32_e32 v100, v100
	v_and_b32_e32 v105, 0xffff0000, v101
	v_mul_f32_e32 v103, 0.5, v103
	v_add_f32_e32 v101, 1.0, v104
	v_and_b32_e32 v104, 0xffff0000, v149
	v_fmac_f32_e32 v105, v106, v100
	v_mul_f32_e32 v106, 0x3d372713, v104
	v_mul_f32_e32 v106, v106, v104
	v_fma_f32 v106, v106, v104, v104
	v_mul_f32_e32 v106, 0x3f4c422a, v106
	v_rcp_f32_e32 v101, v101
	v_add_f32_e32 v106, v106, v106
	v_mul_f32_e32 v106, 0x3fb8aa3b, v106
	v_exp_f32_e32 v106, v106
	v_fma_f32 v101, v101, -2.0, 1.0
	v_add_f32_e32 v101, 1.0, v101
	v_mul_f32_e32 v101, v103, v101
	v_add_f32_e32 v103, 1.0, v106
	v_rcp_f32_e32 v103, v103
	v_lshlrev_b32_e32 v100, 16, v140
	v_add_f32_e32 v100, v102, v100
	v_mul_f32_e32 v100, v101, v100
	v_fma_f32 v103, v103, -2.0, 1.0
	v_and_b32_e32 v101, 0xffff0000, v140
	v_mul_f32_e32 v104, 0.5, v104
	v_add_f32_e32 v103, 1.0, v103
	v_add_f32_e32 v101, v105, v101
	v_mul_f32_e32 v103, v104, v103
	v_mul_f32_e32 v101, v103, v101
	v_cvt_pk_bf16_f32 v103, v100, v101
	ds_read_b64 v[100:101], v116 offset:128
	ds_write_b32 v190, v103 offset:256
	s_waitcnt lgkmcnt(1)
	v_lshlrev_b32_e32 v104, 16, v100
	v_exp_f32_e32 v104, v104
	v_and_b32_e32 v103, 0xffff0000, v100
	v_lshlrev_b32_e32 v100, 16, v101
	v_fmac_f32_e32 v103, v102, v104
	v_lshlrev_b32_e32 v102, 16, v147
	v_mul_f32_e32 v104, 0x3d372713, v102
	v_mul_f32_e32 v104, v104, v102
	v_fma_f32 v104, v104, v102, v102
	v_mul_f32_e32 v104, 0x3f4c422a, v104
	v_add_f32_e32 v104, v104, v104
	v_mul_f32_e32 v104, 0x3fb8aa3b, v104
	v_exp_f32_e32 v104, v104
	v_exp_f32_e32 v100, v100
	v_and_b32_e32 v106, 0xffff0000, v101
	v_mul_f32_e32 v102, 0.5, v102
	v_add_f32_e32 v101, 1.0, v104
	v_and_b32_e32 v104, 0xffff0000, v147
	v_fmac_f32_e32 v106, v105, v100
	v_mul_f32_e32 v105, 0x3d372713, v104
	v_mul_f32_e32 v105, v105, v104
	v_fma_f32 v105, v105, v104, v104
	v_mul_f32_e32 v105, 0x3f4c422a, v105
	v_rcp_f32_e32 v101, v101
	v_add_f32_e32 v105, v105, v105
	v_mul_f32_e32 v105, 0x3fb8aa3b, v105
	v_exp_f32_e32 v105, v105
	v_fma_f32 v101, v101, -2.0, 1.0
	v_add_f32_e32 v101, 1.0, v101
	v_mul_f32_e32 v101, v102, v101
	v_add_f32_e32 v102, 1.0, v105
	v_rcp_f32_e32 v102, v102
	v_lshlrev_b32_e32 v100, 16, v139
	v_add_f32_e32 v100, v103, v100
	v_mul_f32_e32 v100, v101, v100
	v_fma_f32 v102, v102, -2.0, 1.0
	v_and_b32_e32 v101, 0xffff0000, v139
	v_mul_f32_e32 v104, 0.5, v104
	v_add_f32_e32 v102, 1.0, v102
	v_add_f32_e32 v101, v106, v101
	v_mul_f32_e32 v102, v104, v102
	v_mul_f32_e32 v101, v102, v101
	v_cvt_pk_bf16_f32 v102, v100, v101
	ds_read_b64 v[100:101], v116
	ds_write_b32 v190, v102 offset:128
	s_waitcnt lgkmcnt(1)
	v_lshlrev_b32_e32 v104, 16, v100
	v_exp_f32_e32 v104, v104
	v_and_b32_e32 v100, 0xffff0000, v100
	v_lshlrev_b32_e32 v102, 16, v101
	v_fmac_f32_e32 v100, v103, v104
	v_lshlrev_b32_e32 v103, 16, v145
	v_mul_f32_e32 v104, 0x3d372713, v103
	v_mul_f32_e32 v104, v104, v103
	v_fma_f32 v104, v104, v103, v103
	v_mul_f32_e32 v104, 0x3f4c422a, v104
	v_add_f32_e32 v104, v104, v104
	v_mul_f32_e32 v104, 0x3fb8aa3b, v104
	v_exp_f32_e32 v104, v104
	v_exp_f32_e32 v102, v102
	v_and_b32_e32 v101, 0xffff0000, v101
	v_mul_f32_e32 v103, 0.5, v103
	v_add_f32_e32 v104, 1.0, v104
	v_rcp_f32_e32 v104, v104
	v_fmac_f32_e32 v101, v106, v102
	v_lshlrev_b32_e32 v102, 16, v138
	v_add_f32_e32 v100, v100, v102
	v_fma_f32 v102, v104, -2.0, 1.0
	v_and_b32_e32 v104, 0xffff0000, v145
	v_mul_f32_e32 v105, 0x3d372713, v104
	v_mul_f32_e32 v105, v105, v104
	v_fma_f32 v105, v105, v104, v104
	v_mul_f32_e32 v105, 0x3f4c422a, v105
	v_add_f32_e32 v105, v105, v105
	v_mul_f32_e32 v105, 0x3fb8aa3b, v105
	v_exp_f32_e32 v105, v105
	v_add_f32_e32 v102, 1.0, v102
	v_mul_f32_e32 v102, v103, v102
	v_mul_f32_e32 v100, v102, v100
	v_add_f32_e32 v103, 1.0, v105
	v_rcp_f32_e32 v103, v103
	v_and_b32_e32 v102, 0xffff0000, v138
	v_add_f32_e32 v101, v101, v102
	v_fma_f32 v102, v103, -2.0, 1.0
	v_mul_f32_e32 v103, 0.5, v104
	v_add_f32_e32 v102, 1.0, v102
	v_mul_f32_e32 v102, v103, v102
	v_mul_f32_e32 v101, v102, v101
	v_cvt_pk_bf16_f32 v100, v100, v101
	ds_write_b32 v190, v100
	v_or_b32_e32 v102, s44, v72
	v_mov_b64_e32 v[100:101], s[20:21]
	v_mad_u64_u32 v[100:101], s[48:49], v102, s52, v[100:101]
	v_mad_i32_i24 v101, s45, v192, v101
	v_lshl_add_u64 v[100:101], s[42:43], 1, v[100:101]
	v_lshl_add_u64 v[100:101], v[100:101], 0, s[36:37]
	v_lshl_add_u64 v[104:105], v[100:101], 0, v[70:71]
	ds_read_b128 v[100:103], v191
	s_waitcnt lgkmcnt(0)
	global_store_dwordx4 v[104:105], v[100:103], off
	v_lshl_add_u64 v[104:105], v[104:105], 0, s[40:41]
	ds_read_b128 v[100:103], v191 offset:2048
	s_waitcnt lgkmcnt(0)
	global_store_dwordx4 v[104:105], v[100:103], off
	v_lshl_add_u64 v[104:105], v[104:105], 0, s[40:41]
	ds_read_b128 v[100:103], v191 offset:4224
	s_waitcnt lgkmcnt(0)
	global_store_dwordx4 v[104:105], v[100:103], off
	v_lshl_add_u64 v[104:105], v[104:105], 0, s[40:41]
	ds_read_b128 v[100:103], v191 offset:6272
	s_waitcnt lgkmcnt(0)
	global_store_dwordx4 v[104:105], v[100:103], off
	v_lshl_add_u64 v[104:105], v[104:105], 0, s[40:41]
	ds_read_b128 v[100:103], v191 offset:8448
	s_waitcnt lgkmcnt(0)
	global_store_dwordx4 v[104:105], v[100:103], off
	v_lshl_add_u64 v[104:105], v[104:105], 0, s[40:41]
	ds_read_b128 v[100:103], v191 offset:10496
	s_waitcnt lgkmcnt(0)
	global_store_dwordx4 v[104:105], v[100:103], off
	v_lshl_add_u64 v[104:105], v[104:105], 0, s[40:41]
	ds_read_b128 v[100:103], v191 offset:12672
	s_waitcnt lgkmcnt(0)
	global_store_dwordx4 v[104:105], v[100:103], off
	v_lshl_add_u64 v[104:105], v[104:105], 0, s[40:41]
	ds_read_b128 v[100:103], v191 offset:14720
	s_waitcnt lgkmcnt(0)
	global_store_dwordx4 v[104:105], v[100:103], off
	s_cbranch_vccz .LBB0_1505

.LBB0_1503:
	s_or_b64 exec, exec, s[48:49]
	s_ashr_i32 s45, s44, 31
	v_readlane_b32 s43, v254, 9
	s_ashr_i32 s47, s46, 31
	s_add_i32 s53, s53, s43
	s_lshl_b64 s[44:45], s[44:45], 7
	s_lshl_b64 s[46:47], s[46:47], 17
	s_add_u32 s46, s31, s46
	s_addc_u32 s47, s33, s47
	ds_write_b128 v173, v[22:25]
	s_waitcnt lgkmcnt(0)
	ds_write_b128 v174, v[2:5]
	ds_write_b128 v175, v[6:9]
	ds_write_b128 v176, v[10:13]
	ds_write_b128 v177, v[14:17] offset:128
	ds_write_b128 v178, v[18:21] offset:128
	ds_write_b128 v179, v[26:29] offset:128
	ds_write_b128 v180, v[30:33] offset:128
	ds_write_b128 v181, v[34:37] offset:256
	ds_write_b128 v182, v[38:41] offset:256
	ds_write_b128 v183, v[42:45] offset:256
	ds_write_b128 v184, v[46:49] offset:256
	ds_write_b128 v185, v[50:53] offset:384
	ds_write_b128 v186, v[54:57] offset:384
	ds_write_b128 v187, v[58:61] offset:384
	ds_write_b128 v188, v[62:65] offset:384
	v_lshl_add_u64 v[10:11], s[46:47], 0, v[66:67]
	v_lshl_add_u64 v[14:15], s[46:47], 0, v[74:75]
	v_lshl_add_u64 v[18:19], s[46:47], 0, v[76:77]
	v_lshl_add_u64 v[26:27], s[46:47], 0, v[78:79]
	v_lshl_add_u64 v[30:31], s[46:47], 0, v[80:81]
	v_lshl_add_u64 v[34:35], s[46:47], 0, v[82:83]
	v_lshl_add_u64 v[38:39], s[46:47], 0, v[84:85]
	v_lshl_add_u64 v[42:43], s[46:47], 0, v[86:87]
	v_lshl_add_u64 v[46:47], s[46:47], 0, v[88:89]
	global_load_dwordx4 v[22:25], v[10:11], off nt
	global_load_dwordx4 v[2:5], v[10:11], off offset:1024 nt
	global_load_dwordx4 v[6:9], v[10:11], off offset:2048 nt
	s_nop 0
	global_load_dwordx4 v[10:13], v[10:11], off offset:3072 nt
	s_nop 0
	global_load_dwordx4 v[14:17], v[14:15], off nt
	s_nop 0
	global_load_dwordx4 v[18:21], v[18:19], off nt
	s_nop 0
	global_load_dwordx4 v[26:29], v[26:27], off nt
	s_nop 0
	global_load_dwordx4 v[30:33], v[30:31], off nt
	s_nop 0
	global_load_dwordx4 v[34:37], v[34:35], off nt
	s_nop 0
	global_load_dwordx4 v[38:41], v[38:39], off nt
	s_nop 0
	global_load_dwordx4 v[42:45], v[42:43], off nt
	s_nop 0
	global_load_dwordx4 v[46:49], v[46:47], off nt
	ds_read2_b64 v[60:63], v189 offset1:16
	s_waitcnt lgkmcnt(14)
	v_pk_fma_f32 v[148:149], v[148:149], 0, v[152:153] op_sel_hi:[1,0,1]
	v_lshl_add_u64 v[50:51], s[46:47], 0, v[90:91]
	v_pk_fma_f32 v[144:145], v[148:149], v[144:145], v[150:151]
	v_lshl_add_u64 v[54:55], s[46:47], 0, v[92:93]
	s_waitcnt lgkmcnt(0)
	v_lshlrev_b32_e32 v64, 16, v60
	v_pk_fma_f32 v[140:141], v[144:145], v[140:141], v[146:147]
	v_lshlrev_b32_e32 v65, 16, v61
	v_add_f32_e32 v144, 0, v64
	v_pk_fma_f32 v[138:139], v[140:141], v[138:139], v[142:143]
	v_exp_f32_e32 v142, v64
	v_add_f32_e32 v145, 0, v65
	v_exp_f32_e32 v143, v65
	v_lshlrev_b32_e32 v64, 16, v62
	v_lshlrev_b32_e32 v65, 16, v63
	global_load_dwordx4 v[50:53], v[50:51], off nt
	s_nop 0
	global_load_dwordx4 v[54:57], v[54:55], off nt
	v_add_f32_e32 v148, v144, v64
	v_add_f32_e32 v149, v145, v65
	ds_read2_b64 v[144:147], v189 offset0:32 offset1:48
	v_exp_f32_e32 v64, v64
	v_exp_f32_e32 v65, v65
	v_and_b32_e32 v141, 0xffff0000, v60
	v_fma_f32 v60, 0, v142, v141
	v_and_b32_e32 v140, 0xffff0000, v61
	v_and_b32_e32 v62, 0xffff0000, v62
	v_fma_f32 v61, 0, v143, v140
	v_fmac_f32_e32 v62, v64, v60
	v_and_b32_e32 v60, 0xffff0000, v63
	s_waitcnt lgkmcnt(0)
	v_lshlrev_b32_e32 v63, 16, v145
	v_fmac_f32_e32 v60, v65, v61
	v_lshlrev_b32_e32 v61, 16, v144
	v_add_f32_e32 v65, v149, v63
	v_add_f32_e32 v64, v148, v61
	v_exp_f32_e32 v63, v63
	v_exp_f32_e32 v61, v61
	v_and_b32_e32 v145, 0xffff0000, v145
	v_and_b32_e32 v144, 0xffff0000, v144
	v_fmac_f32_e32 v145, v63, v60
	v_lshlrev_b32_e32 v60, 16, v146
	v_fmac_f32_e32 v144, v61, v62
	v_lshlrev_b32_e32 v61, 16, v147
	v_add_f32_e32 v64, v64, v60
	v_exp_f32_e32 v148, v60
	v_add_f32_e32 v65, v65, v61
	v_exp_f32_e32 v149, v61
	ds_read2_b64 v[60:63], v189 offset0:64 offset1:80
	v_and_b32_e32 v146, 0xffff0000, v146
	v_fmac_f32_e32 v146, v148, v144
	v_and_b32_e32 v144, 0xffff0000, v147
	v_fmac_f32_e32 v144, v149, v145
	s_waitcnt lgkmcnt(0)
	v_lshlrev_b32_e32 v147, 16, v61
	v_lshlrev_b32_e32 v145, 16, v60
	v_add_f32_e32 v65, v65, v147
	v_add_f32_e32 v64, v64, v145
	v_exp_f32_e32 v147, v147
	v_exp_f32_e32 v145, v145
	v_and_b32_e32 v61, 0xffff0000, v61
	v_and_b32_e32 v60, 0xffff0000, v60
	v_fmac_f32_e32 v61, v147, v144
	v_lshlrev_b32_e32 v144, 16, v62
	v_fmac_f32_e32 v60, v145, v146
	v_lshlrev_b32_e32 v145, 16, v63
	v_add_f32_e32 v64, v64, v144
	v_exp_f32_e32 v148, v144
	v_add_f32_e32 v65, v65, v145
	v_exp_f32_e32 v149, v145
	ds_read2_b64 v[144:147], v189 offset0:96 offset1:112
	v_and_b32_e32 v62, 0xffff0000, v62
	v_fmac_f32_e32 v62, v148, v60
	v_and_b32_e32 v60, 0xffff0000, v63
	v_fmac_f32_e32 v60, v149, v61
	s_waitcnt lgkmcnt(0)
	v_lshlrev_b32_e32 v63, 16, v145
	v_lshlrev_b32_e32 v61, 16, v144
	v_add_f32_e32 v65, v65, v63
	v_add_f32_e32 v64, v64, v61
	v_exp_f32_e32 v63, v63
	v_exp_f32_e32 v61, v61
	v_and_b32_e32 v145, 0xffff0000, v145
	v_and_b32_e32 v144, 0xffff0000, v144
	v_fmac_f32_e32 v145, v63, v60
	v_lshlrev_b32_e32 v60, 16, v146
	v_fmac_f32_e32 v144, v61, v62
	v_lshlrev_b32_e32 v61, 16, v147
	v_add_f32_e32 v64, v64, v60
	v_exp_f32_e32 v148, v60
	v_add_f32_e32 v65, v65, v61
	v_exp_f32_e32 v149, v61
	ds_read2_b64 v[60:63], v189 offset0:128 offset1:144
	v_and_b32_e32 v146, 0xffff0000, v146
	v_fmac_f32_e32 v146, v148, v144
	v_and_b32_e32 v144, 0xffff0000, v147
	v_fmac_f32_e32 v144, v149, v145
	s_waitcnt lgkmcnt(0)
	v_lshlrev_b32_e32 v147, 16, v61
	v_lshlrev_b32_e32 v145, 16, v60
	v_add_f32_e32 v65, v65, v147
	v_add_f32_e32 v64, v64, v145
	v_exp_f32_e32 v147, v147
	v_exp_f32_e32 v145, v145
	v_and_b32_e32 v61, 0xffff0000, v61
	v_and_b32_e32 v60, 0xffff0000, v60
	v_fmac_f32_e32 v61, v147, v144
	v_lshlrev_b32_e32 v144, 16, v62
	v_fmac_f32_e32 v60, v145, v146
	v_lshlrev_b32_e32 v145, 16, v63
	v_add_f32_e32 v64, v64, v144
	v_exp_f32_e32 v148, v144
	v_add_f32_e32 v65, v65, v145
	v_exp_f32_e32 v149, v145
	ds_read2_b64 v[144:147], v189 offset0:160 offset1:176
	v_and_b32_e32 v62, 0xffff0000, v62
	v_fmac_f32_e32 v62, v148, v60
	v_and_b32_e32 v60, 0xffff0000, v63
	v_fmac_f32_e32 v60, v149, v61
	s_waitcnt lgkmcnt(0)
	v_lshlrev_b32_e32 v63, 16, v145
	v_lshlrev_b32_e32 v61, 16, v144
	v_add_f32_e32 v65, v65, v63
	v_add_f32_e32 v64, v64, v61
	v_exp_f32_e32 v63, v63
	v_exp_f32_e32 v61, v61
	v_and_b32_e32 v145, 0xffff0000, v145
	v_and_b32_e32 v144, 0xffff0000, v144
	v_fmac_f32_e32 v145, v63, v60
	v_lshlrev_b32_e32 v60, 16, v146
	v_fmac_f32_e32 v144, v61, v62
	v_lshlrev_b32_e32 v61, 16, v147
	v_add_f32_e32 v64, v64, v60
	v_exp_f32_e32 v148, v60
	v_add_f32_e32 v65, v65, v61
	v_exp_f32_e32 v149, v61
	ds_read2_b64 v[60:63], v189 offset0:192 offset1:208
	v_and_b32_e32 v146, 0xffff0000, v146
	v_fmac_f32_e32 v146, v148, v144
	v_and_b32_e32 v144, 0xffff0000, v147
	v_fmac_f32_e32 v144, v149, v145
	s_waitcnt lgkmcnt(0)
	v_lshlrev_b32_e32 v147, 16, v61
	v_lshlrev_b32_e32 v145, 16, v60
	v_add_f32_e32 v65, v65, v147
	v_add_f32_e32 v64, v64, v145
	v_exp_f32_e32 v147, v147
	v_exp_f32_e32 v145, v145
	v_and_b32_e32 v61, 0xffff0000, v61
	v_and_b32_e32 v60, 0xffff0000, v60
	v_fmac_f32_e32 v61, v147, v144
	v_lshlrev_b32_e32 v144, 16, v62
	v_fmac_f32_e32 v60, v145, v146
	v_lshlrev_b32_e32 v145, 16, v63
	v_add_f32_e32 v64, v64, v144
	v_exp_f32_e32 v148, v144
	v_add_f32_e32 v65, v65, v145
	v_exp_f32_e32 v149, v145
	ds_read2_b64 v[144:147], v189 offset0:224 offset1:240
	v_and_b32_e32 v62, 0xffff0000, v62
	v_fmac_f32_e32 v62, v148, v60
	v_and_b32_e32 v60, 0xffff0000, v63
	v_fmac_f32_e32 v60, v149, v61
	s_waitcnt lgkmcnt(0)
	v_lshlrev_b32_e32 v63, 16, v145
	v_lshlrev_b32_e32 v61, 16, v144
	v_add_f32_e32 v65, v65, v63
	v_add_f32_e32 v64, v64, v61
	v_exp_f32_e32 v63, v63
	v_exp_f32_e32 v61, v61
	v_and_b32_e32 v145, 0xffff0000, v145
	v_and_b32_e32 v144, 0xffff0000, v144
	v_fmac_f32_e32 v145, v63, v60
	v_lshlrev_b32_e32 v60, 16, v146
	v_fmac_f32_e32 v144, v61, v62
	v_lshlrev_b32_e32 v61, 16, v147
	v_add_f32_e32 v64, v64, v60
	v_exp_f32_e32 v148, v60
	v_add_u32_e32 v150, 0x800, v189
	v_add_f32_e32 v65, v65, v61
	v_exp_f32_e32 v149, v61
	ds_read2_b64 v[60:63], v150 offset1:16
	v_and_b32_e32 v146, 0xffff0000, v146
	v_fmac_f32_e32 v146, v148, v144
	v_and_b32_e32 v144, 0xffff0000, v147
	v_fmac_f32_e32 v144, v149, v145
	s_waitcnt lgkmcnt(0)
	v_lshlrev_b32_e32 v147, 16, v61
	v_lshlrev_b32_e32 v145, 16, v60
	v_add_f32_e32 v65, v65, v147
	v_add_f32_e32 v64, v64, v145
	v_exp_f32_e32 v147, v147
	v_exp_f32_e32 v145, v145
	v_and_b32_e32 v61, 0xffff0000, v61
	v_and_b32_e32 v60, 0xffff0000, v60
	v_fmac_f32_e32 v61, v147, v144
	v_lshlrev_b32_e32 v144, 16, v62
	v_fmac_f32_e32 v60, v145, v146
	v_lshlrev_b32_e32 v145, 16, v63
	v_add_f32_e32 v64, v64, v144
	v_exp_f32_e32 v148, v144
	v_add_f32_e32 v65, v65, v145
	v_exp_f32_e32 v149, v145
	ds_read2_b64 v[144:147], v150 offset0:32 offset1:48
	v_and_b32_e32 v62, 0xffff0000, v62
	v_fmac_f32_e32 v62, v148, v60
	v_and_b32_e32 v60, 0xffff0000, v63
	v_fmac_f32_e32 v60, v149, v61
	s_waitcnt lgkmcnt(0)
	v_lshlrev_b32_e32 v63, 16, v145
	v_lshlrev_b32_e32 v61, 16, v144
	v_add_f32_e32 v65, v65, v63
	v_add_f32_e32 v64, v64, v61
	v_exp_f32_e32 v63, v63
	v_exp_f32_e32 v61, v61
	v_and_b32_e32 v145, 0xffff0000, v145
	v_and_b32_e32 v144, 0xffff0000, v144
	v_fmac_f32_e32 v145, v63, v60
	v_lshlrev_b32_e32 v60, 16, v146
	v_fmac_f32_e32 v144, v61, v62
	v_lshlrev_b32_e32 v61, 16, v147
	v_add_f32_e32 v64, v64, v60
	v_exp_f32_e32 v148, v60
	v_add_f32_e32 v65, v65, v61
	v_exp_f32_e32 v149, v61
	ds_read2_b64 v[60:63], v150 offset0:64 offset1:80
	v_and_b32_e32 v146, 0xffff0000, v146
	v_fmac_f32_e32 v146, v148, v144
	v_and_b32_e32 v144, 0xffff0000, v147
	v_fmac_f32_e32 v144, v149, v145
	s_waitcnt lgkmcnt(0)
	v_lshlrev_b32_e32 v147, 16, v61
	v_lshlrev_b32_e32 v145, 16, v60
	v_add_f32_e32 v65, v65, v147
	v_add_f32_e32 v64, v64, v145
	v_exp_f32_e32 v147, v147
	v_exp_f32_e32 v145, v145
	v_and_b32_e32 v61, 0xffff0000, v61
	v_and_b32_e32 v60, 0xffff0000, v60
	v_fmac_f32_e32 v61, v147, v144
	v_lshlrev_b32_e32 v144, 16, v62
	v_fmac_f32_e32 v60, v145, v146
	v_lshlrev_b32_e32 v145, 16, v63
	v_add_f32_e32 v64, v64, v144
	v_exp_f32_e32 v148, v144
	v_add_f32_e32 v65, v65, v145
	v_exp_f32_e32 v149, v145
	ds_read2_b64 v[144:147], v150 offset0:96 offset1:112
	v_and_b32_e32 v62, 0xffff0000, v62
	v_fmac_f32_e32 v62, v148, v60
	v_and_b32_e32 v60, 0xffff0000, v63
	v_fmac_f32_e32 v60, v149, v61
	s_waitcnt lgkmcnt(0)
	v_lshlrev_b32_e32 v63, 16, v145
	v_lshlrev_b32_e32 v61, 16, v144
	v_add_f32_e32 v65, v65, v63
	v_add_f32_e32 v64, v64, v61
	v_exp_f32_e32 v63, v63
	v_exp_f32_e32 v61, v61
	v_and_b32_e32 v145, 0xffff0000, v145
	v_and_b32_e32 v144, 0xffff0000, v144
	v_fmac_f32_e32 v145, v63, v60
	v_lshlrev_b32_e32 v60, 16, v146
	v_fmac_f32_e32 v144, v61, v62
	v_lshlrev_b32_e32 v61, 16, v147
	v_add_f32_e32 v64, v64, v60
	v_exp_f32_e32 v148, v60
	v_add_f32_e32 v65, v65, v61
	v_exp_f32_e32 v149, v61
	ds_read2_b64 v[60:63], v150 offset0:128 offset1:144
	v_and_b32_e32 v146, 0xffff0000, v146
	v_fmac_f32_e32 v146, v148, v144
	v_and_b32_e32 v144, 0xffff0000, v147
	v_fmac_f32_e32 v144, v149, v145
	s_waitcnt lgkmcnt(0)
	v_lshlrev_b32_e32 v147, 16, v61
	v_lshlrev_b32_e32 v145, 16, v60
	v_add_f32_e32 v65, v65, v147
	v_add_f32_e32 v64, v64, v145
	v_exp_f32_e32 v147, v147
	v_exp_f32_e32 v145, v145
	v_and_b32_e32 v61, 0xffff0000, v61
	v_and_b32_e32 v60, 0xffff0000, v60
	v_fmac_f32_e32 v61, v147, v144
	v_lshlrev_b32_e32 v144, 16, v62
	v_fmac_f32_e32 v60, v145, v146
	v_lshlrev_b32_e32 v145, 16, v63
	v_add_f32_e32 v64, v64, v144
	v_exp_f32_e32 v148, v144
	v_add_f32_e32 v65, v65, v145
	v_exp_f32_e32 v149, v145
	ds_read2_b64 v[144:147], v150 offset0:160 offset1:176
	v_and_b32_e32 v62, 0xffff0000, v62
	v_fmac_f32_e32 v62, v148, v60
	v_and_b32_e32 v60, 0xffff0000, v63
	v_fmac_f32_e32 v60, v149, v61
	s_waitcnt lgkmcnt(0)
	v_lshlrev_b32_e32 v63, 16, v145
	v_lshlrev_b32_e32 v61, 16, v144
	v_add_f32_e32 v65, v65, v63
	v_add_f32_e32 v64, v64, v61
	v_exp_f32_e32 v63, v63
	v_exp_f32_e32 v61, v61
	v_and_b32_e32 v145, 0xffff0000, v145
	v_and_b32_e32 v144, 0xffff0000, v144
	v_fmac_f32_e32 v145, v63, v60
	v_lshlrev_b32_e32 v60, 16, v146
	v_fmac_f32_e32 v144, v61, v62
	v_lshlrev_b32_e32 v61, 16, v147
	v_add_f32_e32 v64, v64, v60
	v_exp_f32_e32 v148, v60
	v_add_f32_e32 v65, v65, v61
	v_exp_f32_e32 v149, v61
	ds_read2_b64 v[60:63], v150 offset0:192 offset1:208
	v_and_b32_e32 v146, 0xffff0000, v146
	v_fmac_f32_e32 v146, v148, v144
	v_and_b32_e32 v144, 0xffff0000, v147
	v_fmac_f32_e32 v144, v149, v145
	s_waitcnt lgkmcnt(0)
	v_lshlrev_b32_e32 v147, 16, v61
	v_lshlrev_b32_e32 v145, 16, v60
	v_add_f32_e32 v65, v65, v147
	v_add_f32_e32 v64, v64, v145
	v_exp_f32_e32 v147, v147
	v_exp_f32_e32 v145, v145
	v_and_b32_e32 v61, 0xffff0000, v61
	v_and_b32_e32 v60, 0xffff0000, v60
	v_fmac_f32_e32 v61, v147, v144
	v_lshlrev_b32_e32 v144, 16, v62
	v_fmac_f32_e32 v60, v145, v146
	v_lshlrev_b32_e32 v145, 16, v63
	v_add_f32_e32 v64, v64, v144
	v_exp_f32_e32 v148, v144
	v_add_f32_e32 v65, v65, v145
	v_exp_f32_e32 v149, v145
	ds_read2_b64 v[144:147], v150 offset0:224 offset1:240
	v_and_b32_e32 v62, 0xffff0000, v62
	v_fmac_f32_e32 v62, v148, v60
	v_and_b32_e32 v60, 0xffff0000, v63
	v_fmac_f32_e32 v60, v149, v61
	s_waitcnt lgkmcnt(0)
	v_lshlrev_b32_e32 v61, 16, v144
	v_lshlrev_b32_e32 v63, 16, v145
	v_add_f32_e32 v64, v64, v61
	v_add_f32_e32 v65, v65, v63
	v_exp_f32_e32 v61, v61
	v_exp_f32_e32 v63, v63
	v_and_b32_e32 v144, 0xffff0000, v144
	v_fmac_f32_e32 v144, v61, v62
	v_and_b32_e32 v61, 0xffff0000, v145
	v_fmac_f32_e32 v61, v63, v60
	v_lshlrev_b32_e32 v60, 16, v146
	v_exp_f32_e32 v63, v60
	v_lshlrev_b32_e32 v62, 16, v147
	v_add_f32_e32 v60, v64, v60
	v_add_f32_e32 v64, v65, v62
	v_and_b32_e32 v145, 0xffff0000, v146
	v_fmac_f32_e32 v145, v63, v144
	v_exp_f32_e32 v62, v62
	v_exp_f32_e32 v144, v60
	v_exp_f32_e32 v146, v64
	v_and_b32_e32 v147, 0xffff0000, v147
	v_fmac_f32_e32 v147, v62, v61
	ds_bpermute_b32 v148, v73, v144
	ds_bpermute_b32 v149, v73, v146
	ds_bpermute_b32 v150, v73, v145
	ds_bpermute_b32 v151, v73, v147
	v_lshl_add_u64 v[58:59], s[46:47], 0, v[94:95]
	v_lshl_add_u64 v[62:63], s[46:47], 0, v[96:97]
	global_load_dwordx4 v[58:61], v[58:59], off nt
	s_nop 0
	global_load_dwordx4 v[62:65], v[62:63], off nt
	s_waitcnt lgkmcnt(1)
	v_fmac_f32_e32 v150, v138, v148
	s_waitcnt lgkmcnt(0)
	v_fmac_f32_e32 v151, v139, v149
	ds_bpermute_b32 v148, v166, v144
	ds_bpermute_b32 v149, v166, v145
	v_cndmask_b32_e64 v139, v151, v139, s[0:1]
	v_cndmask_b32_e64 v138, v150, v138, s[0:1]
	ds_bpermute_b32 v150, v166, v146
	ds_bpermute_b32 v151, v166, v147
	ds_bpermute_b32 v144, v167, v144
	ds_bpermute_b32 v146, v167, v146
	ds_bpermute_b32 v145, v167, v145
	ds_bpermute_b32 v147, v167, v147
	s_waitcnt lgkmcnt(6)
	v_fmac_f32_e32 v149, v138, v148
	s_waitcnt lgkmcnt(4)
	v_fmac_f32_e32 v151, v139, v150
	v_cndmask_b32_e64 v139, v139, v151, s[4:5]
	v_cndmask_b32_e64 v138, v138, v149, s[4:5]
	s_waitcnt lgkmcnt(1)
	v_fmac_f32_e32 v145, v138, v144
	s_waitcnt lgkmcnt(0)
	v_fmac_f32_e32 v147, v139, v146
	v_cndmask_b32_e64 v139, v139, v147, s[6:7]
	v_cndmask_b32_e64 v138, v138, v145, s[6:7]
	v_fmac_f32_e32 v141, v142, v138
	v_fmac_f32_e32 v140, v143, v139
	v_cvt_pk_bf16_f32 v138, v141, v140
	ds_read_b64 v[142:143], v189 offset:128
	s_cmpk_gt_i32 s53, 0x27ff
	s_waitcnt lgkmcnt(0)
	v_lshlrev_b32_e32 v139, 16, v142
	v_lshlrev_b32_e32 v144, 16, v143
	v_exp_f32_e32 v139, v139
	v_exp_f32_e32 v144, v144
	v_and_b32_e32 v142, 0xffff0000, v142
	v_and_b32_e32 v143, 0xffff0000, v143
	v_fmac_f32_e32 v142, v141, v139
	v_fmac_f32_e32 v143, v140, v144
	v_cvt_pk_bf16_f32 v139, v142, v143
	ds_read_b64 v[140:141], v189 offset:256
	s_waitcnt lgkmcnt(0)
	v_lshlrev_b32_e32 v144, 16, v140
	v_lshlrev_b32_e32 v145, 16, v141
	v_exp_f32_e32 v144, v144
	v_exp_f32_e32 v145, v145
	v_and_b32_e32 v146, 0xffff0000, v140
	v_and_b32_e32 v141, 0xffff0000, v141
	v_fmac_f32_e32 v146, v142, v144
	v_fmac_f32_e32 v141, v143, v145
	v_cvt_pk_bf16_f32 v140, v146, v141
	ds_read_b64 v[142:143], v189 offset:384
	s_waitcnt lgkmcnt(0)
	v_lshlrev_b32_e32 v144, 16, v142
	v_lshlrev_b32_e32 v145, 16, v143
	v_exp_f32_e32 v144, v144
	v_exp_f32_e32 v145, v145
	v_and_b32_e32 v147, 0xffff0000, v142
	v_fmac_f32_e32 v147, v146, v144
	v_and_b32_e32 v144, 0xffff0000, v143
	v_fmac_f32_e32 v144, v141, v145
	v_cvt_pk_bf16_f32 v141, v147, v144
	ds_read_b64 v[142:143], v189 offset:512
	s_waitcnt lgkmcnt(0)
	v_lshlrev_b32_e32 v145, 16, v142
	v_lshlrev_b32_e32 v146, 16, v143
	v_exp_f32_e32 v145, v145
	v_exp_f32_e32 v146, v146
	v_and_b32_e32 v148, 0xffff0000, v142
	v_and_b32_e32 v143, 0xffff0000, v143
	v_fmac_f32_e32 v148, v147, v145
	v_fmac_f32_e32 v143, v144, v146
	v_cvt_pk_bf16_f32 v142, v148, v143
	ds_read_b64 v[144:145], v189 offset:640
	s_waitcnt lgkmcnt(0)
	v_lshlrev_b32_e32 v146, 16, v144
	v_lshlrev_b32_e32 v147, 16, v145
	v_exp_f32_e32 v146, v146
	v_exp_f32_e32 v147, v147
	v_and_b32_e32 v149, 0xffff0000, v144
	v_fmac_f32_e32 v149, v148, v146
	v_and_b32_e32 v146, 0xffff0000, v145
	v_fmac_f32_e32 v146, v143, v147
	v_cvt_pk_bf16_f32 v143, v149, v146
	ds_read_b64 v[144:145], v189 offset:768
	s_waitcnt lgkmcnt(0)
	v_lshlrev_b32_e32 v147, 16, v144
	v_lshlrev_b32_e32 v148, 16, v145
	v_exp_f32_e32 v147, v147
	v_exp_f32_e32 v148, v148
	v_and_b32_e32 v150, 0xffff0000, v144
	v_and_b32_e32 v145, 0xffff0000, v145
	v_fmac_f32_e32 v150, v149, v147
	v_fmac_f32_e32 v145, v146, v148
	v_cvt_pk_bf16_f32 v144, v150, v145
	ds_read_b64 v[146:147], v189 offset:896
	s_waitcnt lgkmcnt(0)
	v_lshlrev_b32_e32 v148, 16, v146
	v_lshlrev_b32_e32 v149, 16, v147
	v_exp_f32_e32 v148, v148
	v_exp_f32_e32 v149, v149
	v_and_b32_e32 v151, 0xffff0000, v146
	v_and_b32_e32 v147, 0xffff0000, v147
	v_fmac_f32_e32 v151, v150, v148
	v_fmac_f32_e32 v147, v145, v149
	v_cvt_pk_bf16_f32 v146, v151, v147
	ds_read_b64 v[148:149], v189 offset:1024
	s_waitcnt lgkmcnt(0)
	v_lshlrev_b32_e32 v145, 16, v148
	v_lshlrev_b32_e32 v150, 16, v149
	v_exp_f32_e32 v145, v145
	v_exp_f32_e32 v150, v150
	v_and_b32_e32 v152, 0xffff0000, v148
	v_fmac_f32_e32 v152, v151, v145
	v_and_b32_e32 v145, 0xffff0000, v149
	v_fmac_f32_e32 v145, v147, v150
	v_cvt_pk_bf16_f32 v148, v152, v145
	ds_read_b64 v[150:151], v189 offset:1152
	s_waitcnt lgkmcnt(0)
	v_lshlrev_b32_e32 v147, 16, v150
	v_lshlrev_b32_e32 v149, 16, v151
	v_exp_f32_e32 v147, v147
	v_exp_f32_e32 v149, v149
	v_and_b32_e32 v154, 0xffff0000, v150
	v_fmac_f32_e32 v154, v152, v147
	v_and_b32_e32 v147, 0xffff0000, v151
	v_fmac_f32_e32 v147, v145, v149
	v_cvt_pk_bf16_f32 v150, v154, v147
	ds_read_b64 v[152:153], v189 offset:1280
	s_waitcnt lgkmcnt(0)
	v_lshlrev_b32_e32 v145, 16, v152
	v_lshlrev_b32_e32 v149, 16, v153
	v_exp_f32_e32 v145, v145
	v_exp_f32_e32 v149, v149
	v_and_b32_e32 v151, 0xffff0000, v152
	v_fmac_f32_e32 v151, v154, v145
	v_and_b32_e32 v145, 0xffff0000, v153
	v_fmac_f32_e32 v145, v147, v149
	v_cvt_pk_bf16_f32 v152, v151, v145
	ds_read_b64 v[154:155], v189 offset:1408
	s_waitcnt lgkmcnt(0)
	v_lshlrev_b32_e32 v147, 16, v154
	v_lshlrev_b32_e32 v149, 16, v155
	v_exp_f32_e32 v147, v147
	v_exp_f32_e32 v149, v149
	v_and_b32_e32 v153, 0xffff0000, v154
	v_fmac_f32_e32 v153, v151, v147
	v_and_b32_e32 v147, 0xffff0000, v155
	v_fmac_f32_e32 v147, v145, v149
	v_cvt_pk_bf16_f32 v155, v153, v147
	ds_read_b64 v[156:157], v189 offset:1536
	s_waitcnt lgkmcnt(0)
	v_lshlrev_b32_e32 v145, 16, v156
	v_lshlrev_b32_e32 v149, 16, v157
	v_exp_f32_e32 v145, v145
	v_exp_f32_e32 v149, v149
	v_and_b32_e32 v151, 0xffff0000, v156
	v_fmac_f32_e32 v151, v153, v145
	v_and_b32_e32 v145, 0xffff0000, v157
	v_fmac_f32_e32 v145, v147, v149
	v_cvt_pk_bf16_f32 v157, v151, v145
	ds_read_b64 v[194:195], v189 offset:1664
	s_waitcnt lgkmcnt(0)
	v_lshlrev_b32_e32 v147, 16, v194
	v_lshlrev_b32_e32 v149, 16, v195
	v_exp_f32_e32 v147, v147
	v_exp_f32_e32 v149, v149
	v_and_b32_e32 v153, 0xffff0000, v194
	v_fmac_f32_e32 v153, v151, v147
	v_and_b32_e32 v147, 0xffff0000, v195
	v_fmac_f32_e32 v147, v145, v149
	v_cvt_pk_bf16_f32 v194, v153, v147
	ds_read_b64 v[196:197], v189 offset:1792
	s_waitcnt lgkmcnt(0)
	v_lshlrev_b32_e32 v145, 16, v196
	v_lshlrev_b32_e32 v149, 16, v197
	v_exp_f32_e32 v145, v145
	v_exp_f32_e32 v149, v149
	v_and_b32_e32 v151, 0xffff0000, v196
	v_fmac_f32_e32 v151, v153, v145
	v_and_b32_e32 v145, 0xffff0000, v197
	v_fmac_f32_e32 v145, v147, v149
	v_cvt_pk_bf16_f32 v196, v151, v145
	ds_read_b64 v[198:199], v189 offset:1920
	s_waitcnt lgkmcnt(0)
	v_lshlrev_b32_e32 v147, 16, v198
	v_lshlrev_b32_e32 v149, 16, v199
	v_exp_f32_e32 v147, v147
	v_exp_f32_e32 v149, v149
	v_and_b32_e32 v153, 0xffff0000, v198
	v_fmac_f32_e32 v153, v151, v147
	v_and_b32_e32 v147, 0xffff0000, v199
	v_fmac_f32_e32 v147, v145, v149
	v_cvt_pk_bf16_f32 v198, v153, v147
	ds_read_b64 v[200:201], v189 offset:2048
	s_waitcnt lgkmcnt(0)
	v_lshlrev_b32_e32 v145, 16, v200
	v_lshlrev_b32_e32 v149, 16, v201
	v_exp_f32_e32 v145, v145
	v_exp_f32_e32 v149, v149
	v_and_b32_e32 v151, 0xffff0000, v200
	v_fmac_f32_e32 v151, v153, v145
	v_and_b32_e32 v145, 0xffff0000, v201
	v_fmac_f32_e32 v145, v147, v149
	v_cvt_pk_bf16_f32 v201, v151, v145
	ds_read_b64 v[202:203], v189 offset:2176
	s_waitcnt lgkmcnt(0)
	v_lshlrev_b32_e32 v147, 16, v202
	v_lshlrev_b32_e32 v149, 16, v203
	v_exp_f32_e32 v147, v147
	v_exp_f32_e32 v149, v149
	v_and_b32_e32 v153, 0xffff0000, v202
	v_fmac_f32_e32 v153, v151, v147
	v_and_b32_e32 v147, 0xffff0000, v203
	v_fmac_f32_e32 v147, v145, v149
	v_cvt_pk_bf16_f32 v203, v153, v147
	ds_read_b64 v[204:205], v189 offset:2304
	s_waitcnt lgkmcnt(0)
	v_lshlrev_b32_e32 v145, 16, v204
	v_lshlrev_b32_e32 v149, 16, v205
	v_exp_f32_e32 v145, v145
	v_exp_f32_e32 v149, v149
	v_and_b32_e32 v151, 0xffff0000, v204
	v_fmac_f32_e32 v151, v153, v145
	v_and_b32_e32 v145, 0xffff0000, v205
	v_fmac_f32_e32 v145, v147, v149
	v_cvt_pk_bf16_f32 v205, v151, v145
	ds_read_b64 v[206:207], v189 offset:2432
	s_waitcnt lgkmcnt(0)
	v_lshlrev_b32_e32 v147, 16, v206
	v_lshlrev_b32_e32 v149, 16, v207
	v_exp_f32_e32 v147, v147
	v_exp_f32_e32 v149, v149
	v_and_b32_e32 v153, 0xffff0000, v206
	v_fmac_f32_e32 v153, v151, v147
	v_and_b32_e32 v147, 0xffff0000, v207
	v_fmac_f32_e32 v147, v145, v149
	v_cvt_pk_bf16_f32 v207, v153, v147
	ds_read_b64 v[208:209], v189 offset:2560
	s_waitcnt lgkmcnt(0)
	v_lshlrev_b32_e32 v145, 16, v208
	v_lshlrev_b32_e32 v149, 16, v209
	v_exp_f32_e32 v145, v145
	v_exp_f32_e32 v149, v149
	v_and_b32_e32 v151, 0xffff0000, v208
	v_fmac_f32_e32 v151, v153, v145
	v_and_b32_e32 v145, 0xffff0000, v209
	v_fmac_f32_e32 v145, v147, v149
	v_cvt_pk_bf16_f32 v209, v151, v145
	ds_read_b64 v[210:211], v189 offset:2688
	s_waitcnt lgkmcnt(0)
	v_lshlrev_b32_e32 v147, 16, v210
	v_lshlrev_b32_e32 v149, 16, v211
	v_exp_f32_e32 v147, v147
	v_exp_f32_e32 v149, v149
	v_and_b32_e32 v153, 0xffff0000, v210
	v_fmac_f32_e32 v153, v151, v147
	v_and_b32_e32 v147, 0xffff0000, v211
	v_fmac_f32_e32 v147, v145, v149
	v_cvt_pk_bf16_f32 v211, v153, v147
	ds_read_b64 v[212:213], v189 offset:2816
	s_waitcnt lgkmcnt(0)
	v_lshlrev_b32_e32 v145, 16, v212
	v_lshlrev_b32_e32 v149, 16, v213
	v_exp_f32_e32 v145, v145
	v_exp_f32_e32 v149, v149
	v_and_b32_e32 v151, 0xffff0000, v212
	v_fmac_f32_e32 v151, v153, v145
	v_and_b32_e32 v145, 0xffff0000, v213
	v_fmac_f32_e32 v145, v147, v149
	v_cvt_pk_bf16_f32 v214, v151, v145
	ds_read_b64 v[212:213], v189 offset:2944
	s_waitcnt lgkmcnt(0)
	v_lshlrev_b32_e32 v147, 16, v212
	v_lshlrev_b32_e32 v149, 16, v213
	v_exp_f32_e32 v147, v147
	v_exp_f32_e32 v149, v149
	v_and_b32_e32 v153, 0xffff0000, v212
	v_fmac_f32_e32 v153, v151, v147
	v_and_b32_e32 v147, 0xffff0000, v213
	v_fmac_f32_e32 v147, v145, v149
	v_cvt_pk_bf16_f32 v216, v153, v147
	ds_read_b64 v[212:213], v189 offset:3072
	s_waitcnt lgkmcnt(0)
	v_lshlrev_b32_e32 v145, 16, v212
	v_lshlrev_b32_e32 v149, 16, v213
	v_exp_f32_e32 v145, v145
	v_exp_f32_e32 v149, v149
	v_and_b32_e32 v151, 0xffff0000, v212
	v_fmac_f32_e32 v151, v153, v145
	v_and_b32_e32 v145, 0xffff0000, v213
	v_fmac_f32_e32 v145, v147, v149
	v_cvt_pk_bf16_f32 v218, v151, v145
	ds_read_b64 v[212:213], v189 offset:3200
	s_waitcnt lgkmcnt(0)
	v_lshlrev_b32_e32 v147, 16, v212
	v_lshlrev_b32_e32 v149, 16, v213
	v_exp_f32_e32 v147, v147
	v_exp_f32_e32 v149, v149
	v_and_b32_e32 v153, 0xffff0000, v212
	v_fmac_f32_e32 v153, v151, v147
	v_and_b32_e32 v147, 0xffff0000, v213
	v_fmac_f32_e32 v147, v145, v149
	v_cvt_pk_bf16_f32 v220, v153, v147
	ds_read_b64 v[212:213], v189 offset:3328
	s_waitcnt lgkmcnt(0)
	v_lshlrev_b32_e32 v145, 16, v212
	v_lshlrev_b32_e32 v149, 16, v213
	v_exp_f32_e32 v145, v145
	v_exp_f32_e32 v149, v149
	v_and_b32_e32 v151, 0xffff0000, v212
	v_fmac_f32_e32 v151, v153, v145
	v_and_b32_e32 v145, 0xffff0000, v213
	v_fmac_f32_e32 v145, v147, v149
	v_cvt_pk_bf16_f32 v222, v151, v145
	ds_read_b64 v[212:213], v189 offset:3456
	s_waitcnt lgkmcnt(0)
	v_lshlrev_b32_e32 v147, 16, v212
	v_lshlrev_b32_e32 v149, 16, v213
	v_exp_f32_e32 v147, v147
	v_exp_f32_e32 v149, v149
	v_and_b32_e32 v153, 0xffff0000, v212
	v_fmac_f32_e32 v153, v151, v147
	v_and_b32_e32 v147, 0xffff0000, v213
	v_fmac_f32_e32 v147, v145, v149
	v_cvt_pk_bf16_f32 v225, v153, v147
	ds_read_b64 v[212:213], v189 offset:3584
	s_waitcnt lgkmcnt(0)
	v_lshlrev_b32_e32 v145, 16, v212
	v_lshlrev_b32_e32 v149, 16, v213
	v_exp_f32_e32 v145, v145
	v_exp_f32_e32 v149, v149
	v_and_b32_e32 v151, 0xffff0000, v212
	v_fmac_f32_e32 v151, v153, v145
	v_and_b32_e32 v145, 0xffff0000, v213
	v_fmac_f32_e32 v145, v147, v149
	v_cvt_pk_bf16_f32 v227, v151, v145
	ds_read_b64 v[212:213], v189 offset:3712
	s_waitcnt lgkmcnt(0)
	v_lshlrev_b32_e32 v147, 16, v212
	v_lshlrev_b32_e32 v149, 16, v213
	v_exp_f32_e32 v147, v147
	v_exp_f32_e32 v149, v149
	v_and_b32_e32 v153, 0xffff0000, v212
	v_fmac_f32_e32 v153, v151, v147
	v_and_b32_e32 v147, 0xffff0000, v213
	v_fmac_f32_e32 v147, v145, v149
	v_cvt_pk_bf16_f32 v229, v153, v147
	ds_read_b64 v[212:213], v189 offset:3840
	s_waitcnt lgkmcnt(0)
	v_lshlrev_b32_e32 v145, 16, v212
	v_lshlrev_b32_e32 v149, 16, v213
	v_exp_f32_e32 v145, v145
	v_exp_f32_e32 v149, v149
	v_and_b32_e32 v151, 0xffff0000, v212
	v_fmac_f32_e32 v151, v153, v145
	v_and_b32_e32 v145, 0xffff0000, v213
	v_fmac_f32_e32 v145, v147, v149
	v_cvt_pk_bf16_f32 v231, v151, v145
	ds_read_b64 v[212:213], v189 offset:3968
	s_waitcnt lgkmcnt(0)
	v_lshlrev_b32_e32 v147, 16, v212
	v_lshlrev_b32_e32 v149, 16, v213
	v_exp_f32_e32 v147, v147
	v_exp_f32_e32 v149, v149
	v_and_b32_e32 v153, 0xffff0000, v212
	v_fmac_f32_e32 v153, v151, v147
	v_and_b32_e32 v147, 0xffff0000, v213
	v_fmac_f32_e32 v147, v145, v149
	v_or_b32_e32 v145, s44, v68
	v_mov_b64_e32 v[212:213], s[12:13]
	v_mad_u64_u32 v[212:213], s[46:47], v145, s3, v[212:213]
	v_mad_i32_i24 v213, s45, v169, v213
	v_lshl_add_u64 v[100:101], v[100:101], 1, v[212:213]
	v_cvt_pk_bf16_f32 v233, v153, v147
	global_load_dword v145, v[100:101], off
	v_lshl_add_u64 v[100:101], v[100:101], 0, s[38:39]
	global_load_dword v147, v[100:101], off
	v_lshl_add_u64 v[100:101], v[100:101], 0, s[38:39]
	global_load_dword v149, v[100:101], off
	v_lshl_add_u64 v[100:101], v[100:101], 0, s[38:39]
	global_load_dword v151, v[100:101], off
	v_lshl_add_u64 v[100:101], v[100:101], 0, s[38:39]
	global_load_dword v153, v[100:101], off
	v_lshl_add_u64 v[100:101], v[100:101], 0, s[38:39]
	global_load_dword v154, v[100:101], off
	v_lshl_add_u64 v[100:101], v[100:101], 0, s[38:39]
	global_load_dword v156, v[100:101], off
	v_lshl_add_u64 v[100:101], v[100:101], 0, s[38:39]
	global_load_dword v193, v[100:101], off
	v_lshl_add_u64 v[100:101], v[100:101], 0, s[38:39]
	global_load_dword v195, v[100:101], off
	v_lshl_add_u64 v[100:101], v[100:101], 0, s[38:39]
	global_load_dword v197, v[100:101], off
	v_lshl_add_u64 v[100:101], v[100:101], 0, s[38:39]
	global_load_dword v199, v[100:101], off
	v_lshl_add_u64 v[100:101], v[100:101], 0, s[38:39]
	global_load_dword v200, v[100:101], off
	v_lshl_add_u64 v[100:101], v[100:101], 0, s[38:39]
	global_load_dword v202, v[100:101], off
	v_lshl_add_u64 v[100:101], v[100:101], 0, s[38:39]
	global_load_dword v204, v[100:101], off
	v_lshl_add_u64 v[100:101], v[100:101], 0, s[38:39]
	global_load_dword v206, v[100:101], off
	v_lshl_add_u64 v[100:101], v[100:101], 0, s[38:39]
	global_load_dword v208, v[100:101], off
	v_lshl_add_u64 v[100:101], v[100:101], 0, s[38:39]
	global_load_dword v210, v[100:101], off
	v_lshl_add_u64 v[100:101], v[100:101], 0, s[38:39]
	global_load_dword v212, v[100:101], off
	v_lshl_add_u64 v[100:101], v[100:101], 0, s[38:39]
	global_load_dword v213, v[100:101], off
	v_lshl_add_u64 v[100:101], v[100:101], 0, s[38:39]
	global_load_dword v215, v[100:101], off
	v_lshl_add_u64 v[100:101], v[100:101], 0, s[38:39]
	global_load_dword v217, v[100:101], off
	v_lshl_add_u64 v[100:101], v[100:101], 0, s[38:39]
	global_load_dword v219, v[100:101], off
	v_lshl_add_u64 v[100:101], v[100:101], 0, s[38:39]
	global_load_dword v221, v[100:101], off
	v_lshl_add_u64 v[100:101], v[100:101], 0, s[38:39]
	global_load_dword v223, v[100:101], off
	v_lshl_add_u64 v[100:101], v[100:101], 0, s[38:39]
	global_load_dword v224, v[100:101], off
	v_lshl_add_u64 v[100:101], v[100:101], 0, s[38:39]
	global_load_dword v226, v[100:101], off
	v_lshl_add_u64 v[100:101], v[100:101], 0, s[38:39]
	global_load_dword v228, v[100:101], off
	v_lshl_add_u64 v[100:101], v[100:101], 0, s[38:39]
	global_load_dword v230, v[100:101], off
	v_lshl_add_u64 v[100:101], v[100:101], 0, s[38:39]
	global_load_dword v232, v[100:101], off
	v_lshl_add_u64 v[100:101], v[100:101], 0, s[38:39]
	global_load_dword v234, v[100:101], off
	v_lshl_add_u64 v[100:101], v[100:101], 0, s[38:39]
	global_load_dword v235, v[100:101], off
	v_lshl_add_u64 v[100:101], v[100:101], 0, s[38:39]
	global_load_dword v236, v[100:101], off
	s_waitcnt vmcnt(32)
	v_pk_fma_f32 v[100:101], v[102:103], 0, v[106:107] op_sel_hi:[1,0,1]
	v_pk_mul_f32 v[102:103], v[102:103], v[110:111]
	v_pk_fma_f32 v[100:101], v[100:101], v[110:111], v[104:105]
	v_pk_mul_f32 v[102:103], v[102:103], v[108:109]
	v_pk_fma_f32 v[100:101], v[100:101], v[108:109], v[114:115]
	v_pk_mul_f32 v[102:103], v[102:103], v[118:119]
	v_pk_fma_f32 v[100:101], v[100:101], v[118:119], v[112:113]
	v_pk_mul_f32 v[102:103], v[102:103], v[116:117]
	v_pk_fma_f32 v[100:101], v[100:101], v[116:117], v[122:123]
	v_pk_mul_f32 v[102:103], v[102:103], v[126:127]
	v_pk_fma_f32 v[100:101], v[100:101], v[126:127], v[120:121]
	v_pk_mul_f32 v[102:103], v[102:103], v[124:125]
	v_pk_fma_f32 v[100:101], v[100:101], v[124:125], v[130:131]
	v_pk_mul_f32 v[102:103], v[102:103], v[134:135]
	v_pk_fma_f32 v[100:101], v[100:101], v[134:135], v[128:129]
	v_pk_mul_f32 v[108:109], v[102:103], v[132:133]
	v_pk_fma_f32 v[110:111], v[100:101], v[132:133], v[136:137]
	ds_bpermute_b32 v112, v73, v108
	ds_bpermute_b32 v113, v73, v109
	ds_bpermute_b32 v114, v73, v110
	ds_bpermute_b32 v115, v73, v111
	ds_bpermute_b32 v100, v166, v108
	ds_bpermute_b32 v101, v166, v109
	ds_bpermute_b32 v102, v166, v110
	ds_bpermute_b32 v103, v166, v111
	ds_bpermute_b32 v104, v167, v108
	ds_bpermute_b32 v105, v167, v109
	ds_bpermute_b32 v106, v167, v110
	ds_bpermute_b32 v107, v167, v111
	ds_bpermute_b32 v108, v168, v108
	ds_bpermute_b32 v109, v168, v109
	ds_bpermute_b32 v110, v168, v110
	ds_bpermute_b32 v111, v168, v111
	s_cselect_b64 s[46:47], -1, 0
	s_and_b64 vcc, exec, s[46:47]
	ds_write_b128 v173, v[22:25]
	ds_write_b128 v174, v[2:5]
	ds_write_b128 v175, v[6:9]
	ds_write_b128 v176, v[10:13]
	ds_write_b128 v177, v[14:17] offset:128
	ds_write_b128 v178, v[18:21] offset:128
	ds_write_b128 v179, v[26:29] offset:128
	ds_write_b128 v180, v[30:33] offset:128
	ds_write_b128 v181, v[34:37] offset:256
	ds_write_b128 v182, v[38:41] offset:256
	ds_write_b128 v183, v[42:45] offset:256
	ds_write_b128 v184, v[46:49] offset:256
	ds_write_b128 v185, v[50:53] offset:384
	ds_write_b128 v186, v[54:57] offset:384
	ds_write_b128 v187, v[58:61] offset:384
	ds_write_b128 v188, v[62:65] offset:384
	s_cbranch_vccnz .Lp9_nonext
	s_ashr_i32 s48, s53, 2
	s_ashr_i32 s49, s48, 31
	s_lshl_b64 s[48:49], s[48:49], 17
	s_add_u32 s43, s29, s48
	s_addc_u32 s49, s30, s49
	s_and_b32 s48, s34, 0xc000
	s_add_u32 s48, s43, s48
	s_addc_u32 s49, s49, 0
	v_lshl_add_u64 v[10:11], s[48:49], 0, v[66:67]
	global_load_dwordx4 v[22:25], v[10:11], off nt
	global_load_dwordx4 v[2:5], v[10:11], off offset:1024 nt
	global_load_dwordx4 v[6:9], v[10:11], off offset:2048 nt
	s_nop 0
	global_load_dwordx4 v[10:13], v[10:11], off offset:3072 nt
	v_lshl_add_u64 v[14:15], s[48:49], 0, v[74:75]
	v_lshl_add_u64 v[18:19], s[48:49], 0, v[76:77]
	v_lshl_add_u64 v[26:27], s[48:49], 0, v[78:79]
	v_lshl_add_u64 v[30:31], s[48:49], 0, v[80:81]
	v_lshl_add_u64 v[34:35], s[48:49], 0, v[82:83]
	v_lshl_add_u64 v[38:39], s[48:49], 0, v[84:85]
	v_lshl_add_u64 v[42:43], s[48:49], 0, v[86:87]
	v_lshl_add_u64 v[46:47], s[48:49], 0, v[88:89]
	v_lshl_add_u64 v[50:51], s[48:49], 0, v[90:91]
	v_lshl_add_u64 v[54:55], s[48:49], 0, v[92:93]
	v_lshl_add_u64 v[58:59], s[48:49], 0, v[94:95]
	v_lshl_add_u64 v[62:63], s[48:49], 0, v[96:97]
	global_load_dwordx4 v[14:17], v[14:15], off nt
	s_nop 0
	global_load_dwordx4 v[18:21], v[18:19], off nt
	s_nop 0
	global_load_dwordx4 v[26:29], v[26:27], off nt
	s_nop 0
	global_load_dwordx4 v[30:33], v[30:31], off nt
	s_nop 0
	global_load_dwordx4 v[34:37], v[34:35], off nt
	s_nop 0
	global_load_dwordx4 v[38:41], v[38:39], off nt
	s_nop 0
	global_load_dwordx4 v[42:45], v[42:43], off nt
	s_nop 0
	global_load_dwordx4 v[46:49], v[46:47], off nt
	s_nop 0
	global_load_dwordx4 v[50:53], v[50:51], off nt
	s_nop 0
	global_load_dwordx4 v[54:57], v[54:55], off nt
	s_nop 0
	global_load_dwordx4 v[58:61], v[58:59], off nt
	s_nop 0
	global_load_dwordx4 v[62:65], v[62:63], off nt
	s_branch .LBB0_1466
